# all remaining GEMM epilogue tile stores marked non-temporal (residual stream, Z, P, K/V, G^T, VWT, pool)
# baseline (speedup 1.0000x reference)
.LBB0_309:
	s_ashr_i32 s46, s66, 1
	s_ashr_i32 s47, s46, 31
	s_ashr_i32 s45, s44, 31
	s_lshl_b64 s[46:47], s[46:47], 22
	s_lshl_b64 s[44:45], s[44:45], 18
	s_add_u32 s44, s25, s44
	s_addc_u32 s45, s54, s45
	s_add_u32 s44, s44, s46
	v_mbcnt_lo_u32_b32 v131, -1, 0
	v_mbcnt_hi_u32_b32 v131, -1, v131
	s_addc_u32 s45, s45, s47
	s_lshl_b32 s46, s66, 9
	v_and_or_b32 v138, v131, 15, s56
	v_ashrrev_i32_e32 v131, 1, v131
	s_and_b32 s46, s46, 0x200
	v_and_b32_e32 v131, -8, v131
	s_add_u32 s44, s44, s46
	v_ashrrev_i32_e32 v139, 31, v138
	s_addc_u32 s45, s45, 0
	v_add_u32_e32 v140, s57, v131
	v_lshlrev_b64 v[138:139], 10, v[138:139]
	v_lshl_add_u64 v[138:139], s[44:45], 0, v[138:139]
	v_ashrrev_i32_e32 v141, 31, v140
	v_lshl_add_u64 v[138:139], v[140:141], 1, v[138:139]
	v_cvt_pk_bf16_f32 v126, v126, v127
	v_cvt_pk_bf16_f32 v127, v128, v129
	v_cvt_pk_bf16_f32 v128, v118, v119
	v_lshl_add_u64 v[118:119], v[138:139], 0, s[4:5]
	v_cvt_pk_bf16_f32 v129, v120, v121
	global_store_dwordx4 v[138:139], v[126:129], off nt
	v_cvt_pk_bf16_f32 v110, v110, v111
	v_cvt_pk_bf16_f32 v111, v112, v113
	v_cvt_pk_bf16_f32 v112, v102, v103
	v_cvt_pk_bf16_f32 v113, v104, v105
	global_store_dwordx4 v[118:119], v[110:113], off nt
	v_lshl_add_u64 v[102:103], v[118:119], 0, s[4:5]
	v_cvt_pk_bf16_f32 v94, v94, v95
	v_cvt_pk_bf16_f32 v95, v96, v97
	v_cvt_pk_bf16_f32 v96, v86, v87
	v_cvt_pk_bf16_f32 v97, v88, v89
	global_store_dwordx4 v[102:103], v[94:97], off nt
	v_lshl_add_u64 v[86:87], v[102:103], 0, s[4:5]
	v_cvt_pk_bf16_f32 v78, v78, v79
	v_cvt_pk_bf16_f32 v79, v80, v81
	v_cvt_pk_bf16_f32 v80, v70, v71
	v_cvt_pk_bf16_f32 v81, v72, v73
	global_store_dwordx4 v[86:87], v[78:81], off nt
	v_lshl_add_u64 v[70:71], v[86:87], 0, s[4:5]
	s_mov_b64 s[44:45], 0x4100
	v_lshl_add_u64 v[78:79], v[70:71], 0, s[6:7]
	v_cvt_pk_bf16_f32 v70, v122, v123
	v_cvt_pk_bf16_f32 v71, v124, v125
	v_cvt_pk_bf16_f32 v72, v114, v115
	v_cvt_pk_bf16_f32 v73, v116, v117
	global_store_dwordx4 v[78:79], v[70:73], off nt
	v_lshl_add_u64 v[78:79], v[78:79], 0, s[4:5]
	s_and_b64 vcc, exec, s[38:39]
	v_cvt_pk_bf16_f32 v70, v106, v107
	v_cvt_pk_bf16_f32 v71, v108, v109
	v_cvt_pk_bf16_f32 v72, v98, v99
	v_cvt_pk_bf16_f32 v73, v100, v101
	global_store_dwordx4 v[78:79], v[70:73], off nt
	v_lshl_add_u64 v[78:79], v[78:79], 0, s[4:5]
	s_mov_b64 s[38:39], -1
	v_cvt_pk_bf16_f32 v70, v90, v91
	v_cvt_pk_bf16_f32 v71, v92, v93
	v_cvt_pk_bf16_f32 v72, v82, v83
	v_cvt_pk_bf16_f32 v73, v84, v85
	global_store_dwordx4 v[78:79], v[70:73], off nt
	v_lshl_add_u64 v[78:79], v[78:79], 0, s[4:5]
	s_nop 0
	v_cvt_pk_bf16_f32 v70, v74, v75
	v_cvt_pk_bf16_f32 v71, v76, v77
	v_cvt_pk_bf16_f32 v72, v66, v67
	v_lshl_add_u64 v[66:67], v[78:79], 0, s[4:5]
	v_cvt_pk_bf16_f32 v73, v68, v69
	global_store_dwordx4 v[78:79], v[70:73], off nt
	s_nop 0
	v_lshl_add_u64 v[66:67], v[66:67], 0, s[6:7]
	v_cvt_pk_bf16_f32 v54, v54, v55
	v_cvt_pk_bf16_f32 v55, v56, v57
	v_cvt_pk_bf16_f32 v56, v46, v47
	v_lshl_add_u64 v[46:47], v[138:139], 0, s[44:45]
	v_cvt_pk_bf16_f32 v57, v48, v49
	global_store_dwordx4 v[138:139], v[54:57], off offset:256 nt
	v_cvt_pk_bf16_f32 v38, v38, v39
	v_cvt_pk_bf16_f32 v39, v40, v41
	v_cvt_pk_bf16_f32 v40, v30, v31
	v_cvt_pk_bf16_f32 v41, v32, v33
	global_store_dwordx4 v[46:47], v[38:41], off nt
	v_lshl_add_u64 v[30:31], v[46:47], 0, s[4:5]
	v_cvt_pk_bf16_f32 v22, v22, v23
	v_cvt_pk_bf16_f32 v23, v24, v25
	v_cvt_pk_bf16_f32 v24, v14, v15
	v_cvt_pk_bf16_f32 v25, v16, v17
	global_store_dwordx4 v[30:31], v[22:25], off nt
	v_lshl_add_u64 v[14:15], v[30:31], 0, s[4:5]
	v_cvt_pk_bf16_f32 v6, v6, v7
	v_cvt_pk_bf16_f32 v7, v8, v9
	v_cvt_pk_bf16_f32 v8, v2, v3
	v_cvt_pk_bf16_f32 v9, v4, v5
	global_store_dwordx4 v[14:15], v[6:9], off nt
	v_lshl_add_u64 v[2:3], v[14:15], 0, s[4:5]
	s_nop 0
	v_lshl_add_u64 v[6:7], v[2:3], 0, s[6:7]
	v_cvt_pk_bf16_f32 v2, v50, v51
	v_cvt_pk_bf16_f32 v3, v52, v53
	v_cvt_pk_bf16_f32 v4, v42, v43
	v_cvt_pk_bf16_f32 v5, v44, v45
	global_store_dwordx4 v[6:7], v[2:5], off nt
	v_lshl_add_u64 v[6:7], v[6:7], 0, s[4:5]
	s_nop 0
	v_cvt_pk_bf16_f32 v2, v34, v35
	v_cvt_pk_bf16_f32 v3, v36, v37
	v_cvt_pk_bf16_f32 v4, v26, v27
	v_cvt_pk_bf16_f32 v5, v28, v29
	global_store_dwordx4 v[6:7], v[2:5], off nt
	v_lshl_add_u64 v[6:7], v[6:7], 0, s[4:5]
	s_nop 0
	v_cvt_pk_bf16_f32 v2, v18, v19
	v_cvt_pk_bf16_f32 v3, v20, v21
	v_cvt_pk_bf16_f32 v4, v10, v11
	v_cvt_pk_bf16_f32 v5, v12, v13
	global_store_dwordx4 v[6:7], v[2:5], off nt
	v_lshl_add_u64 v[6:7], v[6:7], 0, s[4:5]
	s_nop 0
	v_cvt_pk_bf16_f32 v2, v58, v59
	v_cvt_pk_bf16_f32 v3, v60, v61
	v_cvt_pk_bf16_f32 v4, v62, v63
	v_cvt_pk_bf16_f32 v5, v64, v65
	global_store_dwordx4 v[6:7], v[2:5], off nt
	s_nop 1
	v_lshl_add_u64 v[2:3], v[6:7], 0, s[4:5]
	s_nop 0
	v_lshl_add_u64 v[2:3], v[2:3], 0, s[6:7]
	s_cbranch_vccnz .LBB0_293
	v_mov_b32_e32 v62, v1
	v_mov_b32_e32 v63, v1
	s_andn2_b64 vcc, exec, s[30:31]
	s_nop 0
	v_mfma_f32_4x4x4_16b_f16 v[126:129], v[62:63], v[62:63], 0 cbsz:4
	v_mfma_f32_4x4x4_16b_f16 v[118:121], v[62:63], v[62:63], 0 cbsz:4 abid:1
	v_mfma_f32_4x4x4_16b_f16 v[110:113], v[62:63], v[62:63], 0 cbsz:4 abid:2
	v_mfma_f32_4x4x4_16b_f16 v[102:105], v[62:63], v[62:63], 0 cbsz:4 abid:3
	v_mfma_f32_4x4x4_16b_f16 v[94:97], v[62:63], v[62:63], 0 cbsz:4 abid:4
	v_mfma_f32_4x4x4_16b_f16 v[86:89], v[62:63], v[62:63], 0 cbsz:4 abid:5
	v_mfma_f32_4x4x4_16b_f16 v[78:81], v[62:63], v[62:63], 0 cbsz:4 abid:6
	v_mfma_f32_4x4x4_16b_f16 v[70:73], v[62:63], v[62:63], 0 cbsz:4 abid:7
	v_mfma_f32_4x4x4_16b_f16 v[54:57], v[62:63], v[62:63], 0 cbsz:4 abid:8
	v_mfma_f32_4x4x4_16b_f16 v[46:49], v[62:63], v[62:63], 0 cbsz:4 abid:9
	v_mfma_f32_4x4x4_16b_f16 v[38:41], v[62:63], v[62:63], 0 cbsz:4 abid:10
	v_mfma_f32_4x4x4_16b_f16 v[30:33], v[62:63], v[62:63], 0 cbsz:4 abid:11
	v_mfma_f32_4x4x4_16b_f16 v[22:25], v[62:63], v[62:63], 0 cbsz:4 abid:12
	v_mfma_f32_4x4x4_16b_f16 v[14:17], v[62:63], v[62:63], 0 cbsz:4 abid:13
	v_mfma_f32_4x4x4_16b_f16 v[6:9], v[62:63], v[62:63], 0 cbsz:4 abid:14
	v_mfma_f32_4x4x4_16b_f16 v[2:5], v[62:63], v[62:63], 0 cbsz:4 abid:15
	v_mfma_f32_4x4x4_16b_f16 v[122:125], v[62:63], v[62:63], 0 cbsz:4 blgp:1
	v_mfma_f32_4x4x4_16b_f16 v[114:117], v[62:63], v[62:63], 0 cbsz:4 abid:1 blgp:1
	v_mfma_f32_4x4x4_16b_f16 v[106:109], v[62:63], v[62:63], 0 cbsz:4 abid:2 blgp:1
	v_mfma_f32_4x4x4_16b_f16 v[98:101], v[62:63], v[62:63], 0 cbsz:4 abid:3 blgp:1
	v_mfma_f32_4x4x4_16b_f16 v[90:93], v[62:63], v[62:63], 0 cbsz:4 abid:4 blgp:1
	v_mfma_f32_4x4x4_16b_f16 v[82:85], v[62:63], v[62:63], 0 cbsz:4 abid:5 blgp:1
	v_mfma_f32_4x4x4_16b_f16 v[74:77], v[62:63], v[62:63], 0 cbsz:4 abid:6 blgp:1
	v_mfma_f32_4x4x4_16b_f16 v[66:69], v[62:63], v[62:63], 0 cbsz:4 abid:7 blgp:1
	v_mfma_f32_4x4x4_16b_f16 v[50:53], v[62:63], v[62:63], 0 cbsz:4 abid:8 blgp:1
	v_mfma_f32_4x4x4_16b_f16 v[42:45], v[62:63], v[62:63], 0 cbsz:4 abid:9 blgp:1
	v_mfma_f32_4x4x4_16b_f16 v[34:37], v[62:63], v[62:63], 0 cbsz:4 abid:10 blgp:1
	v_mfma_f32_4x4x4_16b_f16 v[26:29], v[62:63], v[62:63], 0 cbsz:4 abid:11 blgp:1
	v_mfma_f32_4x4x4_16b_f16 v[18:21], v[62:63], v[62:63], 0 cbsz:4 abid:12 blgp:1
	v_mfma_f32_4x4x4_16b_f16 v[10:13], v[62:63], v[62:63], 0 cbsz:4 abid:13 blgp:1
	v_mfma_f32_4x4x4_16b_f16 v[58:61], v[62:63], v[62:63], 0 cbsz:4 abid:14 blgp:1
	v_mfma_f32_4x4x4_16b_f16 v[62:65], v[62:63], v[62:63], 0 cbsz:4 abid:15 blgp:1
	s_cbranch_vccnz .LBB0_292
	s_barrier
	s_branch .LBB0_292

.LBB0_382:
	s_lshl_b32 s26, s11, 5
	s_lshl_b32 s21, s21, 2
	s_add_i32 s26, s26, s21
	s_or_b32 s26, s26, s60
	s_ashr_i32 s27, s26, 31
	s_lshl_b64 s[26:27], s[26:27], 8
	v_mbcnt_lo_u32_b32 v238, -1, 0
	v_mbcnt_hi_u32_b32 v238, -1, v238
	s_add_u32 s21, s26, s57
	v_ashrrev_i32_e32 v123, 4, v238
	v_and_b32_e32 v122, 15, v238
	s_addc_u32 s26, s27, s61
	v_lshlrev_b32_e32 v116, 3, v123
	v_or_b32_e32 v114, s21, v122
	v_mov_b32_e32 v115, s26
	v_ashrrev_i32_e32 v117, 31, v116
	v_lshl_add_u64 v[116:117], v[116:117], 1, s[50:51]
	v_lshlrev_b64 v[114:115], 7, v[114:115]
	v_lshl_add_u64 v[224:225], v[116:117], 0, v[114:115]
	global_load_dwordx4 v[194:197], v[224:225], off
	s_mov_b32 s21, 0x10000
	v_add_co_u32_e32 v222, vcc, s21, v224
	s_mov_b32 s21, 0x11000
	s_nop 0
	v_addc_co_u32_e32 v223, vcc, 0, v225, vcc
	v_add_co_u32_e32 v218, vcc, s21, v224
	s_movk_i32 s21, 0x4000
	s_nop 0
	v_addc_co_u32_e32 v219, vcc, 0, v225, vcc
	global_load_dwordx4 v[186:189], v[218:219], off offset:-4096
	global_load_dwordx4 v[182:185], v[224:225], off offset:2048
	global_load_dwordx4 v[178:181], v[222:223], off offset:2048
	v_add_co_u32_e32 v220, vcc, s94, v224
	v_lshlrev_b32_e32 v239, 6, v123
	s_nop 0
	v_addc_co_u32_e32 v221, vcc, 0, v225, vcc
	global_load_dwordx4 v[174:177], v[220:221], off
	global_load_dwordx4 v[162:165], v[218:219], off
	global_load_dwordx4 v[158:161], v[220:221], off offset:2048
	global_load_dwordx4 v[154:157], v[218:219], off offset:2048
	v_add_co_u32_e32 v216, vcc, s21, v224
	s_movk_i32 s21, 0x5000
	s_nop 0
	v_addc_co_u32_e32 v217, vcc, 0, v225, vcc
	v_add_co_u32_e32 v212, vcc, s21, v224
	s_mov_b32 s21, 0x14000
	s_nop 0
	v_addc_co_u32_e32 v213, vcc, 0, v225, vcc
	global_load_dwordx4 v[150:153], v[212:213], off offset:-4096
	v_add_co_u32_e32 v214, vcc, s21, v224
	s_mov_b32 s21, 0x15000
	s_nop 0
	v_addc_co_u32_e32 v215, vcc, 0, v225, vcc
	v_add_co_u32_e32 v210, vcc, s21, v224
	v_lshlrev_b32_e32 v240, 2, v122
	s_nop 0
	v_addc_co_u32_e32 v211, vcc, 0, v225, vcc
	global_load_dwordx4 v[146:149], v[210:211], off offset:-4096
	global_load_dwordx4 v[142:145], v[216:217], off offset:2048
	global_load_dwordx4 v[138:141], v[214:215], off offset:2048
	global_load_dwordx4 v[134:137], v[212:213], off
	global_load_dwordx4 v[130:133], v[210:211], off
	global_load_dwordx4 v[122:125], v[212:213], off offset:2048
	global_load_dwordx4 v[114:117], v[210:211], off offset:2048
	v_bitop3_b32 v241, v239, 64, v240 bitop3:0x36
	s_movk_i32 s21, 0x80
	v_cmp_gt_u32_e32 vcc, 16, v238
	s_waitcnt vmcnt(0)
	v_lshlrev_b32_e32 v190, 16, v194
	v_and_b32_e32 v191, 0xffff0000, v194
	v_lshlrev_b32_e32 v194, 16, v195
	v_and_b32_e32 v195, 0xffff0000, v195
	v_pk_fma_f32 v[166:167], v[166:167], 0.5, v[190:191] op_sel_hi:[1,0,1]
	v_pk_fma_f32 v[194:195], v[168:169], 0.5, v[194:195] op_sel_hi:[1,0,1]
	v_cvt_pk_bf16_f32 v168, v166, v167
	v_mov_b32_e32 v166, v1
	v_lshlrev_b32_e32 v198, 16, v196
	v_and_b32_e32 v199, 0xffff0000, v196
	v_dot2c_f32_bf16_e32 v166, v168, v168
	v_lshlrev_b32_e32 v196, 16, v197
	v_and_b32_e32 v197, 0xffff0000, v197
	v_pk_fma_f32 v[170:171], v[170:171], 0.5, v[198:199] op_sel_hi:[1,0,1]
	v_cvt_pk_bf16_f32 v169, v194, v195
	v_pk_fma_f32 v[172:173], v[172:173], 0.5, v[196:197] op_sel_hi:[1,0,1]
	v_dot2c_f32_bf16_e32 v166, v169, v169
	v_cvt_pk_bf16_f32 v170, v170, v171
	v_cvt_pk_bf16_f32 v171, v172, v173
	global_store_dwordx4 v[224:225], v[168:171], off nt
	v_dot2c_f32_bf16_e32 v166, v170, v170
	v_dot2c_f32_bf16_e32 v166, v171, v171
	v_lshlrev_b32_e32 v168, 16, v186
	v_and_b32_e32 v169, 0xffff0000, v186
	v_lshlrev_b32_e32 v170, 16, v187
	v_and_b32_e32 v171, 0xffff0000, v187
	v_lshlrev_b32_e32 v172, 16, v188
	v_and_b32_e32 v173, 0xffff0000, v188
	v_lshlrev_b32_e32 v186, 16, v189
	v_and_b32_e32 v187, 0xffff0000, v189
	v_pk_fma_f32 v[126:127], v[126:127], 0.5, v[168:169] op_sel_hi:[1,0,1]
	v_pk_fma_f32 v[168:169], v[120:121], 0.5, v[186:187] op_sel_hi:[1,0,1]
	v_pk_fma_f32 v[120:121], v[118:119], 0.5, v[172:173] op_sel_hi:[1,0,1]
	v_cvt_pk_bf16_f32 v118, v126, v127
	v_pk_fma_f32 v[128:129], v[128:129], 0.5, v[170:171] op_sel_hi:[1,0,1]
	v_dot2c_f32_bf16_e32 v166, v118, v118
	v_cvt_pk_bf16_f32 v119, v128, v129
	v_cvt_pk_bf16_f32 v120, v120, v121
	v_cvt_pk_bf16_f32 v121, v168, v169
	global_store_dwordx4 v[218:219], v[118:121], off offset:-4096 nt
	v_dot2c_f32_bf16_e32 v166, v119, v119
	v_dot2c_f32_bf16_e32 v166, v120, v120
	v_lshlrev_b32_e32 v118, 16, v182
	v_and_b32_e32 v119, 0xffff0000, v182
	v_lshlrev_b32_e32 v126, 16, v184
	v_and_b32_e32 v127, 0xffff0000, v184
	v_dot2c_f32_bf16_e32 v166, v121, v121
	v_lshlrev_b32_e32 v120, 16, v183
	v_and_b32_e32 v121, 0xffff0000, v183
	v_lshlrev_b32_e32 v128, 16, v185
	v_and_b32_e32 v129, 0xffff0000, v185
	v_pk_fma_f32 v[110:111], v[110:111], 0.5, v[118:119] op_sel_hi:[1,0,1]
	v_pk_fma_f32 v[106:107], v[106:107], 0.5, v[126:127] op_sel_hi:[1,0,1]
	v_pk_fma_f32 v[112:113], v[112:113], 0.5, v[120:121] op_sel_hi:[1,0,1]
	v_pk_fma_f32 v[118:119], v[108:109], 0.5, v[128:129] op_sel_hi:[1,0,1]
	v_cvt_pk_bf16_f32 v108, v110, v111
	v_cvt_pk_bf16_f32 v109, v112, v113
	v_cvt_pk_bf16_f32 v110, v106, v107
	v_mov_b32_e32 v106, v1
	v_dot2c_f32_bf16_e32 v106, v108, v108
	v_dot2c_f32_bf16_e32 v106, v109, v109
	v_dot2c_f32_bf16_e32 v106, v110, v110
	v_cvt_pk_bf16_f32 v111, v118, v119
	global_store_dwordx4 v[224:225], v[108:111], off offset:2048 nt
	v_dot2c_f32_bf16_e32 v106, v111, v111
	v_lshlrev_b32_e32 v112, 16, v180
	v_lshlrev_b32_e32 v108, 16, v178
	v_and_b32_e32 v109, 0xffff0000, v178
	v_and_b32_e32 v113, 0xffff0000, v180
	v_lshlrev_b32_e32 v118, 16, v181
	v_and_b32_e32 v119, 0xffff0000, v181
	v_lshlrev_b32_e32 v110, 16, v179
	v_and_b32_e32 v111, 0xffff0000, v179
	v_pk_fma_f32 v[102:103], v[102:103], 0.5, v[108:109] op_sel_hi:[1,0,1]
	v_pk_fma_f32 v[108:109], v[100:101], 0.5, v[118:119] op_sel_hi:[1,0,1]
	v_pk_fma_f32 v[100:101], v[98:99], 0.5, v[112:113] op_sel_hi:[1,0,1]
	v_cvt_pk_bf16_f32 v98, v102, v103
	v_pk_fma_f32 v[104:105], v[104:105], 0.5, v[110:111] op_sel_hi:[1,0,1]
	v_dot2c_f32_bf16_e32 v106, v98, v98
	v_cvt_pk_bf16_f32 v99, v104, v105
	v_cvt_pk_bf16_f32 v100, v100, v101
	v_cvt_pk_bf16_f32 v101, v108, v109
	global_store_dwordx4 v[222:223], v[98:101], off offset:2048 nt
	v_dot2c_f32_bf16_e32 v106, v99, v99
	v_dot2c_f32_bf16_e32 v106, v100, v100
	v_lshlrev_b32_e32 v98, 16, v174
	v_and_b32_e32 v99, 0xffff0000, v174
	v_lshlrev_b32_e32 v102, 16, v176
	v_and_b32_e32 v103, 0xffff0000, v176
	v_dot2c_f32_bf16_e32 v106, v101, v101
	v_lshlrev_b32_e32 v100, 16, v175
	v_and_b32_e32 v101, 0xffff0000, v175
	v_lshlrev_b32_e32 v104, 16, v177
	v_and_b32_e32 v105, 0xffff0000, v177
	v_pk_fma_f32 v[94:95], v[94:95], 0.5, v[98:99] op_sel_hi:[1,0,1]
	v_pk_fma_f32 v[90:91], v[90:91], 0.5, v[102:103] op_sel_hi:[1,0,1]
	v_pk_fma_f32 v[96:97], v[96:97], 0.5, v[100:101] op_sel_hi:[1,0,1]
	v_pk_fma_f32 v[98:99], v[92:93], 0.5, v[104:105] op_sel_hi:[1,0,1]
	v_cvt_pk_bf16_f32 v92, v94, v95
	v_cvt_pk_bf16_f32 v93, v96, v97
	v_cvt_pk_bf16_f32 v94, v90, v91
	v_mov_b32_e32 v90, v1
	v_dot2c_f32_bf16_e32 v90, v92, v92
	v_dot2c_f32_bf16_e32 v90, v93, v93
	v_dot2c_f32_bf16_e32 v90, v94, v94
	v_cvt_pk_bf16_f32 v95, v98, v99
	global_store_dwordx4 v[220:221], v[92:95], off nt
	v_dot2c_f32_bf16_e32 v90, v95, v95
	v_lshlrev_b32_e32 v96, 16, v164
	v_lshlrev_b32_e32 v92, 16, v162
	v_and_b32_e32 v93, 0xffff0000, v162
	v_and_b32_e32 v97, 0xffff0000, v164
	v_lshlrev_b32_e32 v98, 16, v165
	v_and_b32_e32 v99, 0xffff0000, v165
	v_lshlrev_b32_e32 v94, 16, v163
	v_and_b32_e32 v95, 0xffff0000, v163
	v_pk_fma_f32 v[86:87], v[86:87], 0.5, v[92:93] op_sel_hi:[1,0,1]
	v_pk_fma_f32 v[92:93], v[84:85], 0.5, v[98:99] op_sel_hi:[1,0,1]
	v_pk_fma_f32 v[84:85], v[82:83], 0.5, v[96:97] op_sel_hi:[1,0,1]
	v_cvt_pk_bf16_f32 v82, v86, v87
	v_pk_fma_f32 v[88:89], v[88:89], 0.5, v[94:95] op_sel_hi:[1,0,1]
	v_dot2c_f32_bf16_e32 v90, v82, v82
	v_cvt_pk_bf16_f32 v83, v88, v89
	v_cvt_pk_bf16_f32 v84, v84, v85
	v_cvt_pk_bf16_f32 v85, v92, v93
	global_store_dwordx4 v[218:219], v[82:85], off nt
	v_dot2c_f32_bf16_e32 v90, v83, v83
	v_dot2c_f32_bf16_e32 v90, v84, v84
	v_lshlrev_b32_e32 v82, 16, v158
	v_and_b32_e32 v83, 0xffff0000, v158
	v_lshlrev_b32_e32 v86, 16, v160
	v_and_b32_e32 v87, 0xffff0000, v160
	v_lshlrev_b32_e32 v88, 16, v161
	v_and_b32_e32 v89, 0xffff0000, v161
	v_dot2c_f32_bf16_e32 v90, v85, v85
	v_lshlrev_b32_e32 v84, 16, v159
	v_and_b32_e32 v85, 0xffff0000, v159
	v_pk_fma_f32 v[78:79], v[78:79], 0.5, v[82:83] op_sel_hi:[1,0,1]
	v_pk_fma_f32 v[82:83], v[72:73], 0.5, v[88:89] op_sel_hi:[1,0,1]
	v_pk_fma_f32 v[72:73], v[70:71], 0.5, v[86:87] op_sel_hi:[1,0,1]
	v_pk_fma_f32 v[80:81], v[80:81], 0.5, v[84:85] op_sel_hi:[1,0,1]
	v_cvt_pk_bf16_f32 v70, v78, v79
	v_lshlrev_b32_e32 v78, 16, v156
	v_cvt_pk_bf16_f32 v71, v80, v81
	v_cvt_pk_bf16_f32 v72, v72, v73
	v_cvt_pk_bf16_f32 v73, v82, v83
	v_mov_b32_e32 v82, v1
	v_dot2c_f32_bf16_e32 v82, v70, v70
	v_dot2c_f32_bf16_e32 v82, v71, v71
	v_dot2c_f32_bf16_e32 v82, v72, v72
	global_store_dwordx4 v[220:221], v[70:73], off offset:2048 nt
	v_dot2c_f32_bf16_e32 v82, v73, v73
	v_and_b32_e32 v79, 0xffff0000, v156
	v_lshlrev_b32_e32 v70, 16, v154
	v_and_b32_e32 v71, 0xffff0000, v154
	v_lshlrev_b32_e32 v72, 16, v155
	v_and_b32_e32 v73, 0xffff0000, v155
	v_lshlrev_b32_e32 v80, 16, v157
	v_and_b32_e32 v81, 0xffff0000, v157
	v_pk_fma_f32 v[64:65], v[64:65], 0.5, v[72:73] op_sel_hi:[1,0,1]
	v_pk_fma_f32 v[62:63], v[62:63], 0.5, v[70:71] op_sel_hi:[1,0,1]
	v_pk_fma_f32 v[70:71], v[56:57], 0.5, v[80:81] op_sel_hi:[1,0,1]
	v_pk_fma_f32 v[56:57], v[54:55], 0.5, v[78:79] op_sel_hi:[1,0,1]
	v_cvt_pk_bf16_f32 v54, v62, v63
	v_cvt_pk_bf16_f32 v55, v64, v65
	v_lshlrev_b32_e32 v62, 16, v152
	v_dot2c_f32_bf16_e32 v82, v54, v54
	v_cvt_pk_bf16_f32 v56, v56, v57
	v_cvt_pk_bf16_f32 v57, v70, v71
	global_store_dwordx4 v[218:219], v[54:57], off offset:2048 nt
	v_dot2c_f32_bf16_e32 v82, v55, v55
	v_and_b32_e32 v63, 0xffff0000, v152
	v_lshlrev_b32_e32 v54, 16, v150
	v_and_b32_e32 v55, 0xffff0000, v150
	v_dot2c_f32_bf16_e32 v82, v56, v56
	v_pk_fma_f32 v[54:55], v[74:75], 0.5, v[54:55] op_sel_hi:[1,0,1]
	v_pk_fma_f32 v[62:63], v[66:67], 0.5, v[62:63] op_sel_hi:[1,0,1]
	v_mov_b32_e32 v66, v1
	v_dot2c_f32_bf16_e32 v82, v57, v57
	v_lshlrev_b32_e32 v56, 16, v151
	v_and_b32_e32 v57, 0xffff0000, v151
	v_cvt_pk_bf16_f32 v54, v54, v55
	v_lshlrev_b32_e32 v64, 16, v153
	v_dot2c_f32_bf16_e32 v66, v54, v54
	v_and_b32_e32 v65, 0xffff0000, v153
	v_pk_fma_f32 v[56:57], v[76:77], 0.5, v[56:57] op_sel_hi:[1,0,1]
	v_pk_fma_f32 v[64:65], v[68:69], 0.5, v[64:65] op_sel_hi:[1,0,1]
	v_cvt_pk_bf16_f32 v55, v56, v57
	v_cvt_pk_bf16_f32 v56, v62, v63
	v_lshlrev_b32_e32 v62, 16, v148
	v_dot2c_f32_bf16_e32 v66, v55, v55
	v_dot2c_f32_bf16_e32 v66, v56, v56
	v_cvt_pk_bf16_f32 v57, v64, v65
	global_store_dwordx4 v[212:213], v[54:57], off offset:-4096 nt
	v_dot2c_f32_bf16_e32 v66, v57, v57
	v_and_b32_e32 v63, 0xffff0000, v148
	v_lshlrev_b32_e32 v54, 16, v146
	v_and_b32_e32 v55, 0xffff0000, v146
	v_lshlrev_b32_e32 v64, 16, v149
	v_and_b32_e32 v65, 0xffff0000, v149
	v_lshlrev_b32_e32 v56, 16, v147
	v_and_b32_e32 v57, 0xffff0000, v147
	v_pk_fma_f32 v[54:55], v[58:59], 0.5, v[54:55] op_sel_hi:[1,0,1]
	v_pk_fma_f32 v[58:59], v[52:53], 0.5, v[64:65] op_sel_hi:[1,0,1]
	v_pk_fma_f32 v[52:53], v[50:51], 0.5, v[62:63] op_sel_hi:[1,0,1]
	v_cvt_pk_bf16_f32 v50, v54, v55
	v_pk_fma_f32 v[56:57], v[60:61], 0.5, v[56:57] op_sel_hi:[1,0,1]
	v_dot2c_f32_bf16_e32 v66, v50, v50
	v_cvt_pk_bf16_f32 v51, v56, v57
	v_cvt_pk_bf16_f32 v52, v52, v53
	v_cvt_pk_bf16_f32 v53, v58, v59
	global_store_dwordx4 v[210:211], v[50:53], off offset:-4096 nt
	v_dot2c_f32_bf16_e32 v66, v51, v51
	v_dot2c_f32_bf16_e32 v66, v52, v52
	v_lshlrev_b32_e32 v50, 16, v142
	v_and_b32_e32 v51, 0xffff0000, v142
	v_lshlrev_b32_e32 v54, 16, v144
	v_and_b32_e32 v55, 0xffff0000, v144
	v_lshlrev_b32_e32 v56, 16, v145
	v_and_b32_e32 v57, 0xffff0000, v145
	v_dot2c_f32_bf16_e32 v66, v53, v53
	v_lshlrev_b32_e32 v52, 16, v143
	v_and_b32_e32 v53, 0xffff0000, v143
	v_pk_fma_f32 v[46:47], v[46:47], 0.5, v[50:51] op_sel_hi:[1,0,1]
	v_pk_fma_f32 v[50:51], v[44:45], 0.5, v[56:57] op_sel_hi:[1,0,1]
	v_pk_fma_f32 v[44:45], v[42:43], 0.5, v[54:55] op_sel_hi:[1,0,1]
	v_pk_fma_f32 v[48:49], v[48:49], 0.5, v[52:53] op_sel_hi:[1,0,1]
	v_cvt_pk_bf16_f32 v42, v46, v47
	v_lshlrev_b32_e32 v46, 16, v140
	v_cvt_pk_bf16_f32 v43, v48, v49
	v_cvt_pk_bf16_f32 v44, v44, v45
	v_cvt_pk_bf16_f32 v45, v50, v51
	v_mov_b32_e32 v50, v1
	v_dot2c_f32_bf16_e32 v50, v42, v42
	v_dot2c_f32_bf16_e32 v50, v43, v43
	v_dot2c_f32_bf16_e32 v50, v44, v44
	global_store_dwordx4 v[216:217], v[42:45], off offset:2048 nt
	v_dot2c_f32_bf16_e32 v50, v45, v45
	v_and_b32_e32 v47, 0xffff0000, v140
	v_lshlrev_b32_e32 v42, 16, v138
	v_and_b32_e32 v43, 0xffff0000, v138
	v_lshlrev_b32_e32 v48, 16, v141
	v_and_b32_e32 v49, 0xffff0000, v141
	v_lshlrev_b32_e32 v44, 16, v139
	v_and_b32_e32 v45, 0xffff0000, v139
	v_pk_fma_f32 v[38:39], v[38:39], 0.5, v[42:43] op_sel_hi:[1,0,1]
	v_pk_fma_f32 v[42:43], v[36:37], 0.5, v[48:49] op_sel_hi:[1,0,1]
	v_pk_fma_f32 v[36:37], v[34:35], 0.5, v[46:47] op_sel_hi:[1,0,1]
	v_cvt_pk_bf16_f32 v34, v38, v39
	v_pk_fma_f32 v[40:41], v[40:41], 0.5, v[44:45] op_sel_hi:[1,0,1]
	v_dot2c_f32_bf16_e32 v50, v34, v34
	v_cvt_pk_bf16_f32 v35, v40, v41
	v_cvt_pk_bf16_f32 v36, v36, v37
	v_cvt_pk_bf16_f32 v37, v42, v43
	global_store_dwordx4 v[214:215], v[34:37], off offset:2048 nt
	v_dot2c_f32_bf16_e32 v50, v35, v35
	v_dot2c_f32_bf16_e32 v50, v36, v36
	v_lshlrev_b32_e32 v34, 16, v134
	v_and_b32_e32 v35, 0xffff0000, v134
	v_lshlrev_b32_e32 v38, 16, v136
	v_and_b32_e32 v39, 0xffff0000, v136
	v_lshlrev_b32_e32 v40, 16, v137
	v_and_b32_e32 v41, 0xffff0000, v137
	v_dot2c_f32_bf16_e32 v50, v37, v37
	v_lshlrev_b32_e32 v36, 16, v135
	v_and_b32_e32 v37, 0xffff0000, v135
	v_pk_fma_f32 v[30:31], v[30:31], 0.5, v[34:35] op_sel_hi:[1,0,1]
	v_pk_fma_f32 v[34:35], v[28:29], 0.5, v[40:41] op_sel_hi:[1,0,1]
	v_pk_fma_f32 v[28:29], v[26:27], 0.5, v[38:39] op_sel_hi:[1,0,1]
	v_pk_fma_f32 v[32:33], v[32:33], 0.5, v[36:37] op_sel_hi:[1,0,1]
	v_cvt_pk_bf16_f32 v26, v30, v31
	v_lshlrev_b32_e32 v30, 16, v132
	v_cvt_pk_bf16_f32 v27, v32, v33
	v_cvt_pk_bf16_f32 v28, v28, v29
	v_cvt_pk_bf16_f32 v29, v34, v35
	v_mov_b32_e32 v34, v1
	v_dot2c_f32_bf16_e32 v34, v26, v26
	v_dot2c_f32_bf16_e32 v34, v27, v27
	v_dot2c_f32_bf16_e32 v34, v28, v28
	global_store_dwordx4 v[212:213], v[26:29], off nt
	v_dot2c_f32_bf16_e32 v34, v29, v29
	v_and_b32_e32 v31, 0xffff0000, v132
	v_lshlrev_b32_e32 v26, 16, v130
	v_and_b32_e32 v27, 0xffff0000, v130
	v_lshlrev_b32_e32 v32, 16, v133
	v_and_b32_e32 v33, 0xffff0000, v133
	v_lshlrev_b32_e32 v28, 16, v131
	v_and_b32_e32 v29, 0xffff0000, v131
	v_pk_fma_f32 v[22:23], v[22:23], 0.5, v[26:27] op_sel_hi:[1,0,1]
	v_pk_fma_f32 v[26:27], v[20:21], 0.5, v[32:33] op_sel_hi:[1,0,1]
	v_pk_fma_f32 v[20:21], v[18:19], 0.5, v[30:31] op_sel_hi:[1,0,1]
	v_cvt_pk_bf16_f32 v18, v22, v23
	v_pk_fma_f32 v[24:25], v[24:25], 0.5, v[28:29] op_sel_hi:[1,0,1]
	v_dot2c_f32_bf16_e32 v34, v18, v18
	v_cvt_pk_bf16_f32 v19, v24, v25
	v_cvt_pk_bf16_f32 v20, v20, v21
	v_cvt_pk_bf16_f32 v21, v26, v27
	global_store_dwordx4 v[210:211], v[18:21], off nt
	v_dot2c_f32_bf16_e32 v34, v19, v19
	v_dot2c_f32_bf16_e32 v34, v20, v20
	v_lshlrev_b32_e32 v18, 16, v122
	v_and_b32_e32 v19, 0xffff0000, v122
	v_lshlrev_b32_e32 v22, 16, v124
	v_and_b32_e32 v23, 0xffff0000, v124
	v_lshlrev_b32_e32 v24, 16, v125
	v_and_b32_e32 v25, 0xffff0000, v125
	v_dot2c_f32_bf16_e32 v34, v21, v21
	v_lshlrev_b32_e32 v20, 16, v123
	v_and_b32_e32 v21, 0xffff0000, v123
	v_pk_fma_f32 v[14:15], v[14:15], 0.5, v[18:19] op_sel_hi:[1,0,1]
	v_pk_fma_f32 v[18:19], v[12:13], 0.5, v[24:25] op_sel_hi:[1,0,1]
	v_pk_fma_f32 v[12:13], v[10:11], 0.5, v[22:23] op_sel_hi:[1,0,1]
	v_pk_fma_f32 v[16:17], v[16:17], 0.5, v[20:21] op_sel_hi:[1,0,1]
	v_cvt_pk_bf16_f32 v10, v14, v15
	v_lshlrev_b32_e32 v14, 16, v116
	v_cvt_pk_bf16_f32 v11, v16, v17
	v_cvt_pk_bf16_f32 v12, v12, v13
	v_cvt_pk_bf16_f32 v13, v18, v19
	v_mov_b32_e32 v18, v1
	v_dot2c_f32_bf16_e32 v18, v10, v10
	v_dot2c_f32_bf16_e32 v18, v11, v11
	v_dot2c_f32_bf16_e32 v18, v12, v12
	global_store_dwordx4 v[212:213], v[10:13], off offset:2048 nt
	v_dot2c_f32_bf16_e32 v18, v13, v13
	v_and_b32_e32 v15, 0xffff0000, v116
	v_lshlrev_b32_e32 v10, 16, v114
	v_and_b32_e32 v11, 0xffff0000, v114
	v_lshlrev_b32_e32 v16, 16, v117
	v_and_b32_e32 v17, 0xffff0000, v117
	v_lshlrev_b32_e32 v12, 16, v115
	v_and_b32_e32 v13, 0xffff0000, v115
	v_pk_fma_f32 v[6:7], v[6:7], 0.5, v[10:11] op_sel_hi:[1,0,1]
	v_pk_fma_f32 v[10:11], v[4:5], 0.5, v[16:17] op_sel_hi:[1,0,1]
	v_pk_fma_f32 v[4:5], v[2:3], 0.5, v[14:15] op_sel_hi:[1,0,1]
	v_cvt_pk_bf16_f32 v2, v6, v7
	v_pk_fma_f32 v[8:9], v[8:9], 0.5, v[12:13] op_sel_hi:[1,0,1]
	v_dot2c_f32_bf16_e32 v18, v2, v2
	v_cvt_pk_bf16_f32 v3, v8, v9
	v_cvt_pk_bf16_f32 v4, v4, v5
	v_cvt_pk_bf16_f32 v5, v10, v11
	global_store_dwordx4 v[210:211], v[2:5], off offset:2048 nt
	v_dot2c_f32_bf16_e32 v18, v3, v3
	v_dot2c_f32_bf16_e32 v18, v4, v4
	v_dot2c_f32_bf16_e32 v18, v5, v5
	ds_bpermute_b32 v2, v241, v166
	ds_bpermute_b32 v3, v241, v106
	ds_bpermute_b32 v4, v241, v90
	ds_bpermute_b32 v5, v241, v82
	ds_bpermute_b32 v6, v241, v66
	ds_bpermute_b32 v7, v241, v50
	ds_bpermute_b32 v8, v241, v34
	ds_bpermute_b32 v9, v241, v18
	s_waitcnt lgkmcnt(7)
	v_add_f32_e32 v2, v166, v2
	s_waitcnt lgkmcnt(6)
	v_add_f32_e32 v3, v106, v3
	s_waitcnt lgkmcnt(5)
	v_add_f32_e32 v4, v90, v4
	s_waitcnt lgkmcnt(4)
	v_add_f32_e32 v5, v82, v5
	s_waitcnt lgkmcnt(3)
	v_add_f32_e32 v6, v66, v6
	s_waitcnt lgkmcnt(2)
	v_add_f32_e32 v7, v50, v7
	s_waitcnt lgkmcnt(1)
	v_add_f32_e32 v8, v34, v8
	s_waitcnt lgkmcnt(0)
	v_add_f32_e32 v11, v18, v9
	v_bitop3_b32 v17, v239, s21, v240 bitop3:0x36
	ds_bpermute_b32 v9, v17, v2
	ds_bpermute_b32 v10, v17, v3
	ds_bpermute_b32 v12, v17, v4
	ds_bpermute_b32 v13, v17, v5
	ds_bpermute_b32 v14, v17, v6
	ds_bpermute_b32 v15, v17, v7
	ds_bpermute_b32 v16, v17, v8
	ds_bpermute_b32 v17, v17, v11
	s_and_saveexec_b64 s[26:27], vcc
	s_cbranch_execz .LBB0_368
	s_lshl_b32 s11, s11, 8
	s_add_i32 s11, s11, s57
	s_waitcnt lgkmcnt(5)
	v_add_f32_e32 v12, v4, v12
	v_add_f32_e32 v4, v2, v9
	v_or_b32_e32 v2, s11, v238
	s_mov_b32 s11, 0x49800000
	v_fma_f32 v4, v4, s11, 0.5
	v_trunc_f32_e32 v4, v4
	s_waitcnt lgkmcnt(4)
	v_add_f32_e32 v13, v5, v13
	v_mul_f32_e32 v5, 0x2f800000, v4
	v_floor_f32_e32 v5, v5
	v_fmac_f32_e32 v4, 0xcf800000, v5
	v_cvt_u32_f32_e32 v4, v4
	v_cvt_u32_f32_e32 v5, v5
	v_add_f32_e32 v10, v3, v10
	v_ashrrev_i32_e32 v3, 31, v2
	v_lshl_add_u64 v[2:3], v[2:3], 3, s[38:39]
	global_atomic_add_x2 v[2:3], v[4:5], off
	v_fma_f32 v4, v10, s11, 0.5
	v_trunc_f32_e32 v4, v4
	v_mul_f32_e32 v5, 0x2f800000, v4
	v_floor_f32_e32 v5, v5
	v_fmac_f32_e32 v4, 0xcf800000, v5
	v_cvt_u32_f32_e32 v4, v4
	v_cvt_u32_f32_e32 v5, v5
	s_waitcnt lgkmcnt(3)
	v_add_f32_e32 v6, v6, v14
	s_waitcnt lgkmcnt(2)
	v_add_f32_e32 v7, v7, v15
	s_waitcnt lgkmcnt(1)
	v_add_f32_e32 v8, v8, v16
	global_atomic_add_x2 v[2:3], v[4:5], off offset:128
	v_fma_f32 v4, v12, s11, 0.5
	v_trunc_f32_e32 v4, v4
	v_mul_f32_e32 v5, 0x2f800000, v4
	v_floor_f32_e32 v5, v5
	v_fmac_f32_e32 v4, 0xcf800000, v5
	v_cvt_u32_f32_e32 v4, v4
	v_cvt_u32_f32_e32 v5, v5
	s_waitcnt lgkmcnt(0)
	v_add_f32_e32 v11, v11, v17
	global_atomic_add_x2 v[2:3], v[4:5], off offset:256
	v_fma_f32 v4, v13, s11, 0.5
	v_trunc_f32_e32 v4, v4
	v_mul_f32_e32 v5, 0x2f800000, v4
	v_floor_f32_e32 v5, v5
	v_fmac_f32_e32 v4, 0xcf800000, v5
	v_cvt_u32_f32_e32 v4, v4
	v_cvt_u32_f32_e32 v5, v5
	global_atomic_add_x2 v[2:3], v[4:5], off offset:384
	v_fma_f32 v4, v6, s11, 0.5
	v_trunc_f32_e32 v4, v4
	v_mul_f32_e32 v5, 0x2f800000, v4
	v_floor_f32_e32 v5, v5
	v_fmac_f32_e32 v4, 0xcf800000, v5
	v_cvt_u32_f32_e32 v4, v4
	v_cvt_u32_f32_e32 v5, v5
	global_atomic_add_x2 v[2:3], v[4:5], off offset:1024
	v_fma_f32 v4, v7, s11, 0.5
	v_trunc_f32_e32 v4, v4
	v_mul_f32_e32 v5, 0x2f800000, v4
	v_floor_f32_e32 v5, v5
	v_fmac_f32_e32 v4, 0xcf800000, v5
	v_cvt_u32_f32_e32 v4, v4
	v_cvt_u32_f32_e32 v5, v5
	global_atomic_add_x2 v[2:3], v[4:5], off offset:1152
	v_fma_f32 v4, v8, s11, 0.5
	v_trunc_f32_e32 v4, v4
	v_mul_f32_e32 v5, 0x2f800000, v4
	v_floor_f32_e32 v5, v5
	v_fmac_f32_e32 v4, 0xcf800000, v5
	v_cvt_u32_f32_e32 v4, v4
	v_cvt_u32_f32_e32 v5, v5
	global_atomic_add_x2 v[2:3], v[4:5], off offset:1280
	v_fma_f32 v4, v11, s11, 0.5
	v_trunc_f32_e32 v4, v4
	v_mul_f32_e32 v5, 0x2f800000, v4
	v_floor_f32_e32 v5, v5
	v_fmac_f32_e32 v4, 0xcf800000, v5
	v_cvt_u32_f32_e32 v4, v4
	v_cvt_u32_f32_e32 v5, v5
	global_atomic_add_x2 v[2:3], v[4:5], off offset:1408
	s_branch .LBB0_368

.LBB0_459:
	s_lshl_b32 s1, s84, 10
	v_mbcnt_lo_u32_b32 v138, -1, 0
	v_mbcnt_hi_u32_b32 v138, -1, v138
	s_add_i32 s1, s1, 0
	v_and_or_b32 v0, v138, 15, s79
	v_lshl_add_u32 v130, v0, 2, s1
	v_add_u32_e32 v130, 0x23000, v130
	ds_read2_b32 v[136:137], v130 offset1:16
	ds_read2_b32 v[134:135], v130 offset0:32 offset1:48
	ds_read2_b32 v[132:133], v130 offset0:128 offset1:144
	ds_read2_b32 v[130:131], v130 offset0:160 offset1:176
	v_ashrrev_i32_e32 v149, 4, v138
	s_cmp_lg_u32 s0, 20
	s_mov_b64 s[26:27], -1
	s_cbranch_scc0 .LBB0_461
	s_mul_i32 s2, s88, 0x2a0000
	s_mul_hi_i32 s1, s88, 0x2a0000
	s_add_u32 s2, s75, s2
	s_addc_u32 s11, s76, s1
	s_lshl_b32 s0, s0, 8
	s_ashr_i32 s1, s0, 31
	s_lshl_b64 s[0:1], s[0:1], 1
	s_add_u32 s0, s2, s0
	s_addc_u32 s1, s11, s1
	v_lshl_add_u32 v138, v149, 3, s80
	v_mov_b64_e32 v[150:151], s[0:1]
	v_mad_i64_i32 v[150:151], s[0:1], v0, s33, v[150:151]
	v_ashrrev_i32_e32 v139, 31, v138
	v_lshl_add_u64 v[138:139], v[138:139], 1, v[150:151]
	s_waitcnt lgkmcnt(0)
	v_pk_mul_f32 v[152:153], v[68:69], v[136:137] op_sel_hi:[1,0]
	v_pk_mul_f32 v[150:151], v[66:67], v[136:137] op_sel_hi:[1,0]
	v_pk_mul_f32 v[156:157], v[70:71], v[136:137] op_sel_hi:[1,0]
	v_pk_mul_f32 v[154:155], v[72:73], v[136:137] op_sel_hi:[1,0]
	v_cvt_pk_bf16_f32 v150, v150, v151
	v_cvt_pk_bf16_f32 v151, v152, v153
	v_cvt_pk_bf16_f32 v152, v156, v157
	s_mov_b64 s[14:15], 0x2a000
	v_cvt_pk_bf16_f32 v153, v154, v155
	v_mov_b32_e32 v156, v137
	global_store_dwordx4 v[138:139], v[150:153], off nt
	v_lshl_add_u64 v[154:155], v[138:139], 0, s[14:15]
	v_pk_mul_f32 v[158:159], v[64:65], v[156:157] op_sel_hi:[1,0]
	v_pk_mul_f32 v[152:153], v[60:61], v[156:157] op_sel_hi:[1,0]
	v_pk_mul_f32 v[150:151], v[58:59], v[156:157] op_sel_hi:[1,0]
	v_pk_mul_f32 v[160:161], v[62:63], v[156:157] op_sel_hi:[1,0]
	v_cvt_pk_bf16_f32 v150, v150, v151
	v_cvt_pk_bf16_f32 v151, v152, v153
	s_mov_b64 s[20:21], 0xa8000
	v_cvt_pk_bf16_f32 v152, v160, v161
	v_cvt_pk_bf16_f32 v153, v158, v159
	global_store_dwordx4 v[154:155], v[150:153], off nt
	v_lshl_add_u64 v[154:155], v[154:155], 0, s[14:15]
	v_pk_mul_f32 v[158:159], v[56:57], v[134:135] op_sel_hi:[1,0]
	v_pk_mul_f32 v[152:153], v[52:53], v[134:135] op_sel_hi:[1,0]
	v_pk_mul_f32 v[150:151], v[50:51], v[134:135] op_sel_hi:[1,0]
	v_pk_mul_f32 v[160:161], v[54:55], v[134:135] op_sel_hi:[1,0]
	v_cvt_pk_bf16_f32 v150, v150, v151
	v_cvt_pk_bf16_f32 v151, v152, v153
	v_pk_mul_f32 v[128:129], v[128:129], v[136:137] op_sel_hi:[1,0]
	v_cvt_pk_bf16_f32 v152, v160, v161
	v_cvt_pk_bf16_f32 v153, v158, v159
	v_mov_b32_e32 v158, v135
	global_store_dwordx4 v[154:155], v[150:153], off nt
	v_lshl_add_u64 v[154:155], v[154:155], 0, s[14:15]
	v_pk_mul_f32 v[160:161], v[48:49], v[158:159] op_sel_hi:[1,0]
	v_pk_mul_f32 v[150:151], v[42:43], v[158:159] op_sel_hi:[1,0]
	v_pk_mul_f32 v[152:153], v[44:45], v[158:159] op_sel_hi:[1,0]
	v_cvt_pk_bf16_f32 v150, v150, v151
	v_pk_mul_f32 v[162:163], v[46:47], v[158:159] op_sel_hi:[1,0]
	v_cvt_pk_bf16_f32 v151, v152, v153
	v_pk_mul_f32 v[126:127], v[126:127], v[136:137] op_sel_hi:[1,0]
	v_cvt_pk_bf16_f32 v152, v162, v163
	v_cvt_pk_bf16_f32 v153, v160, v161
	global_store_dwordx4 v[154:155], v[150:153], off nt
	v_pk_mul_f32 v[160:161], v[32:33], v[132:133] op_sel_hi:[1,0]
	v_pk_mul_f32 v[162:163], v[30:31], v[132:133] op_sel_hi:[1,0]
	v_lshl_add_u64 v[150:151], v[154:155], 0, s[14:15]
	v_pk_mul_f32 v[152:153], v[28:29], v[132:133] op_sel_hi:[1,0]
	v_lshl_add_u64 v[154:155], v[150:151], 0, s[20:21]
	v_pk_mul_f32 v[150:151], v[26:27], v[132:133] op_sel_hi:[1,0]
	s_mov_b64 s[0:1], 0x2a100
	v_cvt_pk_bf16_f32 v150, v150, v151
	v_cvt_pk_bf16_f32 v151, v152, v153
	v_cvt_pk_bf16_f32 v152, v162, v163
	v_cvt_pk_bf16_f32 v153, v160, v161
	v_mov_b32_e32 v160, v133
	global_store_dwordx4 v[154:155], v[150:153], off nt
	v_lshl_add_u64 v[154:155], v[154:155], 0, s[14:15]
	v_pk_mul_f32 v[162:163], v[24:25], v[160:161] op_sel_hi:[1,0]
	v_pk_mul_f32 v[152:153], v[20:21], v[160:161] op_sel_hi:[1,0]
	v_pk_mul_f32 v[150:151], v[18:19], v[160:161] op_sel_hi:[1,0]
	v_pk_mul_f32 v[164:165], v[22:23], v[160:161] op_sel_hi:[1,0]
	v_cvt_pk_bf16_f32 v150, v150, v151
	v_cvt_pk_bf16_f32 v151, v152, v153
	v_pk_mul_f32 v[120:121], v[120:121], v[156:157] op_sel_hi:[1,0]
	v_cvt_pk_bf16_f32 v152, v164, v165
	v_cvt_pk_bf16_f32 v153, v162, v163
	global_store_dwordx4 v[154:155], v[150:153], off nt
	v_lshl_add_u64 v[154:155], v[154:155], 0, s[14:15]
	v_pk_mul_f32 v[162:163], v[16:17], v[130:131] op_sel_hi:[1,0]
	v_pk_mul_f32 v[152:153], v[12:13], v[130:131] op_sel_hi:[1,0]
	v_pk_mul_f32 v[150:151], v[10:11], v[130:131] op_sel_hi:[1,0]
	v_pk_mul_f32 v[164:165], v[14:15], v[130:131] op_sel_hi:[1,0]
	v_cvt_pk_bf16_f32 v150, v150, v151
	v_cvt_pk_bf16_f32 v151, v152, v153
	v_pk_mul_f32 v[118:119], v[118:119], v[156:157] op_sel_hi:[1,0]
	v_cvt_pk_bf16_f32 v152, v164, v165
	v_cvt_pk_bf16_f32 v153, v162, v163
	v_mov_b32_e32 v162, v131
	global_store_dwordx4 v[154:155], v[150:153], off nt
	v_lshl_add_u64 v[154:155], v[154:155], 0, s[14:15]
	v_pk_mul_f32 v[164:165], v[8:9], v[162:163] op_sel_hi:[1,0]
	v_pk_mul_f32 v[150:151], v[2:3], v[162:163] op_sel_hi:[1,0]
	v_pk_mul_f32 v[152:153], v[4:5], v[162:163] op_sel_hi:[1,0]
	v_cvt_pk_bf16_f32 v150, v150, v151
	v_pk_mul_f32 v[166:167], v[6:7], v[162:163] op_sel_hi:[1,0]
	v_cvt_pk_bf16_f32 v151, v152, v153
	v_pk_mul_f32 v[112:113], v[112:113], v[134:135] op_sel_hi:[1,0]
	v_cvt_pk_bf16_f32 v152, v166, v167
	v_cvt_pk_bf16_f32 v153, v164, v165
	global_store_dwordx4 v[154:155], v[150:153], off nt
	v_pk_mul_f32 v[110:111], v[110:111], v[134:135] op_sel_hi:[1,0]
	v_pk_mul_f32 v[96:97], v[96:97], v[158:159] op_sel_hi:[1,0]
	v_lshl_add_u64 v[150:151], v[154:155], 0, s[14:15]
	v_pk_mul_f32 v[94:95], v[94:95], v[158:159] op_sel_hi:[1,0]
	v_lshl_add_u64 v[150:151], v[150:151], 0, s[20:21]
	v_pk_mul_f32 v[98:99], v[98:99], v[132:133] op_sel_hi:[1,0]
	v_pk_mul_f32 v[150:151], v[124:125], v[136:137] op_sel_hi:[1,0]
	v_pk_mul_f32 v[124:125], v[122:123], v[136:137] op_sel_hi:[1,0]
	v_cvt_pk_bf16_f32 v122, v126, v127
	v_cvt_pk_bf16_f32 v123, v128, v129
	v_pk_mul_f32 v[82:83], v[82:83], v[160:161] op_sel_hi:[1,0]
	v_cvt_pk_bf16_f32 v124, v124, v125
	v_cvt_pk_bf16_f32 v125, v150, v151
	global_store_dwordx4 v[138:139], v[122:125], off offset:256 nt
	v_pk_mul_f32 v[84:85], v[84:85], v[160:161] op_sel_hi:[1,0]
	v_pk_mul_f32 v[88:89], v[88:89], v[160:161] op_sel_hi:[1,0]
	v_lshl_add_u64 v[122:123], v[138:139], 0, s[0:1]
	v_pk_mul_f32 v[124:125], v[116:117], v[156:157] op_sel_hi:[1,0]
	v_pk_mul_f32 v[116:117], v[114:115], v[156:157] op_sel_hi:[1,0]
	v_cvt_pk_bf16_f32 v114, v118, v119
	v_cvt_pk_bf16_f32 v115, v120, v121
	v_pk_mul_f32 v[86:87], v[86:87], v[160:161] op_sel_hi:[1,0]
	v_cvt_pk_bf16_f32 v116, v116, v117
	v_cvt_pk_bf16_f32 v117, v124, v125
	global_store_dwordx4 v[122:123], v[114:117], off nt
	v_pk_mul_f32 v[80:81], v[80:81], v[130:131] op_sel_hi:[1,0]
	v_pk_mul_f32 v[78:79], v[78:79], v[130:131] op_sel_hi:[1,0]
	v_lshl_add_u64 v[114:115], v[122:123], 0, s[14:15]
	v_pk_mul_f32 v[116:117], v[108:109], v[134:135] op_sel_hi:[1,0]
	v_pk_mul_f32 v[108:109], v[106:107], v[134:135] op_sel_hi:[1,0]
	v_cvt_pk_bf16_f32 v106, v110, v111
	v_cvt_pk_bf16_f32 v107, v112, v113
	v_pk_mul_f32 v[34:35], v[34:35], v[162:163] op_sel_hi:[1,0]
	v_cvt_pk_bf16_f32 v108, v108, v109
	v_cvt_pk_bf16_f32 v109, v116, v117
	global_store_dwordx4 v[114:115], v[106:109], off nt
	v_pk_mul_f32 v[36:37], v[36:37], v[162:163] op_sel_hi:[1,0]
	v_pk_mul_f32 v[40:41], v[40:41], v[162:163] op_sel_hi:[1,0]
	v_lshl_add_u64 v[106:107], v[114:115], 0, s[14:15]
	v_pk_mul_f32 v[108:109], v[92:93], v[158:159] op_sel_hi:[1,0]
	v_pk_mul_f32 v[92:93], v[90:91], v[158:159] op_sel_hi:[1,0]
	v_cvt_pk_bf16_f32 v90, v94, v95
	v_cvt_pk_bf16_f32 v91, v96, v97
	v_pk_mul_f32 v[96:97], v[100:101], v[132:133] op_sel_hi:[1,0]
	v_cvt_pk_bf16_f32 v92, v92, v93
	v_cvt_pk_bf16_f32 v93, v108, v109
	global_store_dwordx4 v[106:107], v[90:93], off nt
	v_pk_mul_f32 v[38:39], v[38:39], v[162:163] op_sel_hi:[1,0]
	s_nop 0
	v_lshl_add_u64 v[90:91], v[106:107], 0, s[14:15]
	v_pk_mul_f32 v[92:93], v[104:105], v[132:133] op_sel_hi:[1,0]
	v_lshl_add_u64 v[94:95], v[90:91], 0, s[20:21]
	v_pk_mul_f32 v[90:91], v[102:103], v[132:133] op_sel_hi:[1,0]
	s_nop 0
	v_cvt_pk_bf16_f32 v90, v90, v91
	v_cvt_pk_bf16_f32 v91, v92, v93
	v_cvt_pk_bf16_f32 v92, v98, v99
	v_cvt_pk_bf16_f32 v93, v96, v97
	global_store_dwordx4 v[94:95], v[90:93], off nt
	s_nop 1
	v_lshl_add_u64 v[90:91], v[94:95], 0, s[14:15]
	v_cvt_pk_bf16_f32 v82, v82, v83
	v_cvt_pk_bf16_f32 v83, v84, v85
	v_cvt_pk_bf16_f32 v84, v86, v87
	v_cvt_pk_bf16_f32 v85, v88, v89
	global_store_dwordx4 v[90:91], v[82:85], off nt
	s_nop 1
	v_lshl_add_u64 v[82:83], v[90:91], 0, s[14:15]
	v_pk_mul_f32 v[84:85], v[76:77], v[130:131] op_sel_hi:[1,0]
	v_pk_mul_f32 v[76:77], v[74:75], v[130:131] op_sel_hi:[1,0]
	v_cvt_pk_bf16_f32 v74, v78, v79
	v_cvt_pk_bf16_f32 v75, v80, v81
	s_nop 0
	v_cvt_pk_bf16_f32 v76, v76, v77
	v_cvt_pk_bf16_f32 v77, v84, v85
	global_store_dwordx4 v[82:83], v[74:77], off nt
	s_nop 1
	v_lshl_add_u64 v[74:75], v[82:83], 0, s[14:15]
	v_cvt_pk_bf16_f32 v34, v34, v35
	v_cvt_pk_bf16_f32 v35, v36, v37
	v_cvt_pk_bf16_f32 v36, v38, v39
	v_cvt_pk_bf16_f32 v37, v40, v41
	global_store_dwordx4 v[74:75], v[34:37], off nt
	s_nop 1
	v_lshl_add_u64 v[34:35], v[74:75], 0, s[14:15]
	s_nop 0
	v_lshl_add_u64 v[34:35], v[34:35], 0, s[20:21]
	s_cbranch_execnz .LBB0_465
	s_branch .LBB0_462

.LBB0_501:
	s_lshl_b32 s49, s80, 2
	s_ashr_i32 s48, s80, 4
	s_and_b32 s49, s49, 60
	s_add_i32 s48, s49, s48
	s_ashr_i32 s49, s48, 31
	s_lshl_b32 s50, s79, 8
	s_lshl_b64 s[48:49], s[48:49], 20
	s_ashr_i32 s51, s50, 31
	v_mbcnt_lo_u32_b32 v131, -1, 0
	v_mbcnt_hi_u32_b32 v131, -1, v131
	s_add_u32 s52, s15, s48
	v_and_or_b32 v142, v131, 15, s69
	v_ashrrev_i32_e32 v131, 1, v131
	s_addc_u32 s53, s18, s49
	s_lshl_b64 s[48:49], s[50:51], 1
	v_and_b32_e32 v131, -8, v131
	s_add_u32 s48, s52, s48
	v_ashrrev_i32_e32 v143, 31, v142
	s_addc_u32 s49, s53, s49
	v_add_u32_e32 v144, s70, v131
	v_lshlrev_b64 v[142:143], 12, v[142:143]
	v_lshl_add_u64 v[142:143], s[48:49], 0, v[142:143]
	v_ashrrev_i32_e32 v145, 31, v144
	v_lshl_add_u64 v[142:143], v[144:145], 1, v[142:143]
	v_cvt_pk_bf16_f32 v118, v118, v119
	v_cvt_pk_bf16_f32 v119, v120, v121
	v_cvt_pk_bf16_f32 v120, v114, v115
	v_lshl_add_u64 v[114:115], v[142:143], 0, s[6:7]
	v_cvt_pk_bf16_f32 v121, v116, v117
	global_store_dwordx4 v[142:143], v[118:121], off nt
	v_cvt_pk_bf16_f32 v102, v102, v103
	v_cvt_pk_bf16_f32 v103, v104, v105
	v_cvt_pk_bf16_f32 v104, v98, v99
	v_cvt_pk_bf16_f32 v105, v100, v101
	global_store_dwordx4 v[114:115], v[102:105], off nt
	v_lshl_add_u64 v[98:99], v[114:115], 0, s[6:7]
	v_cvt_pk_bf16_f32 v86, v86, v87
	v_cvt_pk_bf16_f32 v87, v88, v89
	v_cvt_pk_bf16_f32 v88, v82, v83
	v_cvt_pk_bf16_f32 v89, v84, v85
	global_store_dwordx4 v[98:99], v[86:89], off nt
	v_lshl_add_u64 v[82:83], v[98:99], 0, s[6:7]
	v_cvt_pk_bf16_f32 v70, v70, v71
	v_cvt_pk_bf16_f32 v71, v72, v73
	v_cvt_pk_bf16_f32 v72, v66, v67
	v_cvt_pk_bf16_f32 v73, v68, v69
	global_store_dwordx4 v[82:83], v[70:73], off nt
	v_lshl_add_u64 v[66:67], v[82:83], 0, s[6:7]
	s_mov_b64 s[48:49], 0x10100
	v_lshl_add_u64 v[70:71], v[66:67], 0, s[22:23]
	v_cvt_pk_bf16_f32 v66, v126, v127
	v_cvt_pk_bf16_f32 v67, v128, v129
	v_cvt_pk_bf16_f32 v68, v122, v123
	v_cvt_pk_bf16_f32 v69, v124, v125
	global_store_dwordx4 v[70:71], v[66:69], off nt
	v_lshl_add_u64 v[70:71], v[70:71], 0, s[6:7]
	s_and_b64 vcc, exec, s[40:41]
	v_cvt_pk_bf16_f32 v66, v110, v111
	v_cvt_pk_bf16_f32 v67, v112, v113
	v_cvt_pk_bf16_f32 v68, v106, v107
	v_cvt_pk_bf16_f32 v69, v108, v109
	global_store_dwordx4 v[70:71], v[66:69], off nt
	v_lshl_add_u64 v[70:71], v[70:71], 0, s[6:7]
	s_mov_b64 s[40:41], -1
	v_cvt_pk_bf16_f32 v66, v94, v95
	v_cvt_pk_bf16_f32 v67, v96, v97
	v_cvt_pk_bf16_f32 v68, v90, v91
	v_cvt_pk_bf16_f32 v69, v92, v93
	global_store_dwordx4 v[70:71], v[66:69], off nt
	v_lshl_add_u64 v[70:71], v[70:71], 0, s[6:7]
	s_nop 0
	v_cvt_pk_bf16_f32 v66, v78, v79
	v_cvt_pk_bf16_f32 v67, v80, v81
	v_cvt_pk_bf16_f32 v68, v74, v75
	v_cvt_pk_bf16_f32 v69, v76, v77
	global_store_dwordx4 v[70:71], v[66:69], off nt
	s_nop 1
	v_lshl_add_u64 v[66:67], v[70:71], 0, s[6:7]
	s_nop 0
	v_lshl_add_u64 v[66:67], v[66:67], 0, s[22:23]
	v_cvt_pk_bf16_f32 v46, v46, v47
	v_cvt_pk_bf16_f32 v47, v48, v49
	v_cvt_pk_bf16_f32 v48, v42, v43
	v_lshl_add_u64 v[42:43], v[142:143], 0, s[48:49]
	v_cvt_pk_bf16_f32 v49, v44, v45
	global_store_dwordx4 v[142:143], v[46:49], off offset:256 nt
	v_cvt_pk_bf16_f32 v30, v30, v31
	v_cvt_pk_bf16_f32 v31, v32, v33
	v_cvt_pk_bf16_f32 v32, v26, v27
	v_cvt_pk_bf16_f32 v33, v28, v29
	global_store_dwordx4 v[42:43], v[30:33], off nt
	v_lshl_add_u64 v[26:27], v[42:43], 0, s[6:7]
	v_cvt_pk_bf16_f32 v14, v14, v15
	v_cvt_pk_bf16_f32 v15, v16, v17
	v_cvt_pk_bf16_f32 v16, v10, v11
	v_cvt_pk_bf16_f32 v17, v12, v13
	global_store_dwordx4 v[26:27], v[14:17], off nt
	v_lshl_add_u64 v[10:11], v[26:27], 0, s[6:7]
	v_cvt_pk_bf16_f32 v6, v6, v7
	v_cvt_pk_bf16_f32 v7, v8, v9
	v_cvt_pk_bf16_f32 v8, v2, v3
	v_cvt_pk_bf16_f32 v9, v4, v5
	global_store_dwordx4 v[10:11], v[6:9], off nt
	v_lshl_add_u64 v[2:3], v[10:11], 0, s[6:7]
	s_nop 0
	v_lshl_add_u64 v[6:7], v[2:3], 0, s[22:23]
	v_cvt_pk_bf16_f32 v2, v54, v55
	v_cvt_pk_bf16_f32 v3, v56, v57
	v_cvt_pk_bf16_f32 v4, v50, v51
	v_cvt_pk_bf16_f32 v5, v52, v53
	global_store_dwordx4 v[6:7], v[2:5], off nt
	v_lshl_add_u64 v[6:7], v[6:7], 0, s[6:7]
	s_nop 0
	v_cvt_pk_bf16_f32 v2, v38, v39
	v_cvt_pk_bf16_f32 v3, v40, v41
	v_cvt_pk_bf16_f32 v4, v34, v35
	v_cvt_pk_bf16_f32 v5, v36, v37
	global_store_dwordx4 v[6:7], v[2:5], off nt
	v_lshl_add_u64 v[6:7], v[6:7], 0, s[6:7]
	s_nop 0
	v_cvt_pk_bf16_f32 v2, v22, v23
	v_cvt_pk_bf16_f32 v3, v24, v25
	v_cvt_pk_bf16_f32 v4, v18, v19
	v_cvt_pk_bf16_f32 v5, v20, v21
	global_store_dwordx4 v[6:7], v[2:5], off nt
	v_lshl_add_u64 v[6:7], v[6:7], 0, s[6:7]
	s_nop 0
	v_cvt_pk_bf16_f32 v2, v58, v59
	v_cvt_pk_bf16_f32 v3, v60, v61
	v_cvt_pk_bf16_f32 v4, v62, v63
	v_cvt_pk_bf16_f32 v5, v64, v65
	global_store_dwordx4 v[6:7], v[2:5], off nt
	s_nop 1
	v_lshl_add_u64 v[2:3], v[6:7], 0, s[6:7]
	s_nop 0
	v_lshl_add_u64 v[2:3], v[2:3], 0, s[22:23]
	s_cbranch_vccnz .LBB0_485
	v_mov_b32_e32 v62, v1
	v_mov_b32_e32 v63, v1
	s_andn2_b64 vcc, exec, s[34:35]
	s_nop 0
	v_mfma_f32_4x4x4_16b_f16 v[118:121], v[62:63], v[62:63], 0 cbsz:4
	v_mfma_f32_4x4x4_16b_f16 v[114:117], v[62:63], v[62:63], 0 cbsz:4 abid:1
	v_mfma_f32_4x4x4_16b_f16 v[102:105], v[62:63], v[62:63], 0 cbsz:4 abid:2
	v_mfma_f32_4x4x4_16b_f16 v[98:101], v[62:63], v[62:63], 0 cbsz:4 abid:3
	v_mfma_f32_4x4x4_16b_f16 v[86:89], v[62:63], v[62:63], 0 cbsz:4 abid:4
	v_mfma_f32_4x4x4_16b_f16 v[82:85], v[62:63], v[62:63], 0 cbsz:4 abid:5
	v_mfma_f32_4x4x4_16b_f16 v[70:73], v[62:63], v[62:63], 0 cbsz:4 abid:6
	v_mfma_f32_4x4x4_16b_f16 v[66:69], v[62:63], v[62:63], 0 cbsz:4 abid:7
	v_mfma_f32_4x4x4_16b_f16 v[46:49], v[62:63], v[62:63], 0 cbsz:4 abid:8
	v_mfma_f32_4x4x4_16b_f16 v[42:45], v[62:63], v[62:63], 0 cbsz:4 abid:9
	v_mfma_f32_4x4x4_16b_f16 v[30:33], v[62:63], v[62:63], 0 cbsz:4 abid:10
	v_mfma_f32_4x4x4_16b_f16 v[26:29], v[62:63], v[62:63], 0 cbsz:4 abid:11
	v_mfma_f32_4x4x4_16b_f16 v[14:17], v[62:63], v[62:63], 0 cbsz:4 abid:12
	v_mfma_f32_4x4x4_16b_f16 v[10:13], v[62:63], v[62:63], 0 cbsz:4 abid:13
	v_mfma_f32_4x4x4_16b_f16 v[6:9], v[62:63], v[62:63], 0 cbsz:4 abid:14
	v_mfma_f32_4x4x4_16b_f16 v[2:5], v[62:63], v[62:63], 0 cbsz:4 abid:15
	v_mfma_f32_4x4x4_16b_f16 v[126:129], v[62:63], v[62:63], 0 cbsz:4 blgp:1
	v_mfma_f32_4x4x4_16b_f16 v[122:125], v[62:63], v[62:63], 0 cbsz:4 abid:1 blgp:1
	v_mfma_f32_4x4x4_16b_f16 v[110:113], v[62:63], v[62:63], 0 cbsz:4 abid:2 blgp:1
	v_mfma_f32_4x4x4_16b_f16 v[106:109], v[62:63], v[62:63], 0 cbsz:4 abid:3 blgp:1
	v_mfma_f32_4x4x4_16b_f16 v[94:97], v[62:63], v[62:63], 0 cbsz:4 abid:4 blgp:1
	v_mfma_f32_4x4x4_16b_f16 v[90:93], v[62:63], v[62:63], 0 cbsz:4 abid:5 blgp:1
	v_mfma_f32_4x4x4_16b_f16 v[78:81], v[62:63], v[62:63], 0 cbsz:4 abid:6 blgp:1
	v_mfma_f32_4x4x4_16b_f16 v[74:77], v[62:63], v[62:63], 0 cbsz:4 abid:7 blgp:1
	v_mfma_f32_4x4x4_16b_f16 v[54:57], v[62:63], v[62:63], 0 cbsz:4 abid:8 blgp:1
	v_mfma_f32_4x4x4_16b_f16 v[50:53], v[62:63], v[62:63], 0 cbsz:4 abid:9 blgp:1
	v_mfma_f32_4x4x4_16b_f16 v[38:41], v[62:63], v[62:63], 0 cbsz:4 abid:10 blgp:1
	v_mfma_f32_4x4x4_16b_f16 v[34:37], v[62:63], v[62:63], 0 cbsz:4 abid:11 blgp:1
	v_mfma_f32_4x4x4_16b_f16 v[22:25], v[62:63], v[62:63], 0 cbsz:4 abid:12 blgp:1
	v_mfma_f32_4x4x4_16b_f16 v[18:21], v[62:63], v[62:63], 0 cbsz:4 abid:13 blgp:1
	v_mfma_f32_4x4x4_16b_f16 v[58:61], v[62:63], v[62:63], 0 cbsz:4 abid:14 blgp:1
	v_mfma_f32_4x4x4_16b_f16 v[62:65], v[62:63], v[62:63], 0 cbsz:4 abid:15 blgp:1
	s_cbranch_vccnz .LBB0_484
	s_barrier
	s_branch .LBB0_484

.LBB0_534:
	s_ashr_i32 s47, s46, 31
	s_lshl_b64 s[46:47], s[46:47], 22
	s_add_u32 s48, s58, s46
	s_addc_u32 s49, s59, s47
	s_lshl_b32 s46, s79, 5
	s_and_b32 s46, s46, 0xffffff00
	s_lshl_b32 s50, s79, 19
	s_ashr_i32 s47, s46, 31
	s_and_b32 s50, s50, 0x380000
	v_mbcnt_lo_u32_b32 v131, -1, 0
	v_mbcnt_hi_u32_b32 v131, -1, v131
	s_add_u32 s48, s48, s50
	v_and_or_b32 v142, v131, 15, s69
	v_ashrrev_i32_e32 v131, 1, v131
	s_addc_u32 s49, s49, 0
	s_lshl_b64 s[46:47], s[46:47], 1
	v_and_b32_e32 v131, -8, v131
	s_add_u32 s46, s48, s46
	v_ashrrev_i32_e32 v143, 31, v142
	s_addc_u32 s47, s49, s47
	v_add_u32_e32 v144, s70, v131
	v_lshlrev_b64 v[142:143], 11, v[142:143]
	v_lshl_add_u64 v[142:143], s[46:47], 0, v[142:143]
	v_ashrrev_i32_e32 v145, 31, v144
	v_lshl_add_u64 v[142:143], v[144:145], 1, v[142:143]
	v_cvt_pk_bf16_f32 v118, v118, v119
	v_cvt_pk_bf16_f32 v119, v120, v121
	v_cvt_pk_bf16_f32 v120, v114, v115
	v_lshl_add_u64 v[114:115], v[142:143], 0, s[96:97]
	v_cvt_pk_bf16_f32 v121, v116, v117
	global_store_dwordx4 v[142:143], v[118:121], off nt
	v_cvt_pk_bf16_f32 v102, v102, v103
	v_cvt_pk_bf16_f32 v103, v104, v105
	v_cvt_pk_bf16_f32 v104, v98, v99
	v_cvt_pk_bf16_f32 v105, v100, v101
	global_store_dwordx4 v[114:115], v[102:105], off nt
	v_lshl_add_u64 v[98:99], v[114:115], 0, s[96:97]
	v_cvt_pk_bf16_f32 v86, v86, v87
	v_cvt_pk_bf16_f32 v87, v88, v89
	v_cvt_pk_bf16_f32 v88, v82, v83
	v_cvt_pk_bf16_f32 v89, v84, v85
	global_store_dwordx4 v[98:99], v[86:89], off nt
	v_lshl_add_u64 v[82:83], v[98:99], 0, s[96:97]
	v_cvt_pk_bf16_f32 v70, v70, v71
	v_cvt_pk_bf16_f32 v71, v72, v73
	v_cvt_pk_bf16_f32 v72, v66, v67
	v_cvt_pk_bf16_f32 v73, v68, v69
	global_store_dwordx4 v[82:83], v[70:73], off nt
	v_lshl_add_u64 v[66:67], v[82:83], 0, s[96:97]
	s_mov_b64 s[46:47], 0x8100
	v_lshl_add_u64 v[70:71], v[66:67], 0, s[8:9]
	v_cvt_pk_bf16_f32 v66, v126, v127
	v_cvt_pk_bf16_f32 v67, v128, v129
	v_cvt_pk_bf16_f32 v68, v122, v123
	v_cvt_pk_bf16_f32 v69, v124, v125
	global_store_dwordx4 v[70:71], v[66:69], off nt
	v_lshl_add_u64 v[70:71], v[70:71], 0, s[96:97]
	s_and_b64 vcc, exec, s[40:41]
	v_cvt_pk_bf16_f32 v66, v110, v111
	v_cvt_pk_bf16_f32 v67, v112, v113
	v_cvt_pk_bf16_f32 v68, v106, v107
	v_cvt_pk_bf16_f32 v69, v108, v109
	global_store_dwordx4 v[70:71], v[66:69], off nt
	v_lshl_add_u64 v[70:71], v[70:71], 0, s[96:97]
	s_mov_b64 s[40:41], -1
	v_cvt_pk_bf16_f32 v66, v94, v95
	v_cvt_pk_bf16_f32 v67, v96, v97
	v_cvt_pk_bf16_f32 v68, v90, v91
	v_cvt_pk_bf16_f32 v69, v92, v93
	global_store_dwordx4 v[70:71], v[66:69], off nt
	v_lshl_add_u64 v[70:71], v[70:71], 0, s[96:97]
	s_nop 0
	v_cvt_pk_bf16_f32 v66, v78, v79
	v_cvt_pk_bf16_f32 v67, v80, v81
	v_cvt_pk_bf16_f32 v68, v74, v75
	v_cvt_pk_bf16_f32 v69, v76, v77
	global_store_dwordx4 v[70:71], v[66:69], off nt
	s_nop 1
	v_lshl_add_u64 v[66:67], v[70:71], 0, s[96:97]
	s_nop 0
	v_lshl_add_u64 v[66:67], v[66:67], 0, s[8:9]
	v_cvt_pk_bf16_f32 v46, v46, v47
	v_cvt_pk_bf16_f32 v47, v48, v49
	v_cvt_pk_bf16_f32 v48, v42, v43
	v_lshl_add_u64 v[42:43], v[142:143], 0, s[46:47]
	v_cvt_pk_bf16_f32 v49, v44, v45
	global_store_dwordx4 v[142:143], v[46:49], off offset:256 nt
	v_cvt_pk_bf16_f32 v30, v30, v31
	v_cvt_pk_bf16_f32 v31, v32, v33
	v_cvt_pk_bf16_f32 v32, v26, v27
	v_cvt_pk_bf16_f32 v33, v28, v29
	global_store_dwordx4 v[42:43], v[30:33], off nt
	v_lshl_add_u64 v[26:27], v[42:43], 0, s[96:97]
	v_cvt_pk_bf16_f32 v14, v14, v15
	v_cvt_pk_bf16_f32 v15, v16, v17
	v_cvt_pk_bf16_f32 v16, v10, v11
	v_cvt_pk_bf16_f32 v17, v12, v13
	global_store_dwordx4 v[26:27], v[14:17], off nt
	v_lshl_add_u64 v[10:11], v[26:27], 0, s[96:97]
	v_cvt_pk_bf16_f32 v6, v6, v7
	v_cvt_pk_bf16_f32 v7, v8, v9
	v_cvt_pk_bf16_f32 v8, v2, v3
	v_cvt_pk_bf16_f32 v9, v4, v5
	global_store_dwordx4 v[10:11], v[6:9], off nt
	v_lshl_add_u64 v[2:3], v[10:11], 0, s[96:97]
	s_nop 0
	v_lshl_add_u64 v[6:7], v[2:3], 0, s[8:9]
	v_cvt_pk_bf16_f32 v2, v54, v55
	v_cvt_pk_bf16_f32 v3, v56, v57
	v_cvt_pk_bf16_f32 v4, v50, v51
	v_cvt_pk_bf16_f32 v5, v52, v53
	global_store_dwordx4 v[6:7], v[2:5], off nt
	v_lshl_add_u64 v[6:7], v[6:7], 0, s[96:97]
	s_nop 0
	v_cvt_pk_bf16_f32 v2, v38, v39
	v_cvt_pk_bf16_f32 v3, v40, v41
	v_cvt_pk_bf16_f32 v4, v34, v35
	v_cvt_pk_bf16_f32 v5, v36, v37
	global_store_dwordx4 v[6:7], v[2:5], off nt
	v_lshl_add_u64 v[6:7], v[6:7], 0, s[96:97]
	s_nop 0
	v_cvt_pk_bf16_f32 v2, v22, v23
	v_cvt_pk_bf16_f32 v3, v24, v25
	v_cvt_pk_bf16_f32 v4, v18, v19
	v_cvt_pk_bf16_f32 v5, v20, v21
	global_store_dwordx4 v[6:7], v[2:5], off nt
	v_lshl_add_u64 v[6:7], v[6:7], 0, s[96:97]
	s_nop 0
	v_cvt_pk_bf16_f32 v2, v58, v59
	v_cvt_pk_bf16_f32 v3, v60, v61
	v_cvt_pk_bf16_f32 v4, v62, v63
	v_cvt_pk_bf16_f32 v5, v64, v65
	global_store_dwordx4 v[6:7], v[2:5], off nt
	s_nop 1
	v_lshl_add_u64 v[2:3], v[6:7], 0, s[96:97]
	s_nop 0
	v_lshl_add_u64 v[2:3], v[2:3], 0, s[8:9]
	s_cbranch_vccnz .LBB0_518
	v_mov_b32_e32 v62, v1
	v_mov_b32_e32 v63, v1
	s_andn2_b64 vcc, exec, s[30:31]
	s_nop 0
	v_mfma_f32_4x4x4_16b_f16 v[118:121], v[62:63], v[62:63], 0 cbsz:4
	v_mfma_f32_4x4x4_16b_f16 v[114:117], v[62:63], v[62:63], 0 cbsz:4 abid:1
	v_mfma_f32_4x4x4_16b_f16 v[102:105], v[62:63], v[62:63], 0 cbsz:4 abid:2
	v_mfma_f32_4x4x4_16b_f16 v[98:101], v[62:63], v[62:63], 0 cbsz:4 abid:3
	v_mfma_f32_4x4x4_16b_f16 v[86:89], v[62:63], v[62:63], 0 cbsz:4 abid:4
	v_mfma_f32_4x4x4_16b_f16 v[82:85], v[62:63], v[62:63], 0 cbsz:4 abid:5
	v_mfma_f32_4x4x4_16b_f16 v[70:73], v[62:63], v[62:63], 0 cbsz:4 abid:6
	v_mfma_f32_4x4x4_16b_f16 v[66:69], v[62:63], v[62:63], 0 cbsz:4 abid:7
	v_mfma_f32_4x4x4_16b_f16 v[46:49], v[62:63], v[62:63], 0 cbsz:4 abid:8
	v_mfma_f32_4x4x4_16b_f16 v[42:45], v[62:63], v[62:63], 0 cbsz:4 abid:9
	v_mfma_f32_4x4x4_16b_f16 v[30:33], v[62:63], v[62:63], 0 cbsz:4 abid:10
	v_mfma_f32_4x4x4_16b_f16 v[26:29], v[62:63], v[62:63], 0 cbsz:4 abid:11
	v_mfma_f32_4x4x4_16b_f16 v[14:17], v[62:63], v[62:63], 0 cbsz:4 abid:12
	v_mfma_f32_4x4x4_16b_f16 v[10:13], v[62:63], v[62:63], 0 cbsz:4 abid:13
	v_mfma_f32_4x4x4_16b_f16 v[6:9], v[62:63], v[62:63], 0 cbsz:4 abid:14
	v_mfma_f32_4x4x4_16b_f16 v[2:5], v[62:63], v[62:63], 0 cbsz:4 abid:15
	v_mfma_f32_4x4x4_16b_f16 v[126:129], v[62:63], v[62:63], 0 cbsz:4 blgp:1
	v_mfma_f32_4x4x4_16b_f16 v[122:125], v[62:63], v[62:63], 0 cbsz:4 abid:1 blgp:1
	v_mfma_f32_4x4x4_16b_f16 v[110:113], v[62:63], v[62:63], 0 cbsz:4 abid:2 blgp:1
	v_mfma_f32_4x4x4_16b_f16 v[106:109], v[62:63], v[62:63], 0 cbsz:4 abid:3 blgp:1
	v_mfma_f32_4x4x4_16b_f16 v[94:97], v[62:63], v[62:63], 0 cbsz:4 abid:4 blgp:1
	v_mfma_f32_4x4x4_16b_f16 v[90:93], v[62:63], v[62:63], 0 cbsz:4 abid:5 blgp:1
	v_mfma_f32_4x4x4_16b_f16 v[78:81], v[62:63], v[62:63], 0 cbsz:4 abid:6 blgp:1
	v_mfma_f32_4x4x4_16b_f16 v[74:77], v[62:63], v[62:63], 0 cbsz:4 abid:7 blgp:1
	v_mfma_f32_4x4x4_16b_f16 v[54:57], v[62:63], v[62:63], 0 cbsz:4 abid:8 blgp:1
	v_mfma_f32_4x4x4_16b_f16 v[50:53], v[62:63], v[62:63], 0 cbsz:4 abid:9 blgp:1
	v_mfma_f32_4x4x4_16b_f16 v[38:41], v[62:63], v[62:63], 0 cbsz:4 abid:10 blgp:1
	v_mfma_f32_4x4x4_16b_f16 v[34:37], v[62:63], v[62:63], 0 cbsz:4 abid:11 blgp:1
	v_mfma_f32_4x4x4_16b_f16 v[22:25], v[62:63], v[62:63], 0 cbsz:4 abid:12 blgp:1
	v_mfma_f32_4x4x4_16b_f16 v[18:21], v[62:63], v[62:63], 0 cbsz:4 abid:13 blgp:1
	v_mfma_f32_4x4x4_16b_f16 v[58:61], v[62:63], v[62:63], 0 cbsz:4 abid:14 blgp:1
	v_mfma_f32_4x4x4_16b_f16 v[62:65], v[62:63], v[62:63], 0 cbsz:4 abid:15 blgp:1
	s_cbranch_vccnz .LBB0_517
	s_barrier
	s_branch .LBB0_517

.LBB0_710:
	s_lshl_b32 s48, s71, 1
	s_and_b32 s48, s48, 0xffffff00
	v_mbcnt_lo_u32_b32 v139, -1, 0
	v_mbcnt_hi_u32_b32 v139, -1, v139
	s_ashr_i32 s49, s48, 31
	v_ashrrev_i32_e32 v130, 1, v139
	v_and_b32_e32 v140, -8, v130
	s_lshl_b64 s[48:49], s[48:49], 2
	s_add_u32 s48, s57, s48
	v_add_u32_e32 v130, s61, v140
	s_addc_u32 s49, s58, s49
	v_ashrrev_i32_e32 v131, 31, v130
	v_lshl_add_u64 v[142:143], v[130:131], 2, s[48:49]
	global_load_dwordx4 v[134:137], v[142:143], off
	global_load_dwordx4 v[130:133], v[142:143], off offset:16
	s_lshl_b32 s48, s71, 5
	s_ashr_i32 s49, s71, 5
	s_and_b32 s48, s48, 0xfe0
	s_and_b32 s49, s49, -4
	s_add_i32 s48, s48, s49
	s_or_b32 s48, s48, s65
	s_ashr_i32 s49, s48, 31
	v_and_or_b32 v150, v139, 15, s60
	s_lshl_b64 s[48:49], s[48:49], 15
	v_ashrrev_i32_e32 v151, 31, v150
	s_add_u32 s48, s25, s48
	v_lshlrev_b64 v[150:151], 7, v[150:151]
	s_addc_u32 s49, s56, s49
	v_lshl_add_u64 v[150:151], s[48:49], 0, v[150:151]
	v_ashrrev_i32_e32 v141, 31, v140
	v_lshl_add_u64 v[150:151], v[150:151], 0, s[94:95]
	v_lshl_add_u64 v[140:141], v[140:141], 1, v[150:151]
	v_lshl_add_u64 v[150:151], v[140:141], 0, s[12:13]
	s_mov_b64 s[50:51], 0x2000
	s_mov_b32 s48, 0x10000
	s_waitcnt vmcnt(0)
	v_pk_mul_f32 v[124:125], v[124:125], v[136:137]
	v_pk_mul_f32 v[122:123], v[122:123], v[134:135]
	v_pk_mul_f32 v[126:127], v[126:127], v[130:131]
	v_pk_mul_f32 v[114:115], v[114:115], v[130:131]
	v_pk_mul_f32 v[152:153], v[78:79], v[134:135]
	v_pk_mul_f32 v[154:155], v[76:77], v[132:133]
	v_cvt_pk_bf16_f32 v76, v122, v123
	v_cvt_pk_bf16_f32 v77, v124, v125
	v_cvt_pk_bf16_f32 v78, v126, v127
	v_pk_mul_f32 v[128:129], v[128:129], v[132:133]
	v_pk_mul_f32 v[120:121], v[120:121], v[136:137]
	v_pk_mul_f32 v[118:119], v[118:119], v[134:135]
	v_pk_mul_f32 v[98:99], v[98:99], v[130:131]
	v_cvt_pk_bf16_f32 v79, v128, v129
	global_store_dwordx4 v[140:141], v[76:79], off nt
	v_pk_mul_f32 v[116:117], v[116:117], v[132:133]
	v_pk_mul_f32 v[104:105], v[104:105], v[136:137]
	v_cvt_pk_bf16_f32 v76, v118, v119
	v_cvt_pk_bf16_f32 v77, v120, v121
	v_cvt_pk_bf16_f32 v78, v114, v115
	v_lshl_add_u64 v[114:115], v[150:151], 0, s[12:13]
	v_pk_mul_f32 v[102:103], v[102:103], v[134:135]
	v_cvt_pk_bf16_f32 v79, v116, v117
	global_store_dwordx4 v[150:151], v[76:79], off nt
	v_pk_mul_f32 v[100:101], v[100:101], v[132:133]
	v_pk_mul_f32 v[88:89], v[88:89], v[136:137]
	v_cvt_pk_bf16_f32 v76, v102, v103
	v_cvt_pk_bf16_f32 v77, v104, v105
	v_cvt_pk_bf16_f32 v78, v98, v99
	v_lshl_add_u64 v[98:99], v[114:115], 0, s[12:13]
	v_pk_mul_f32 v[86:87], v[86:87], v[134:135]
	v_cvt_pk_bf16_f32 v79, v100, v101
	global_store_dwordx4 v[114:115], v[76:79], off nt
	v_pk_mul_f32 v[84:85], v[84:85], v[132:133]
	v_pk_mul_f32 v[82:83], v[82:83], v[130:131]
	v_cvt_pk_bf16_f32 v76, v86, v87
	v_cvt_pk_bf16_f32 v77, v88, v89
	v_pk_mul_f32 v[112:113], v[112:113], v[136:137]
	v_cvt_pk_bf16_f32 v78, v82, v83
	v_cvt_pk_bf16_f32 v79, v84, v85
	global_store_dwordx4 v[98:99], v[76:79], off nt
	v_pk_mul_f32 v[110:111], v[110:111], v[134:135]
	v_pk_mul_f32 v[108:109], v[108:109], v[132:133]
	v_lshl_add_u64 v[76:77], v[98:99], 0, s[12:13]
	v_pk_mul_f32 v[106:107], v[106:107], v[130:131]
	v_lshl_add_u64 v[82:83], v[76:77], 0, s[50:51]
	v_cvt_pk_bf16_f32 v76, v110, v111
	v_cvt_pk_bf16_f32 v77, v112, v113
	v_cvt_pk_bf16_f32 v78, v106, v107
	v_cvt_pk_bf16_f32 v79, v108, v109
	global_store_dwordx4 v[82:83], v[76:79], off nt
	v_lshl_add_u64 v[82:83], v[82:83], 0, s[12:13]
	v_pk_mul_f32 v[96:97], v[96:97], v[136:137]
	v_pk_mul_f32 v[94:95], v[94:95], v[134:135]
	v_pk_mul_f32 v[92:93], v[92:93], v[132:133]
	v_pk_mul_f32 v[90:91], v[90:91], v[130:131]
	v_cvt_pk_bf16_f32 v76, v94, v95
	v_cvt_pk_bf16_f32 v77, v96, v97
	v_pk_mul_f32 v[80:81], v[80:81], v[136:137]
	v_cvt_pk_bf16_f32 v78, v90, v91
	v_cvt_pk_bf16_f32 v79, v92, v93
	global_store_dwordx4 v[82:83], v[76:79], off nt
	v_pk_mul_f32 v[72:73], v[72:73], v[136:137]
	v_pk_mul_f32 v[70:71], v[70:71], v[134:135]
	v_lshl_add_u64 v[78:79], v[82:83], 0, s[12:13]
	v_pk_mul_f32 v[76:77], v[74:75], v[130:131]
	v_cvt_pk_bf16_f32 v74, v152, v153
	v_cvt_pk_bf16_f32 v75, v80, v81
	s_nop 0
	v_cvt_pk_bf16_f32 v76, v76, v77
	v_cvt_pk_bf16_f32 v77, v154, v155
	global_store_dwordx4 v[78:79], v[74:77], off nt
	s_nop 1
	v_lshl_add_u64 v[74:75], v[78:79], 0, s[12:13]
	v_pk_mul_f32 v[76:77], v[68:69], v[132:133]
	v_pk_mul_f32 v[68:69], v[66:67], v[130:131]
	v_cvt_pk_bf16_f32 v66, v70, v71
	v_cvt_pk_bf16_f32 v67, v72, v73
	s_nop 0
	v_cvt_pk_bf16_f32 v68, v68, v69
	v_cvt_pk_bf16_f32 v69, v76, v77
	global_store_dwordx4 v[74:75], v[66:69], off nt
	s_nop 1
	v_lshl_add_u64 v[66:67], v[74:75], 0, s[12:13]
	v_add_co_u32_e32 v74, vcc, s48, v140
	v_lshl_add_u64 v[66:67], v[66:67], 0, s[50:51]
	global_load_dwordx4 v[70:73], v[142:143], off offset:512
	global_load_dwordx4 v[66:69], v[142:143], off offset:528
	s_mov_b64 s[48:49], 0x10800
	v_addc_co_u32_e32 v75, vcc, 0, v141, vcc
	v_lshl_add_u64 v[76:77], v[140:141], 0, s[48:49]
	s_and_b64 vcc, exec, s[44:45]
	s_mov_b64 s[44:45], -1
	s_waitcnt vmcnt(0)
	v_pk_mul_f32 v[60:61], v[60:61], v[72:73]
	v_pk_mul_f32 v[58:59], v[58:59], v[70:71]
	v_pk_mul_f32 v[62:63], v[62:63], v[66:67]
	v_pk_mul_f32 v[50:51], v[50:51], v[66:67]
	v_pk_mul_f32 v[78:79], v[4:5], v[68:69]
	v_pk_mul_f32 v[80:81], v[2:3], v[66:67]
	v_cvt_pk_bf16_f32 v2, v58, v59
	v_cvt_pk_bf16_f32 v3, v60, v61
	v_cvt_pk_bf16_f32 v4, v62, v63
	v_pk_mul_f32 v[64:65], v[64:65], v[68:69]
	v_pk_mul_f32 v[56:57], v[56:57], v[72:73]
	v_pk_mul_f32 v[54:55], v[54:55], v[70:71]
	v_pk_mul_f32 v[34:35], v[34:35], v[66:67]
	v_cvt_pk_bf16_f32 v5, v64, v65
	global_store_dwordx4 v[74:75], v[2:5], off nt
	v_pk_mul_f32 v[52:53], v[52:53], v[68:69]
	v_pk_mul_f32 v[40:41], v[40:41], v[72:73]
	v_cvt_pk_bf16_f32 v2, v54, v55
	v_cvt_pk_bf16_f32 v3, v56, v57
	v_cvt_pk_bf16_f32 v4, v50, v51
	v_lshl_add_u64 v[50:51], v[76:77], 0, s[12:13]
	v_pk_mul_f32 v[38:39], v[38:39], v[70:71]
	v_cvt_pk_bf16_f32 v5, v52, v53
	global_store_dwordx4 v[76:77], v[2:5], off nt
	v_pk_mul_f32 v[36:37], v[36:37], v[68:69]
	v_pk_mul_f32 v[16:17], v[16:17], v[72:73]
	v_cvt_pk_bf16_f32 v2, v38, v39
	v_cvt_pk_bf16_f32 v3, v40, v41
	v_cvt_pk_bf16_f32 v4, v34, v35
	v_lshl_add_u64 v[34:35], v[50:51], 0, s[12:13]
	v_pk_mul_f32 v[14:15], v[14:15], v[70:71]
	v_cvt_pk_bf16_f32 v5, v36, v37
	global_store_dwordx4 v[50:51], v[2:5], off nt
	v_pk_mul_f32 v[12:13], v[12:13], v[68:69]
	v_pk_mul_f32 v[10:11], v[10:11], v[66:67]
	v_cvt_pk_bf16_f32 v2, v14, v15
	v_cvt_pk_bf16_f32 v3, v16, v17
	v_pk_mul_f32 v[48:49], v[48:49], v[72:73]
	v_cvt_pk_bf16_f32 v4, v10, v11
	v_cvt_pk_bf16_f32 v5, v12, v13
	global_store_dwordx4 v[34:35], v[2:5], off nt
	v_pk_mul_f32 v[46:47], v[46:47], v[70:71]
	v_pk_mul_f32 v[44:45], v[44:45], v[68:69]
	v_lshl_add_u64 v[2:3], v[34:35], 0, s[12:13]
	v_pk_mul_f32 v[42:43], v[42:43], v[66:67]
	v_lshl_add_u64 v[10:11], v[2:3], 0, s[50:51]
	v_cvt_pk_bf16_f32 v2, v46, v47
	v_cvt_pk_bf16_f32 v3, v48, v49
	v_cvt_pk_bf16_f32 v4, v42, v43
	v_cvt_pk_bf16_f32 v5, v44, v45
	global_store_dwordx4 v[10:11], v[2:5], off nt
	v_lshl_add_u64 v[10:11], v[10:11], 0, s[12:13]
	v_pk_mul_f32 v[28:29], v[28:29], v[72:73]
	v_pk_mul_f32 v[26:27], v[26:27], v[70:71]
	v_pk_mul_f32 v[24:25], v[24:25], v[68:69]
	v_pk_mul_f32 v[22:23], v[22:23], v[66:67]
	v_cvt_pk_bf16_f32 v2, v26, v27
	v_cvt_pk_bf16_f32 v3, v28, v29
	v_pk_mul_f32 v[8:9], v[8:9], v[72:73]
	v_cvt_pk_bf16_f32 v4, v22, v23
	v_cvt_pk_bf16_f32 v5, v24, v25
	global_store_dwordx4 v[10:11], v[2:5], off nt
	v_lshl_add_u64 v[10:11], v[10:11], 0, s[12:13]
	v_pk_mul_f32 v[6:7], v[6:7], v[70:71]
	s_nop 0
	v_cvt_pk_bf16_f32 v2, v6, v7
	v_cvt_pk_bf16_f32 v3, v8, v9
	v_cvt_pk_bf16_f32 v4, v80, v81
	v_cvt_pk_bf16_f32 v5, v78, v79
	global_store_dwordx4 v[10:11], v[2:5], off nt
	v_lshl_add_u64 v[6:7], v[10:11], 0, s[12:13]
	v_pk_mul_f32 v[8:9], v[32:33], v[68:69]
	v_pk_mul_f32 v[2:3], v[18:19], v[70:71]
	v_pk_mul_f32 v[4:5], v[20:21], v[72:73]
	v_cvt_pk_bf16_f32 v2, v2, v3
	v_pk_mul_f32 v[10:11], v[30:31], v[66:67]
	v_cvt_pk_bf16_f32 v3, v4, v5
	s_nop 0
	v_cvt_pk_bf16_f32 v4, v10, v11
	v_cvt_pk_bf16_f32 v5, v8, v9
	global_store_dwordx4 v[6:7], v[2:5], off nt
	s_nop 1
	v_lshl_add_u64 v[2:3], v[6:7], 0, s[12:13]
	s_nop 0
	v_lshl_add_u64 v[2:3], v[2:3], 0, s[50:51]
	s_cbranch_vccnz .LBB0_694
	v_mov_b32_e32 v30, v1
	v_mov_b32_e32 v31, v1
	s_andn2_b64 vcc, exec, s[30:31]
	s_nop 0
	v_mfma_f32_4x4x4_16b_f16 v[122:125], v[30:31], v[30:31], 0 cbsz:4
	v_mfma_f32_4x4x4_16b_f16 v[126:129], v[30:31], v[30:31], 0 cbsz:4 abid:1
	v_mfma_f32_4x4x4_16b_f16 v[118:121], v[30:31], v[30:31], 0 cbsz:4 abid:2
	v_mfma_f32_4x4x4_16b_f16 v[114:117], v[30:31], v[30:31], 0 cbsz:4 abid:3
	v_mfma_f32_4x4x4_16b_f16 v[102:105], v[30:31], v[30:31], 0 cbsz:4 abid:4
	v_mfma_f32_4x4x4_16b_f16 v[98:101], v[30:31], v[30:31], 0 cbsz:4 abid:5
	v_mfma_f32_4x4x4_16b_f16 v[86:89], v[30:31], v[30:31], 0 cbsz:4 abid:6
	v_mfma_f32_4x4x4_16b_f16 v[82:85], v[30:31], v[30:31], 0 cbsz:4 abid:7
	v_mfma_f32_4x4x4_16b_f16 v[58:61], v[30:31], v[30:31], 0 cbsz:4 abid:8
	v_mfma_f32_4x4x4_16b_f16 v[62:65], v[30:31], v[30:31], 0 cbsz:4 abid:9
	v_mfma_f32_4x4x4_16b_f16 v[54:57], v[30:31], v[30:31], 0 cbsz:4 abid:10
	v_mfma_f32_4x4x4_16b_f16 v[50:53], v[30:31], v[30:31], 0 cbsz:4 abid:11
	v_mfma_f32_4x4x4_16b_f16 v[38:41], v[30:31], v[30:31], 0 cbsz:4 abid:12
	v_mfma_f32_4x4x4_16b_f16 v[34:37], v[30:31], v[30:31], 0 cbsz:4 abid:13
	v_mfma_f32_4x4x4_16b_f16 v[14:17], v[30:31], v[30:31], 0 cbsz:4 abid:14
	v_mfma_f32_4x4x4_16b_f16 v[10:13], v[30:31], v[30:31], 0 cbsz:4 abid:15
	v_mfma_f32_4x4x4_16b_f16 v[110:113], v[30:31], v[30:31], 0 cbsz:4 blgp:1
	v_mfma_f32_4x4x4_16b_f16 v[106:109], v[30:31], v[30:31], 0 cbsz:4 abid:1 blgp:1
	v_mfma_f32_4x4x4_16b_f16 v[94:97], v[30:31], v[30:31], 0 cbsz:4 abid:2 blgp:1
	v_mfma_f32_4x4x4_16b_f16 v[90:93], v[30:31], v[30:31], 0 cbsz:4 abid:3 blgp:1
	v_mfma_f32_4x4x4_16b_f16 v[78:81], v[30:31], v[30:31], 0 cbsz:4 abid:4 blgp:1
	v_mfma_f32_4x4x4_16b_f16 v[74:77], v[30:31], v[30:31], 0 cbsz:4 abid:5 blgp:1
	v_mfma_f32_4x4x4_16b_f16 v[70:73], v[30:31], v[30:31], 0 cbsz:4 abid:6 blgp:1
	v_mfma_f32_4x4x4_16b_f16 v[66:69], v[30:31], v[30:31], 0 cbsz:4 abid:7 blgp:1
	v_mfma_f32_4x4x4_16b_f16 v[46:49], v[30:31], v[30:31], 0 cbsz:4 abid:8 blgp:1
	v_mfma_f32_4x4x4_16b_f16 v[42:45], v[30:31], v[30:31], 0 cbsz:4 abid:9 blgp:1
	v_mfma_f32_4x4x4_16b_f16 v[26:29], v[30:31], v[30:31], 0 cbsz:4 abid:10 blgp:1
	v_mfma_f32_4x4x4_16b_f16 v[22:25], v[30:31], v[30:31], 0 cbsz:4 abid:11 blgp:1
	v_mfma_f32_4x4x4_16b_f16 v[6:9], v[30:31], v[30:31], 0 cbsz:4 abid:12 blgp:1
	v_mfma_f32_4x4x4_16b_f16 v[2:5], v[30:31], v[30:31], 0 cbsz:4 abid:13 blgp:1
	v_mfma_f32_4x4x4_16b_f16 v[18:21], v[30:31], v[30:31], 0 cbsz:4 abid:14 blgp:1
	v_mfma_f32_4x4x4_16b_f16 v[30:33], v[30:31], v[30:31], 0 cbsz:4 abid:15 blgp:1
	s_cbranch_vccnz .LBB0_693
	s_barrier
	s_branch .LBB0_693

.LBB0_893:
	s_lshl_b32 s26, s11, 5
	s_lshl_b32 s21, s21, 2
	s_add_i32 s26, s26, s21
	s_or_b32 s26, s26, s60
	s_ashr_i32 s27, s26, 31
	s_lshl_b64 s[26:27], s[26:27], 8
	v_mbcnt_lo_u32_b32 v238, -1, 0
	v_mbcnt_hi_u32_b32 v238, -1, v238
	s_add_u32 s21, s26, s57
	v_ashrrev_i32_e32 v123, 4, v238
	v_and_b32_e32 v122, 15, v238
	s_addc_u32 s26, s27, s61
	v_lshlrev_b32_e32 v116, 3, v123
	v_or_b32_e32 v114, s21, v122
	v_mov_b32_e32 v115, s26
	v_ashrrev_i32_e32 v117, 31, v116
	v_lshl_add_u64 v[116:117], v[116:117], 1, s[52:53]
	v_lshlrev_b64 v[114:115], 7, v[114:115]
	v_lshl_add_u64 v[224:225], v[116:117], 0, v[114:115]
	global_load_dwordx4 v[194:197], v[224:225], off
	s_mov_b32 s21, 0x10000
	v_add_co_u32_e32 v222, vcc, s21, v224
	s_mov_b32 s21, 0x11000
	s_nop 0
	v_addc_co_u32_e32 v223, vcc, 0, v225, vcc
	v_add_co_u32_e32 v218, vcc, s21, v224
	s_movk_i32 s21, 0x4000
	s_nop 0
	v_addc_co_u32_e32 v219, vcc, 0, v225, vcc
	global_load_dwordx4 v[186:189], v[218:219], off offset:-4096
	global_load_dwordx4 v[182:185], v[224:225], off offset:2048
	global_load_dwordx4 v[178:181], v[222:223], off offset:2048
	v_add_co_u32_e32 v220, vcc, s94, v224
	v_lshlrev_b32_e32 v239, 6, v123
	s_nop 0
	v_addc_co_u32_e32 v221, vcc, 0, v225, vcc
	global_load_dwordx4 v[174:177], v[220:221], off
	global_load_dwordx4 v[162:165], v[218:219], off
	global_load_dwordx4 v[158:161], v[220:221], off offset:2048
	global_load_dwordx4 v[154:157], v[218:219], off offset:2048
	v_add_co_u32_e32 v216, vcc, s21, v224
	s_movk_i32 s21, 0x5000
	s_nop 0
	v_addc_co_u32_e32 v217, vcc, 0, v225, vcc
	v_add_co_u32_e32 v212, vcc, s21, v224
	s_mov_b32 s21, 0x14000
	s_nop 0
	v_addc_co_u32_e32 v213, vcc, 0, v225, vcc
	global_load_dwordx4 v[150:153], v[212:213], off offset:-4096
	v_add_co_u32_e32 v214, vcc, s21, v224
	s_mov_b32 s21, 0x15000
	s_nop 0
	v_addc_co_u32_e32 v215, vcc, 0, v225, vcc
	v_add_co_u32_e32 v210, vcc, s21, v224
	v_lshlrev_b32_e32 v240, 2, v122
	s_nop 0
	v_addc_co_u32_e32 v211, vcc, 0, v225, vcc
	global_load_dwordx4 v[146:149], v[210:211], off offset:-4096
	global_load_dwordx4 v[142:145], v[216:217], off offset:2048
	global_load_dwordx4 v[138:141], v[214:215], off offset:2048
	global_load_dwordx4 v[134:137], v[212:213], off
	global_load_dwordx4 v[130:133], v[210:211], off
	global_load_dwordx4 v[122:125], v[212:213], off offset:2048
	global_load_dwordx4 v[114:117], v[210:211], off offset:2048
	v_bitop3_b32 v241, v239, 64, v240 bitop3:0x36
	s_movk_i32 s21, 0x80
	v_cmp_gt_u32_e32 vcc, 16, v238
	s_waitcnt vmcnt(0)
	v_lshlrev_b32_e32 v190, 16, v194
	v_and_b32_e32 v191, 0xffff0000, v194
	v_lshlrev_b32_e32 v194, 16, v195
	v_and_b32_e32 v195, 0xffff0000, v195
	v_pk_add_f32 v[166:167], v[166:167], v[190:191]
	v_pk_add_f32 v[194:195], v[168:169], v[194:195]
	v_cvt_pk_bf16_f32 v168, v166, v167
	v_mov_b32_e32 v166, v1
	v_lshlrev_b32_e32 v198, 16, v196
	v_and_b32_e32 v199, 0xffff0000, v196
	v_dot2c_f32_bf16_e32 v166, v168, v168
	v_lshlrev_b32_e32 v196, 16, v197
	v_and_b32_e32 v197, 0xffff0000, v197
	v_pk_add_f32 v[170:171], v[170:171], v[198:199]
	v_cvt_pk_bf16_f32 v169, v194, v195
	v_pk_add_f32 v[172:173], v[172:173], v[196:197]
	v_dot2c_f32_bf16_e32 v166, v169, v169
	v_cvt_pk_bf16_f32 v170, v170, v171
	v_cvt_pk_bf16_f32 v171, v172, v173
	global_store_dwordx4 v[224:225], v[168:171], off nt
	v_dot2c_f32_bf16_e32 v166, v170, v170
	v_dot2c_f32_bf16_e32 v166, v171, v171
	v_lshlrev_b32_e32 v168, 16, v186
	v_and_b32_e32 v169, 0xffff0000, v186
	v_lshlrev_b32_e32 v170, 16, v187
	v_and_b32_e32 v171, 0xffff0000, v187
	v_lshlrev_b32_e32 v172, 16, v188
	v_and_b32_e32 v173, 0xffff0000, v188
	v_lshlrev_b32_e32 v186, 16, v189
	v_and_b32_e32 v187, 0xffff0000, v189
	v_pk_add_f32 v[126:127], v[126:127], v[168:169]
	v_pk_add_f32 v[168:169], v[120:121], v[186:187]
	v_pk_add_f32 v[120:121], v[118:119], v[172:173]
	v_cvt_pk_bf16_f32 v118, v126, v127
	v_pk_add_f32 v[128:129], v[128:129], v[170:171]
	v_dot2c_f32_bf16_e32 v166, v118, v118
	v_cvt_pk_bf16_f32 v119, v128, v129
	v_cvt_pk_bf16_f32 v120, v120, v121
	v_cvt_pk_bf16_f32 v121, v168, v169
	global_store_dwordx4 v[218:219], v[118:121], off offset:-4096 nt
	v_dot2c_f32_bf16_e32 v166, v119, v119
	v_dot2c_f32_bf16_e32 v166, v120, v120
	v_lshlrev_b32_e32 v118, 16, v182
	v_and_b32_e32 v119, 0xffff0000, v182
	v_lshlrev_b32_e32 v126, 16, v184
	v_and_b32_e32 v127, 0xffff0000, v184
	v_dot2c_f32_bf16_e32 v166, v121, v121
	v_lshlrev_b32_e32 v120, 16, v183
	v_and_b32_e32 v121, 0xffff0000, v183
	v_lshlrev_b32_e32 v128, 16, v185
	v_and_b32_e32 v129, 0xffff0000, v185
	v_pk_add_f32 v[110:111], v[110:111], v[118:119]
	v_pk_add_f32 v[106:107], v[106:107], v[126:127]
	v_pk_add_f32 v[112:113], v[112:113], v[120:121]
	v_pk_add_f32 v[118:119], v[108:109], v[128:129]
	v_cvt_pk_bf16_f32 v108, v110, v111
	v_cvt_pk_bf16_f32 v109, v112, v113
	v_cvt_pk_bf16_f32 v110, v106, v107
	v_mov_b32_e32 v106, v1
	v_dot2c_f32_bf16_e32 v106, v108, v108
	v_dot2c_f32_bf16_e32 v106, v109, v109
	v_dot2c_f32_bf16_e32 v106, v110, v110
	v_cvt_pk_bf16_f32 v111, v118, v119
	global_store_dwordx4 v[224:225], v[108:111], off offset:2048 nt
	v_dot2c_f32_bf16_e32 v106, v111, v111
	v_lshlrev_b32_e32 v112, 16, v180
	v_lshlrev_b32_e32 v108, 16, v178
	v_and_b32_e32 v109, 0xffff0000, v178
	v_and_b32_e32 v113, 0xffff0000, v180
	v_lshlrev_b32_e32 v118, 16, v181
	v_and_b32_e32 v119, 0xffff0000, v181
	v_lshlrev_b32_e32 v110, 16, v179
	v_and_b32_e32 v111, 0xffff0000, v179
	v_pk_add_f32 v[102:103], v[102:103], v[108:109]
	v_pk_add_f32 v[108:109], v[100:101], v[118:119]
	v_pk_add_f32 v[100:101], v[98:99], v[112:113]
	v_cvt_pk_bf16_f32 v98, v102, v103
	v_pk_add_f32 v[104:105], v[104:105], v[110:111]
	v_dot2c_f32_bf16_e32 v106, v98, v98
	v_cvt_pk_bf16_f32 v99, v104, v105
	v_cvt_pk_bf16_f32 v100, v100, v101
	v_cvt_pk_bf16_f32 v101, v108, v109
	global_store_dwordx4 v[222:223], v[98:101], off offset:2048 nt
	v_dot2c_f32_bf16_e32 v106, v99, v99
	v_dot2c_f32_bf16_e32 v106, v100, v100
	v_lshlrev_b32_e32 v98, 16, v174
	v_and_b32_e32 v99, 0xffff0000, v174
	v_lshlrev_b32_e32 v102, 16, v176
	v_and_b32_e32 v103, 0xffff0000, v176
	v_dot2c_f32_bf16_e32 v106, v101, v101
	v_lshlrev_b32_e32 v100, 16, v175
	v_and_b32_e32 v101, 0xffff0000, v175
	v_lshlrev_b32_e32 v104, 16, v177
	v_and_b32_e32 v105, 0xffff0000, v177
	v_pk_add_f32 v[94:95], v[94:95], v[98:99]
	v_pk_add_f32 v[90:91], v[90:91], v[102:103]
	v_pk_add_f32 v[96:97], v[96:97], v[100:101]
	v_pk_add_f32 v[98:99], v[92:93], v[104:105]
	v_cvt_pk_bf16_f32 v92, v94, v95
	v_cvt_pk_bf16_f32 v93, v96, v97
	v_cvt_pk_bf16_f32 v94, v90, v91
	v_mov_b32_e32 v90, v1
	v_dot2c_f32_bf16_e32 v90, v92, v92
	v_dot2c_f32_bf16_e32 v90, v93, v93
	v_dot2c_f32_bf16_e32 v90, v94, v94
	v_cvt_pk_bf16_f32 v95, v98, v99
	global_store_dwordx4 v[220:221], v[92:95], off nt
	v_dot2c_f32_bf16_e32 v90, v95, v95
	v_lshlrev_b32_e32 v96, 16, v164
	v_lshlrev_b32_e32 v92, 16, v162
	v_and_b32_e32 v93, 0xffff0000, v162
	v_and_b32_e32 v97, 0xffff0000, v164
	v_lshlrev_b32_e32 v98, 16, v165
	v_and_b32_e32 v99, 0xffff0000, v165
	v_lshlrev_b32_e32 v94, 16, v163
	v_and_b32_e32 v95, 0xffff0000, v163
	v_pk_add_f32 v[86:87], v[86:87], v[92:93]
	v_pk_add_f32 v[92:93], v[84:85], v[98:99]
	v_pk_add_f32 v[84:85], v[82:83], v[96:97]
	v_cvt_pk_bf16_f32 v82, v86, v87
	v_pk_add_f32 v[88:89], v[88:89], v[94:95]
	v_dot2c_f32_bf16_e32 v90, v82, v82
	v_cvt_pk_bf16_f32 v83, v88, v89
	v_cvt_pk_bf16_f32 v84, v84, v85
	v_cvt_pk_bf16_f32 v85, v92, v93
	global_store_dwordx4 v[218:219], v[82:85], off nt
	v_dot2c_f32_bf16_e32 v90, v83, v83
	v_dot2c_f32_bf16_e32 v90, v84, v84
	v_lshlrev_b32_e32 v82, 16, v158
	v_and_b32_e32 v83, 0xffff0000, v158
	v_lshlrev_b32_e32 v86, 16, v160
	v_and_b32_e32 v87, 0xffff0000, v160
	v_lshlrev_b32_e32 v88, 16, v161
	v_and_b32_e32 v89, 0xffff0000, v161
	v_dot2c_f32_bf16_e32 v90, v85, v85
	v_lshlrev_b32_e32 v84, 16, v159
	v_and_b32_e32 v85, 0xffff0000, v159
	v_pk_add_f32 v[78:79], v[78:79], v[82:83]
	v_pk_add_f32 v[82:83], v[72:73], v[88:89]
	v_pk_add_f32 v[72:73], v[70:71], v[86:87]
	v_pk_add_f32 v[80:81], v[80:81], v[84:85]
	v_cvt_pk_bf16_f32 v70, v78, v79
	v_lshlrev_b32_e32 v78, 16, v156
	v_cvt_pk_bf16_f32 v71, v80, v81
	v_cvt_pk_bf16_f32 v72, v72, v73
	v_cvt_pk_bf16_f32 v73, v82, v83
	v_mov_b32_e32 v82, v1
	v_dot2c_f32_bf16_e32 v82, v70, v70
	v_dot2c_f32_bf16_e32 v82, v71, v71
	v_dot2c_f32_bf16_e32 v82, v72, v72
	global_store_dwordx4 v[220:221], v[70:73], off offset:2048 nt
	v_dot2c_f32_bf16_e32 v82, v73, v73
	v_and_b32_e32 v79, 0xffff0000, v156
	v_lshlrev_b32_e32 v70, 16, v154
	v_and_b32_e32 v71, 0xffff0000, v154
	v_lshlrev_b32_e32 v72, 16, v155
	v_and_b32_e32 v73, 0xffff0000, v155
	v_lshlrev_b32_e32 v80, 16, v157
	v_and_b32_e32 v81, 0xffff0000, v157
	v_pk_add_f32 v[64:65], v[64:65], v[72:73]
	v_pk_add_f32 v[62:63], v[62:63], v[70:71]
	v_pk_add_f32 v[70:71], v[56:57], v[80:81]
	v_pk_add_f32 v[56:57], v[54:55], v[78:79]
	v_cvt_pk_bf16_f32 v54, v62, v63
	v_cvt_pk_bf16_f32 v55, v64, v65
	v_lshlrev_b32_e32 v62, 16, v152
	v_dot2c_f32_bf16_e32 v82, v54, v54
	v_cvt_pk_bf16_f32 v56, v56, v57
	v_cvt_pk_bf16_f32 v57, v70, v71
	global_store_dwordx4 v[218:219], v[54:57], off offset:2048 nt
	v_dot2c_f32_bf16_e32 v82, v55, v55
	v_and_b32_e32 v63, 0xffff0000, v152
	v_lshlrev_b32_e32 v54, 16, v150
	v_and_b32_e32 v55, 0xffff0000, v150
	v_dot2c_f32_bf16_e32 v82, v56, v56
	v_pk_add_f32 v[54:55], v[74:75], v[54:55]
	v_pk_add_f32 v[62:63], v[66:67], v[62:63]
	v_mov_b32_e32 v66, v1
	v_dot2c_f32_bf16_e32 v82, v57, v57
	v_lshlrev_b32_e32 v56, 16, v151
	v_and_b32_e32 v57, 0xffff0000, v151
	v_cvt_pk_bf16_f32 v54, v54, v55
	v_lshlrev_b32_e32 v64, 16, v153
	v_dot2c_f32_bf16_e32 v66, v54, v54
	v_and_b32_e32 v65, 0xffff0000, v153
	v_pk_add_f32 v[56:57], v[76:77], v[56:57]
	v_pk_add_f32 v[64:65], v[68:69], v[64:65]
	v_cvt_pk_bf16_f32 v55, v56, v57
	v_cvt_pk_bf16_f32 v56, v62, v63
	v_lshlrev_b32_e32 v62, 16, v148
	v_dot2c_f32_bf16_e32 v66, v55, v55
	v_dot2c_f32_bf16_e32 v66, v56, v56
	v_cvt_pk_bf16_f32 v57, v64, v65
	global_store_dwordx4 v[212:213], v[54:57], off offset:-4096 nt
	v_dot2c_f32_bf16_e32 v66, v57, v57
	v_and_b32_e32 v63, 0xffff0000, v148
	v_lshlrev_b32_e32 v54, 16, v146
	v_and_b32_e32 v55, 0xffff0000, v146
	v_lshlrev_b32_e32 v64, 16, v149
	v_and_b32_e32 v65, 0xffff0000, v149
	v_lshlrev_b32_e32 v56, 16, v147
	v_and_b32_e32 v57, 0xffff0000, v147
	v_pk_add_f32 v[54:55], v[58:59], v[54:55]
	v_pk_add_f32 v[58:59], v[52:53], v[64:65]
	v_pk_add_f32 v[52:53], v[50:51], v[62:63]
	v_cvt_pk_bf16_f32 v50, v54, v55
	v_pk_add_f32 v[56:57], v[60:61], v[56:57]
	v_dot2c_f32_bf16_e32 v66, v50, v50
	v_cvt_pk_bf16_f32 v51, v56, v57
	v_cvt_pk_bf16_f32 v52, v52, v53
	v_cvt_pk_bf16_f32 v53, v58, v59
	global_store_dwordx4 v[210:211], v[50:53], off offset:-4096 nt
	v_dot2c_f32_bf16_e32 v66, v51, v51
	v_dot2c_f32_bf16_e32 v66, v52, v52
	v_lshlrev_b32_e32 v50, 16, v142
	v_and_b32_e32 v51, 0xffff0000, v142
	v_lshlrev_b32_e32 v54, 16, v144
	v_and_b32_e32 v55, 0xffff0000, v144
	v_lshlrev_b32_e32 v56, 16, v145
	v_and_b32_e32 v57, 0xffff0000, v145
	v_dot2c_f32_bf16_e32 v66, v53, v53
	v_lshlrev_b32_e32 v52, 16, v143
	v_and_b32_e32 v53, 0xffff0000, v143
	v_pk_add_f32 v[46:47], v[46:47], v[50:51]
	v_pk_add_f32 v[50:51], v[44:45], v[56:57]
	v_pk_add_f32 v[44:45], v[42:43], v[54:55]
	v_pk_add_f32 v[48:49], v[48:49], v[52:53]
	v_cvt_pk_bf16_f32 v42, v46, v47
	v_lshlrev_b32_e32 v46, 16, v140
	v_cvt_pk_bf16_f32 v43, v48, v49
	v_cvt_pk_bf16_f32 v44, v44, v45
	v_cvt_pk_bf16_f32 v45, v50, v51
	v_mov_b32_e32 v50, v1
	v_dot2c_f32_bf16_e32 v50, v42, v42
	v_dot2c_f32_bf16_e32 v50, v43, v43
	v_dot2c_f32_bf16_e32 v50, v44, v44
	global_store_dwordx4 v[216:217], v[42:45], off offset:2048 nt
	v_dot2c_f32_bf16_e32 v50, v45, v45
	v_and_b32_e32 v47, 0xffff0000, v140
	v_lshlrev_b32_e32 v42, 16, v138
	v_and_b32_e32 v43, 0xffff0000, v138
	v_lshlrev_b32_e32 v48, 16, v141
	v_and_b32_e32 v49, 0xffff0000, v141
	v_lshlrev_b32_e32 v44, 16, v139
	v_and_b32_e32 v45, 0xffff0000, v139
	v_pk_add_f32 v[38:39], v[38:39], v[42:43]
	v_pk_add_f32 v[42:43], v[36:37], v[48:49]
	v_pk_add_f32 v[36:37], v[34:35], v[46:47]
	v_cvt_pk_bf16_f32 v34, v38, v39
	v_pk_add_f32 v[40:41], v[40:41], v[44:45]
	v_dot2c_f32_bf16_e32 v50, v34, v34
	v_cvt_pk_bf16_f32 v35, v40, v41
	v_cvt_pk_bf16_f32 v36, v36, v37
	v_cvt_pk_bf16_f32 v37, v42, v43
	global_store_dwordx4 v[214:215], v[34:37], off offset:2048 nt
	v_dot2c_f32_bf16_e32 v50, v35, v35
	v_dot2c_f32_bf16_e32 v50, v36, v36
	v_lshlrev_b32_e32 v34, 16, v134
	v_and_b32_e32 v35, 0xffff0000, v134
	v_lshlrev_b32_e32 v38, 16, v136
	v_and_b32_e32 v39, 0xffff0000, v136
	v_lshlrev_b32_e32 v40, 16, v137
	v_and_b32_e32 v41, 0xffff0000, v137
	v_dot2c_f32_bf16_e32 v50, v37, v37
	v_lshlrev_b32_e32 v36, 16, v135
	v_and_b32_e32 v37, 0xffff0000, v135
	v_pk_add_f32 v[30:31], v[30:31], v[34:35]
	v_pk_add_f32 v[34:35], v[28:29], v[40:41]
	v_pk_add_f32 v[28:29], v[26:27], v[38:39]
	v_pk_add_f32 v[32:33], v[32:33], v[36:37]
	v_cvt_pk_bf16_f32 v26, v30, v31
	v_lshlrev_b32_e32 v30, 16, v132
	v_cvt_pk_bf16_f32 v27, v32, v33
	v_cvt_pk_bf16_f32 v28, v28, v29
	v_cvt_pk_bf16_f32 v29, v34, v35
	v_mov_b32_e32 v34, v1
	v_dot2c_f32_bf16_e32 v34, v26, v26
	v_dot2c_f32_bf16_e32 v34, v27, v27
	v_dot2c_f32_bf16_e32 v34, v28, v28
	global_store_dwordx4 v[212:213], v[26:29], off nt
	v_dot2c_f32_bf16_e32 v34, v29, v29
	v_and_b32_e32 v31, 0xffff0000, v132
	v_lshlrev_b32_e32 v26, 16, v130
	v_and_b32_e32 v27, 0xffff0000, v130
	v_lshlrev_b32_e32 v32, 16, v133
	v_and_b32_e32 v33, 0xffff0000, v133
	v_lshlrev_b32_e32 v28, 16, v131
	v_and_b32_e32 v29, 0xffff0000, v131
	v_pk_add_f32 v[22:23], v[22:23], v[26:27]
	v_pk_add_f32 v[26:27], v[20:21], v[32:33]
	v_pk_add_f32 v[20:21], v[18:19], v[30:31]
	v_cvt_pk_bf16_f32 v18, v22, v23
	v_pk_add_f32 v[24:25], v[24:25], v[28:29]
	v_dot2c_f32_bf16_e32 v34, v18, v18
	v_cvt_pk_bf16_f32 v19, v24, v25
	v_cvt_pk_bf16_f32 v20, v20, v21
	v_cvt_pk_bf16_f32 v21, v26, v27
	global_store_dwordx4 v[210:211], v[18:21], off nt
	v_dot2c_f32_bf16_e32 v34, v19, v19
	v_dot2c_f32_bf16_e32 v34, v20, v20
	v_lshlrev_b32_e32 v18, 16, v122
	v_and_b32_e32 v19, 0xffff0000, v122
	v_lshlrev_b32_e32 v22, 16, v124
	v_and_b32_e32 v23, 0xffff0000, v124
	v_lshlrev_b32_e32 v24, 16, v125
	v_and_b32_e32 v25, 0xffff0000, v125
	v_dot2c_f32_bf16_e32 v34, v21, v21
	v_lshlrev_b32_e32 v20, 16, v123
	v_and_b32_e32 v21, 0xffff0000, v123
	v_pk_add_f32 v[14:15], v[14:15], v[18:19]
	v_pk_add_f32 v[18:19], v[12:13], v[24:25]
	v_pk_add_f32 v[12:13], v[10:11], v[22:23]
	v_pk_add_f32 v[16:17], v[16:17], v[20:21]
	v_cvt_pk_bf16_f32 v10, v14, v15
	v_lshlrev_b32_e32 v14, 16, v116
	v_cvt_pk_bf16_f32 v11, v16, v17
	v_cvt_pk_bf16_f32 v12, v12, v13
	v_cvt_pk_bf16_f32 v13, v18, v19
	v_mov_b32_e32 v18, v1
	v_dot2c_f32_bf16_e32 v18, v10, v10
	v_dot2c_f32_bf16_e32 v18, v11, v11
	v_dot2c_f32_bf16_e32 v18, v12, v12
	global_store_dwordx4 v[212:213], v[10:13], off offset:2048 nt
	v_dot2c_f32_bf16_e32 v18, v13, v13
	v_and_b32_e32 v15, 0xffff0000, v116
	v_lshlrev_b32_e32 v10, 16, v114
	v_and_b32_e32 v11, 0xffff0000, v114
	v_lshlrev_b32_e32 v16, 16, v117
	v_and_b32_e32 v17, 0xffff0000, v117
	v_lshlrev_b32_e32 v12, 16, v115
	v_and_b32_e32 v13, 0xffff0000, v115
	v_pk_add_f32 v[6:7], v[6:7], v[10:11]
	v_pk_add_f32 v[10:11], v[4:5], v[16:17]
	v_pk_add_f32 v[4:5], v[2:3], v[14:15]
	v_cvt_pk_bf16_f32 v2, v6, v7
	v_pk_add_f32 v[8:9], v[8:9], v[12:13]
	v_dot2c_f32_bf16_e32 v18, v2, v2
	v_cvt_pk_bf16_f32 v3, v8, v9
	v_cvt_pk_bf16_f32 v4, v4, v5
	v_cvt_pk_bf16_f32 v5, v10, v11
	global_store_dwordx4 v[210:211], v[2:5], off offset:2048 nt
	v_dot2c_f32_bf16_e32 v18, v3, v3
	v_dot2c_f32_bf16_e32 v18, v4, v4
	v_dot2c_f32_bf16_e32 v18, v5, v5
	ds_bpermute_b32 v2, v241, v166
	ds_bpermute_b32 v3, v241, v106
	ds_bpermute_b32 v4, v241, v90
	ds_bpermute_b32 v5, v241, v82
	ds_bpermute_b32 v6, v241, v66
	ds_bpermute_b32 v7, v241, v50
	ds_bpermute_b32 v8, v241, v34
	ds_bpermute_b32 v9, v241, v18
	s_waitcnt lgkmcnt(7)
	v_add_f32_e32 v2, v166, v2
	s_waitcnt lgkmcnt(6)
	v_add_f32_e32 v3, v106, v3
	s_waitcnt lgkmcnt(5)
	v_add_f32_e32 v4, v90, v4
	s_waitcnt lgkmcnt(4)
	v_add_f32_e32 v5, v82, v5
	s_waitcnt lgkmcnt(3)
	v_add_f32_e32 v6, v66, v6
	s_waitcnt lgkmcnt(2)
	v_add_f32_e32 v7, v50, v7
	s_waitcnt lgkmcnt(1)
	v_add_f32_e32 v8, v34, v8
	s_waitcnt lgkmcnt(0)
	v_add_f32_e32 v11, v18, v9
	v_bitop3_b32 v17, v239, s21, v240 bitop3:0x36
	ds_bpermute_b32 v9, v17, v2
	ds_bpermute_b32 v10, v17, v3
	ds_bpermute_b32 v12, v17, v4
	ds_bpermute_b32 v13, v17, v5
	ds_bpermute_b32 v14, v17, v6
	ds_bpermute_b32 v15, v17, v7
	ds_bpermute_b32 v16, v17, v8
	ds_bpermute_b32 v17, v17, v11
	s_and_saveexec_b64 s[26:27], vcc
	s_cbranch_execz .LBB0_879
	s_lshl_b32 s11, s11, 8
	s_add_i32 s11, s11, s57
	s_waitcnt lgkmcnt(5)
	v_add_f32_e32 v12, v4, v12
	v_add_f32_e32 v4, v2, v9
	v_or_b32_e32 v2, s11, v238
	s_mov_b32 s11, 0x49800000
	v_fma_f32 v4, v4, s11, 0.5
	v_trunc_f32_e32 v4, v4
	s_waitcnt lgkmcnt(4)
	v_add_f32_e32 v13, v5, v13
	v_mul_f32_e32 v5, 0x2f800000, v4
	v_floor_f32_e32 v5, v5
	v_fmac_f32_e32 v4, 0xcf800000, v5
	v_cvt_u32_f32_e32 v4, v4
	v_cvt_u32_f32_e32 v5, v5
	v_add_f32_e32 v10, v3, v10
	v_ashrrev_i32_e32 v3, 31, v2
	v_lshl_add_u64 v[2:3], v[2:3], 3, s[38:39]
	global_atomic_add_x2 v[2:3], v[4:5], off
	v_fma_f32 v4, v10, s11, 0.5
	v_trunc_f32_e32 v4, v4
	v_mul_f32_e32 v5, 0x2f800000, v4
	v_floor_f32_e32 v5, v5
	v_fmac_f32_e32 v4, 0xcf800000, v5
	v_cvt_u32_f32_e32 v4, v4
	v_cvt_u32_f32_e32 v5, v5
	s_waitcnt lgkmcnt(3)
	v_add_f32_e32 v6, v6, v14
	s_waitcnt lgkmcnt(2)
	v_add_f32_e32 v7, v7, v15
	s_waitcnt lgkmcnt(1)
	v_add_f32_e32 v8, v8, v16
	global_atomic_add_x2 v[2:3], v[4:5], off offset:128
	v_fma_f32 v4, v12, s11, 0.5
	v_trunc_f32_e32 v4, v4
	v_mul_f32_e32 v5, 0x2f800000, v4
	v_floor_f32_e32 v5, v5
	v_fmac_f32_e32 v4, 0xcf800000, v5
	v_cvt_u32_f32_e32 v4, v4
	v_cvt_u32_f32_e32 v5, v5
	s_waitcnt lgkmcnt(0)
	v_add_f32_e32 v11, v11, v17
	global_atomic_add_x2 v[2:3], v[4:5], off offset:256
	v_fma_f32 v4, v13, s11, 0.5
	v_trunc_f32_e32 v4, v4
	v_mul_f32_e32 v5, 0x2f800000, v4
	v_floor_f32_e32 v5, v5
	v_fmac_f32_e32 v4, 0xcf800000, v5
	v_cvt_u32_f32_e32 v4, v4
	v_cvt_u32_f32_e32 v5, v5
	global_atomic_add_x2 v[2:3], v[4:5], off offset:384
	v_fma_f32 v4, v6, s11, 0.5
	v_trunc_f32_e32 v4, v4
	v_mul_f32_e32 v5, 0x2f800000, v4
	v_floor_f32_e32 v5, v5
	v_fmac_f32_e32 v4, 0xcf800000, v5
	v_cvt_u32_f32_e32 v4, v4
	v_cvt_u32_f32_e32 v5, v5
	global_atomic_add_x2 v[2:3], v[4:5], off offset:1024
	v_fma_f32 v4, v7, s11, 0.5
	v_trunc_f32_e32 v4, v4
	v_mul_f32_e32 v5, 0x2f800000, v4
	v_floor_f32_e32 v5, v5
	v_fmac_f32_e32 v4, 0xcf800000, v5
	v_cvt_u32_f32_e32 v4, v4
	v_cvt_u32_f32_e32 v5, v5
	global_atomic_add_x2 v[2:3], v[4:5], off offset:1152
	v_fma_f32 v4, v8, s11, 0.5
	v_trunc_f32_e32 v4, v4
	v_mul_f32_e32 v5, 0x2f800000, v4
	v_floor_f32_e32 v5, v5
	v_fmac_f32_e32 v4, 0xcf800000, v5
	v_cvt_u32_f32_e32 v4, v4
	v_cvt_u32_f32_e32 v5, v5
	global_atomic_add_x2 v[2:3], v[4:5], off offset:1280
	v_fma_f32 v4, v11, s11, 0.5
	v_trunc_f32_e32 v4, v4
	v_mul_f32_e32 v5, 0x2f800000, v4
	v_floor_f32_e32 v5, v5
	v_fmac_f32_e32 v4, 0xcf800000, v5
	v_cvt_u32_f32_e32 v4, v4
	v_cvt_u32_f32_e32 v5, v5
	global_atomic_add_x2 v[2:3], v[4:5], off offset:1408
	s_branch .LBB0_879

.LBB0_1002:
	s_or_b64 exec, exec, s[26:27]
	s_lshl_b32 s21, s21, 4
	s_lshl_b32 s11, s11, 2
	s_add_i32 s21, s21, s11
	s_or_b32 s26, s21, s68
	s_ashr_i32 s27, s26, 31
	s_lshl_b64 s[26:27], s[26:27], 15
	v_ashrrev_i32_e32 v133, 31, v132
	s_add_u32 s26, s61, s26
	s_addc_u32 s27, s62, s27
	v_lshlrev_b64 v[132:133], 7, v[132:133]
	v_lshl_add_u64 v[132:133], s[26:27], 0, v[132:133]
	s_waitcnt lgkmcnt(0)
	v_lshlrev_b32_e32 v134, 3, v131
	s_waitcnt lgkmcnt(0)
	s_barrier
	v_lshl_add_u64 v[132:133], v[132:133], 0, s[94:95]
	v_ashrrev_i32_e32 v135, 31, v134
	v_lshl_add_u64 v[136:137], v[134:135], 1, v[132:133]
	ds_read_b128 v[132:135], v170 offset:4096
	s_mov_b32 s11, 0x10000
	s_mov_b64 s[28:29], 0x2000
	s_waitcnt lgkmcnt(0)
	v_mov_b32_e32 v138, v133
	v_mov_b32_e32 v139, v134
	v_mov_b32_e32 v133, v135
	v_pk_add_f32 v[132:133], v[138:139], v[132:133]
	s_nop 0
	v_add_f32_e32 v131, v132, v133
	v_div_scale_f32 v132, s[26:27], v131, v131, 1.0
	v_rcp_f32_e32 v133, v132
	s_nop 0
	v_fma_f32 v134, -v132, v133, 1.0
	v_fmac_f32_e32 v133, v134, v133
	v_div_scale_f32 v134, vcc, 1.0, v131, 1.0
	v_mul_f32_e32 v135, v134, v133
	v_fma_f32 v138, -v132, v135, v134
	v_fmac_f32_e32 v135, v138, v133
	v_fma_f32 v132, -v132, v135, v134
	v_div_fmas_f32 v132, v132, v133, v135
	v_div_fixup_f32 v132, v132, v131, 1.0
	v_pk_mul_f32 v[120:121], v[120:121], v[132:133] op_sel_hi:[1,0]
	v_pk_mul_f32 v[102:103], v[102:103], v[132:133] op_sel_hi:[1,0]
	v_pk_mul_f32 v[98:99], v[98:99], v[132:133] op_sel_hi:[1,0]
	v_pk_mul_f32 v[128:129], v[128:129], v[132:133] op_sel_hi:[1,0]
	v_pk_mul_f32 v[134:135], v[118:119], v[132:133] op_sel_hi:[1,0]
	v_cvt_pk_bf16_f32 v118, v102, v103
	v_cvt_pk_bf16_f32 v119, v120, v121
	v_pk_mul_f32 v[102:103], v[114:115], v[132:133] op_sel_hi:[1,0]
	v_cvt_pk_bf16_f32 v120, v134, v135
	v_cvt_pk_bf16_f32 v121, v128, v129
	global_store_dwordx4 v[136:137], v[118:121], off nt
	v_pk_mul_f32 v[116:117], v[116:117], v[132:133] op_sel_hi:[1,0]
	v_cvt_pk_bf16_f32 v114, v98, v99
	v_add_co_u32_e32 v98, vcc, s11, v136
	v_pk_mul_f32 v[118:119], v[126:127], v[132:133] op_sel_hi:[1,0]
	v_cvt_pk_bf16_f32 v115, v102, v103
	v_cvt_pk_bf16_f32 v116, v116, v117
	s_nop 0
	v_addc_co_u32_e32 v99, vcc, 0, v137, vcc
	v_cvt_pk_bf16_f32 v117, v118, v119
	v_lshl_add_u64 v[102:103], v[136:137], 0, s[12:13]
	global_store_dwordx4 v[98:99], v[114:117], off nt
	ds_read_b128 v[114:117], v170 offset:4352
	s_waitcnt lgkmcnt(0)
	v_mov_b32_e32 v98, v115
	v_mov_b32_e32 v99, v116
	v_mov_b32_e32 v115, v117
	v_pk_add_f32 v[98:99], v[98:99], v[114:115]
	s_nop 0
	v_add_f32_e32 v98, v98, v99
	v_div_scale_f32 v99, s[26:27], v98, v98, 1.0
	v_rcp_f32_e32 v114, v99
	s_nop 0
	v_fma_f32 v115, -v99, v114, 1.0
	v_fmac_f32_e32 v114, v115, v114
	v_div_scale_f32 v115, vcc, 1.0, v98, 1.0
	v_mul_f32_e32 v116, v115, v114
	v_fma_f32 v117, -v99, v116, v115
	v_fmac_f32_e32 v116, v117, v114
	v_fma_f32 v99, -v99, v116, v115
	v_div_fmas_f32 v99, v99, v114, v116
	v_div_fixup_f32 v114, v99, v98, 1.0
	v_pk_mul_f32 v[98:99], v[112:113], v[114:115] op_sel_hi:[1,0]
	v_pk_mul_f32 v[96:97], v[96:97], v[114:115] op_sel_hi:[1,0]
	v_pk_mul_f32 v[112:113], v[124:125], v[114:115] op_sel_hi:[1,0]
	v_pk_mul_f32 v[108:109], v[108:109], v[114:115] op_sel_hi:[1,0]
	v_cvt_pk_bf16_f32 v96, v96, v97
	v_cvt_pk_bf16_f32 v97, v98, v99
	v_pk_mul_f32 v[82:83], v[82:83], v[114:115] op_sel_hi:[1,0]
	v_cvt_pk_bf16_f32 v98, v108, v109
	v_cvt_pk_bf16_f32 v99, v112, v113
	global_store_dwordx4 v[102:103], v[96:99], off nt
	v_pk_mul_f32 v[104:105], v[104:105], v[114:115] op_sel_hi:[1,0]
	s_nop 0
	v_pk_mul_f32 v[98:99], v[100:101], v[114:115] op_sel_hi:[1,0]
	v_pk_mul_f32 v[100:101], v[122:123], v[114:115] op_sel_hi:[1,0]
	v_cvt_pk_bf16_f32 v96, v82, v83
	v_add_co_u32_e32 v82, vcc, s11, v102
	v_cvt_pk_bf16_f32 v97, v98, v99
	v_cvt_pk_bf16_f32 v98, v104, v105
	v_cvt_pk_bf16_f32 v99, v100, v101
	v_lshl_add_u64 v[100:101], v[102:103], 0, s[12:13]
	s_nop 0
	v_addc_co_u32_e32 v83, vcc, 0, v103, vcc
	global_store_dwordx4 v[82:83], v[96:99], off nt
	ds_read_b128 v[96:99], v170 offset:4608
	s_waitcnt lgkmcnt(0)
	v_mov_b32_e32 v82, v97
	v_mov_b32_e32 v83, v98
	v_mov_b32_e32 v97, v99
	v_pk_add_f32 v[82:83], v[82:83], v[96:97]
	s_nop 0
	v_add_f32_e32 v82, v82, v83
	v_div_scale_f32 v83, s[26:27], v82, v82, 1.0
	v_rcp_f32_e32 v96, v83
	s_nop 0
	v_fma_f32 v97, -v83, v96, 1.0
	v_fmac_f32_e32 v96, v97, v96
	v_div_scale_f32 v97, vcc, 1.0, v82, 1.0
	v_mul_f32_e32 v98, v97, v96
	v_fma_f32 v99, -v83, v98, v97
	v_fmac_f32_e32 v98, v99, v96
	v_fma_f32 v83, -v83, v98, v97
	v_div_fmas_f32 v83, v83, v96, v98
	v_div_fixup_f32 v96, v83, v82, 1.0
	v_pk_mul_f32 v[82:83], v[94:95], v[96:97] op_sel_hi:[1,0]
	v_pk_mul_f32 v[80:81], v[80:81], v[96:97] op_sel_hi:[1,0]
	v_pk_mul_f32 v[94:95], v[110:111], v[96:97] op_sel_hi:[1,0]
	v_pk_mul_f32 v[92:93], v[92:93], v[96:97] op_sel_hi:[1,0]
	v_cvt_pk_bf16_f32 v80, v80, v81
	v_cvt_pk_bf16_f32 v81, v82, v83
	v_pk_mul_f32 v[72:73], v[72:73], v[96:97] op_sel_hi:[1,0]
	v_cvt_pk_bf16_f32 v82, v92, v93
	v_cvt_pk_bf16_f32 v83, v94, v95
	global_store_dwordx4 v[100:101], v[80:83], off nt
	v_pk_mul_f32 v[88:89], v[88:89], v[96:97] op_sel_hi:[1,0]
	s_nop 0
	v_pk_mul_f32 v[82:83], v[84:85], v[96:97] op_sel_hi:[1,0]
	v_pk_mul_f32 v[84:85], v[106:107], v[96:97] op_sel_hi:[1,0]
	v_cvt_pk_bf16_f32 v80, v72, v73
	v_add_co_u32_e32 v72, vcc, s11, v100
	v_cvt_pk_bf16_f32 v81, v82, v83
	v_cvt_pk_bf16_f32 v82, v88, v89
	v_cvt_pk_bf16_f32 v83, v84, v85
	v_lshl_add_u64 v[84:85], v[100:101], 0, s[12:13]
	s_nop 0
	v_addc_co_u32_e32 v73, vcc, 0, v101, vcc
	global_store_dwordx4 v[72:73], v[80:83], off nt
	ds_read_b128 v[80:83], v170 offset:4864
	s_waitcnt lgkmcnt(0)
	v_mov_b32_e32 v72, v81
	v_mov_b32_e32 v73, v82
	v_mov_b32_e32 v81, v83
	v_pk_add_f32 v[72:73], v[72:73], v[80:81]
	s_nop 0
	v_add_f32_e32 v72, v72, v73
	v_div_scale_f32 v73, s[26:27], v72, v72, 1.0
	v_rcp_f32_e32 v80, v73
	s_nop 0
	v_fma_f32 v81, -v73, v80, 1.0
	v_fmac_f32_e32 v80, v81, v80
	v_div_scale_f32 v81, vcc, 1.0, v72, 1.0
	v_mul_f32_e32 v82, v81, v80
	v_fma_f32 v83, -v73, v82, v81
	v_fmac_f32_e32 v82, v83, v80
	v_fma_f32 v73, -v73, v82, v81
	v_div_fmas_f32 v73, v73, v80, v82
	v_div_fixup_f32 v72, v73, v72, 1.0
	v_pk_mul_f32 v[78:79], v[78:79], v[72:73] op_sel_hi:[1,0]
	v_pk_mul_f32 v[66:67], v[66:67], v[72:73] op_sel_hi:[1,0]
	v_pk_mul_f32 v[62:63], v[62:63], v[72:73] op_sel_hi:[1,0]
	v_pk_mul_f32 v[80:81], v[90:91], v[72:73] op_sel_hi:[1,0]
	v_pk_mul_f32 v[82:83], v[76:77], v[72:73] op_sel_hi:[1,0]
	v_cvt_pk_bf16_f32 v76, v66, v67
	v_cvt_pk_bf16_f32 v77, v78, v79
	v_pk_mul_f32 v[66:67], v[70:71], v[72:73] op_sel_hi:[1,0]
	v_cvt_pk_bf16_f32 v78, v82, v83
	v_cvt_pk_bf16_f32 v79, v80, v81
	global_store_dwordx4 v[84:85], v[76:79], off nt
	v_cvt_pk_bf16_f32 v70, v62, v63
	v_add_co_u32_e32 v62, vcc, s11, v84
	s_nop 0
	v_pk_mul_f32 v[76:77], v[86:87], v[72:73] op_sel_hi:[1,0]
	v_pk_mul_f32 v[72:73], v[74:75], v[72:73] op_sel_hi:[1,0]
	v_addc_co_u32_e32 v63, vcc, 0, v85, vcc
	v_cvt_pk_bf16_f32 v71, v66, v67
	v_cvt_pk_bf16_f32 v72, v72, v73
	v_cvt_pk_bf16_f32 v73, v76, v77
	global_store_dwordx4 v[62:63], v[70:73], off nt
	v_lshl_add_u64 v[62:63], v[84:85], 0, s[12:13]
	s_nop 0
	v_lshl_add_u64 v[62:63], v[62:63], 0, s[28:29]
	ds_read_b128 v[70:73], v170 offset:6144
	s_waitcnt lgkmcnt(0)
	v_mov_b32_e32 v66, v71
	v_mov_b32_e32 v67, v72
	v_mov_b32_e32 v71, v73
	v_pk_add_f32 v[66:67], v[66:67], v[70:71]
	s_nop 0
	v_add_f32_e32 v66, v66, v67
	v_div_scale_f32 v67, s[26:27], v66, v66, 1.0
	v_rcp_f32_e32 v70, v67
	s_nop 0
	v_fma_f32 v71, -v67, v70, 1.0
	v_fmac_f32_e32 v70, v71, v70
	v_div_scale_f32 v71, vcc, 1.0, v66, 1.0
	v_mul_f32_e32 v72, v71, v70
	v_fma_f32 v73, -v67, v72, v71
	v_fmac_f32_e32 v72, v73, v70
	v_fma_f32 v67, -v67, v72, v71
	v_div_fmas_f32 v67, v67, v70, v72
	v_div_fixup_f32 v66, v67, v66, 1.0
	v_pk_mul_f32 v[60:61], v[60:61], v[66:67] op_sel_hi:[1,0]
	v_pk_mul_f32 v[48:49], v[48:49], v[66:67] op_sel_hi:[1,0]
	v_pk_mul_f32 v[36:37], v[36:37], v[66:67] op_sel_hi:[1,0]
	v_pk_mul_f32 v[68:69], v[68:69], v[66:67] op_sel_hi:[1,0]
	v_pk_mul_f32 v[70:71], v[58:59], v[66:67] op_sel_hi:[1,0]
	v_cvt_pk_bf16_f32 v58, v48, v49
	v_cvt_pk_bf16_f32 v59, v60, v61
	v_pk_mul_f32 v[50:51], v[50:51], v[66:67] op_sel_hi:[1,0]
	v_cvt_pk_bf16_f32 v60, v70, v71
	v_cvt_pk_bf16_f32 v61, v68, v69
	global_store_dwordx4 v[62:63], v[58:61], off nt
	v_cvt_pk_bf16_f32 v48, v36, v37
	v_add_co_u32_e32 v36, vcc, s11, v62
	s_nop 0
	v_pk_mul_f32 v[58:59], v[64:65], v[66:67] op_sel_hi:[1,0]
	v_addc_co_u32_e32 v37, vcc, 0, v63, vcc
	v_pk_mul_f32 v[54:55], v[54:55], v[66:67] op_sel_hi:[1,0]
	v_cvt_pk_bf16_f32 v49, v50, v51
	s_nop 0
	v_cvt_pk_bf16_f32 v50, v54, v55
	v_cvt_pk_bf16_f32 v51, v58, v59
	global_store_dwordx4 v[36:37], v[48:51], off nt
	v_lshl_add_u64 v[36:37], v[62:63], 0, s[12:13]
	ds_read_b128 v[48:51], v170 offset:6400
	s_waitcnt lgkmcnt(0)
	v_mov_b32_e32 v54, v49
	v_mov_b32_e32 v55, v50
	v_mov_b32_e32 v49, v51
	v_pk_add_f32 v[48:49], v[54:55], v[48:49]
	s_nop 0
	v_add_f32_e32 v48, v48, v49
	v_div_scale_f32 v49, s[26:27], v48, v48, 1.0
	v_rcp_f32_e32 v50, v49
	s_nop 0
	v_fma_f32 v51, -v49, v50, 1.0
	v_fmac_f32_e32 v50, v51, v50
	v_div_scale_f32 v51, vcc, 1.0, v48, 1.0
	v_mul_f32_e32 v54, v51, v50
	v_fma_f32 v55, -v49, v54, v51
	v_fmac_f32_e32 v54, v55, v50
	v_fma_f32 v49, -v49, v54, v51
	v_div_fmas_f32 v49, v49, v50, v54
	v_div_fixup_f32 v48, v49, v48, 1.0
	v_pk_mul_f32 v[46:47], v[46:47], v[48:49] op_sel_hi:[1,0]
	v_pk_mul_f32 v[32:33], v[32:33], v[48:49] op_sel_hi:[1,0]
	v_pk_mul_f32 v[22:23], v[22:23], v[48:49] op_sel_hi:[1,0]
	v_pk_mul_f32 v[50:51], v[56:57], v[48:49] op_sel_hi:[1,0]
	v_pk_mul_f32 v[54:55], v[44:45], v[48:49] op_sel_hi:[1,0]
	v_cvt_pk_bf16_f32 v44, v32, v33
	v_cvt_pk_bf16_f32 v45, v46, v47
	v_pk_mul_f32 v[34:35], v[34:35], v[48:49] op_sel_hi:[1,0]
	v_cvt_pk_bf16_f32 v46, v54, v55
	v_cvt_pk_bf16_f32 v47, v50, v51
	global_store_dwordx4 v[36:37], v[44:47], off nt
	v_cvt_pk_bf16_f32 v32, v22, v23
	v_add_co_u32_e32 v22, vcc, s11, v36
	s_nop 0
	v_pk_mul_f32 v[44:45], v[52:53], v[48:49] op_sel_hi:[1,0]
	v_pk_mul_f32 v[40:41], v[40:41], v[48:49] op_sel_hi:[1,0]
	v_cvt_pk_bf16_f32 v33, v34, v35
	v_addc_co_u32_e32 v23, vcc, 0, v37, vcc
	v_cvt_pk_bf16_f32 v34, v40, v41
	v_cvt_pk_bf16_f32 v35, v44, v45
	v_lshl_add_u64 v[36:37], v[36:37], 0, s[12:13]
	global_store_dwordx4 v[22:23], v[32:35], off nt
	ds_read_b128 v[32:35], v170 offset:6656
	s_waitcnt lgkmcnt(0)
	v_mov_b32_e32 v22, v33
	v_mov_b32_e32 v23, v34
	v_mov_b32_e32 v33, v35
	v_pk_add_f32 v[22:23], v[22:23], v[32:33]
	s_nop 0
	v_add_f32_e32 v22, v22, v23
	v_div_scale_f32 v23, s[26:27], v22, v22, 1.0
	v_rcp_f32_e32 v32, v23
	s_nop 0
	v_fma_f32 v33, -v23, v32, 1.0
	v_fmac_f32_e32 v32, v33, v32
	v_div_scale_f32 v33, vcc, 1.0, v22, 1.0
	v_mul_f32_e32 v34, v33, v32
	v_fma_f32 v35, -v23, v34, v33
	v_fmac_f32_e32 v34, v35, v32
	v_fma_f32 v23, -v23, v34, v33
	v_div_fmas_f32 v23, v23, v32, v34
	v_div_fixup_f32 v22, v23, v22, 1.0
	v_pk_mul_f32 v[30:31], v[30:31], v[22:23] op_sel_hi:[1,0]
	v_pk_mul_f32 v[16:17], v[16:17], v[22:23] op_sel_hi:[1,0]
	v_pk_mul_f32 v[34:35], v[28:29], v[22:23] op_sel_hi:[1,0]
	v_cvt_pk_bf16_f32 v28, v16, v17
	v_cvt_pk_bf16_f32 v29, v30, v31
	v_pk_mul_f32 v[10:11], v[10:11], v[22:23] op_sel_hi:[1,0]
	v_pk_mul_f32 v[32:33], v[42:43], v[22:23] op_sel_hi:[1,0]
	v_cvt_pk_bf16_f32 v30, v34, v35
	v_pk_mul_f32 v[16:17], v[20:21], v[22:23] op_sel_hi:[1,0]
	v_cvt_pk_bf16_f32 v31, v32, v33
	global_store_dwordx4 v[36:37], v[28:31], off nt
	v_cvt_pk_bf16_f32 v20, v10, v11
	v_add_co_u32_e32 v10, vcc, s11, v36
	s_nop 0
	v_pk_mul_f32 v[28:29], v[38:39], v[22:23] op_sel_hi:[1,0]
	v_pk_mul_f32 v[22:23], v[26:27], v[22:23] op_sel_hi:[1,0]
	v_cvt_pk_bf16_f32 v21, v16, v17
	v_addc_co_u32_e32 v11, vcc, 0, v37, vcc
	v_cvt_pk_bf16_f32 v22, v22, v23
	v_cvt_pk_bf16_f32 v23, v28, v29
	v_lshl_add_u64 v[16:17], v[36:37], 0, s[12:13]
	global_store_dwordx4 v[10:11], v[20:23], off nt
	ds_read_b128 v[20:23], v170 offset:6912
	s_waitcnt lgkmcnt(0)
	v_mov_b32_e32 v10, v21
	v_mov_b32_e32 v11, v22
	v_mov_b32_e32 v21, v23
	v_pk_add_f32 v[10:11], v[10:11], v[20:21]
	s_nop 0
	v_add_f32_e32 v10, v10, v11
	v_div_scale_f32 v11, s[26:27], v10, v10, 1.0
	v_rcp_f32_e32 v20, v11
	s_mov_b64 s[26:27], -1
	v_fma_f32 v21, -v11, v20, 1.0
	v_fmac_f32_e32 v20, v21, v20
	v_div_scale_f32 v21, vcc, 1.0, v10, 1.0
	v_mul_f32_e32 v22, v21, v20
	v_fma_f32 v23, -v11, v22, v21
	v_fmac_f32_e32 v22, v23, v20
	v_fma_f32 v11, -v11, v22, v21
	v_div_fmas_f32 v11, v11, v20, v22
	v_div_fixup_f32 v20, v11, v10, 1.0
	v_pk_mul_f32 v[4:5], v[4:5], v[20:21] op_sel_hi:[1,0]
	v_pk_mul_f32 v[12:13], v[12:13], v[20:21] op_sel_hi:[1,0]
	v_cvt_pk_bf16_f32 v10, v4, v5
	v_pk_mul_f32 v[4:5], v[6:7], v[20:21] op_sel_hi:[1,0]
	v_pk_mul_f32 v[2:3], v[2:3], v[20:21] op_sel_hi:[1,0]
	v_pk_mul_f32 v[6:7], v[18:19], v[20:21] op_sel_hi:[1,0]
	v_pk_mul_f32 v[14:15], v[14:15], v[20:21] op_sel_hi:[1,0]
	v_pk_mul_f32 v[22:23], v[24:25], v[20:21] op_sel_hi:[1,0]
	v_cvt_pk_bf16_f32 v11, v14, v15
	v_cvt_pk_bf16_f32 v12, v12, v13
	v_pk_mul_f32 v[8:9], v[8:9], v[20:21] op_sel_hi:[1,0]
	v_cvt_pk_bf16_f32 v13, v22, v23
	global_store_dwordx4 v[16:17], v[10:13], off nt
	v_cvt_pk_bf16_f32 v2, v2, v3
	v_cvt_pk_bf16_f32 v3, v4, v5
	v_cvt_pk_bf16_f32 v4, v8, v9
	v_cvt_pk_bf16_f32 v5, v6, v7
	v_add_co_u32_e32 v6, vcc, 0x10000, v16
	s_nop 1
	v_addc_co_u32_e32 v7, vcc, 0, v17, vcc
	global_store_dwordx4 v[6:7], v[2:5], off nt
	s_and_b64 vcc, exec, s[40:41]
	s_nop 0
	v_lshl_add_u64 v[2:3], v[16:17], 0, s[12:13]
	s_nop 0
	v_lshl_add_u64 v[2:3], v[2:3], 0, s[28:29]
	s_cbranch_vccnz .LBB0_954
	s_andn2_b64 vcc, exec, s[44:45]
	s_cbranch_vccnz .LBB0_953
	s_barrier
	s_branch .LBB0_953

.LBB0_1075:
	s_lshl_b32 s21, s69, 5
	s_lshl_b32 s11, s11, 2
	s_add_i32 s21, s21, s11
	s_or_b32 s26, s21, s64
	s_ashr_i32 s27, s26, 31
	s_lshl_b64 s[26:27], s[26:27], 8
	v_mbcnt_lo_u32_b32 v211, -1, 0
	v_mbcnt_hi_u32_b32 v211, -1, v211
	s_add_u32 s11, s26, s61
	v_ashrrev_i32_e32 v127, 4, v211
	v_and_b32_e32 v126, 15, v211
	s_addc_u32 s21, s27, s65
	v_lshlrev_b32_e32 v116, 3, v127
	v_or_b32_e32 v114, s11, v126
	v_mov_b32_e32 v115, s21
	v_ashrrev_i32_e32 v117, 31, v116
	v_lshl_add_u64 v[116:117], v[116:117], 1, s[52:53]
	v_lshlrev_b64 v[114:115], 7, v[114:115]
	v_lshl_add_u64 v[226:227], v[116:117], 0, v[114:115]
	global_load_dwordx4 v[194:197], v[226:227], off
	s_mov_b32 s11, 0x10000
	v_add_co_u32_e32 v224, vcc, s11, v226
	s_mov_b32 s11, 0x11000
	s_nop 0
	v_addc_co_u32_e32 v225, vcc, 0, v227, vcc
	v_add_co_u32_e32 v220, vcc, s11, v226
	s_movk_i32 s11, 0x4000
	s_nop 0
	v_addc_co_u32_e32 v221, vcc, 0, v227, vcc
	global_load_dwordx4 v[186:189], v[220:221], off offset:-4096
	global_load_dwordx4 v[182:185], v[226:227], off offset:2048
	global_load_dwordx4 v[178:181], v[224:225], off offset:2048
	v_add_co_u32_e32 v222, vcc, s94, v226
	v_lshlrev_b32_e32 v239, 6, v127
	s_nop 0
	v_addc_co_u32_e32 v223, vcc, 0, v227, vcc
	global_load_dwordx4 v[174:177], v[222:223], off
	global_load_dwordx4 v[170:173], v[220:221], off
	global_load_dwordx4 v[158:161], v[222:223], off offset:2048
	global_load_dwordx4 v[154:157], v[220:221], off offset:2048
	v_add_co_u32_e32 v218, vcc, s11, v226
	s_movk_i32 s11, 0x5000
	s_nop 0
	v_addc_co_u32_e32 v219, vcc, 0, v227, vcc
	v_add_co_u32_e32 v214, vcc, s11, v226
	s_mov_b32 s11, 0x14000
	s_nop 0
	v_addc_co_u32_e32 v215, vcc, 0, v227, vcc
	global_load_dwordx4 v[150:153], v[214:215], off offset:-4096
	v_add_co_u32_e32 v216, vcc, s11, v226
	s_mov_b32 s11, 0x15000
	s_nop 0
	v_addc_co_u32_e32 v217, vcc, 0, v227, vcc
	v_add_co_u32_e32 v212, vcc, s11, v226
	v_lshlrev_b32_e32 v240, 2, v126
	s_nop 0
	v_addc_co_u32_e32 v213, vcc, 0, v227, vcc
	global_load_dwordx4 v[146:149], v[212:213], off offset:-4096
	global_load_dwordx4 v[142:145], v[218:219], off offset:2048
	global_load_dwordx4 v[138:141], v[216:217], off offset:2048
	global_load_dwordx4 v[134:137], v[214:215], off
	global_load_dwordx4 v[130:133], v[212:213], off
	global_load_dwordx4 v[126:129], v[214:215], off offset:2048
	global_load_dwordx4 v[114:117], v[212:213], off offset:2048
	v_bitop3_b32 v241, v239, 64, v240 bitop3:0x36
	s_movk_i32 s11, 0x80
	v_cmp_gt_u32_e32 vcc, 16, v211
	s_waitcnt vmcnt(0)
	v_lshlrev_b32_e32 v190, 16, v194
	v_and_b32_e32 v191, 0xffff0000, v194
	v_lshlrev_b32_e32 v194, 16, v195
	v_and_b32_e32 v195, 0xffff0000, v195
	v_pk_add_f32 v[162:163], v[162:163], v[190:191]
	v_pk_add_f32 v[194:195], v[164:165], v[194:195]
	v_cvt_pk_bf16_f32 v164, v162, v163
	v_mov_b32_e32 v162, v1
	v_lshlrev_b32_e32 v198, 16, v196
	v_and_b32_e32 v199, 0xffff0000, v196
	v_dot2c_f32_bf16_e32 v162, v164, v164
	v_lshlrev_b32_e32 v196, 16, v197
	v_and_b32_e32 v197, 0xffff0000, v197
	v_pk_add_f32 v[166:167], v[166:167], v[198:199]
	v_cvt_pk_bf16_f32 v165, v194, v195
	v_pk_add_f32 v[168:169], v[168:169], v[196:197]
	v_dot2c_f32_bf16_e32 v162, v165, v165
	v_cvt_pk_bf16_f32 v166, v166, v167
	v_cvt_pk_bf16_f32 v167, v168, v169
	global_store_dwordx4 v[226:227], v[164:167], off nt
	v_dot2c_f32_bf16_e32 v162, v166, v166
	v_dot2c_f32_bf16_e32 v162, v167, v167
	v_lshlrev_b32_e32 v164, 16, v186
	v_and_b32_e32 v165, 0xffff0000, v186
	v_lshlrev_b32_e32 v166, 16, v187
	v_and_b32_e32 v167, 0xffff0000, v187
	v_lshlrev_b32_e32 v168, 16, v188
	v_and_b32_e32 v169, 0xffff0000, v188
	v_lshlrev_b32_e32 v186, 16, v189
	v_and_b32_e32 v187, 0xffff0000, v189
	v_pk_add_f32 v[122:123], v[122:123], v[164:165]
	v_pk_add_f32 v[164:165], v[120:121], v[186:187]
	v_pk_add_f32 v[120:121], v[118:119], v[168:169]
	v_cvt_pk_bf16_f32 v118, v122, v123
	v_pk_add_f32 v[124:125], v[124:125], v[166:167]
	v_dot2c_f32_bf16_e32 v162, v118, v118
	v_cvt_pk_bf16_f32 v119, v124, v125
	v_cvt_pk_bf16_f32 v120, v120, v121
	v_cvt_pk_bf16_f32 v121, v164, v165
	global_store_dwordx4 v[220:221], v[118:121], off offset:-4096 nt
	v_dot2c_f32_bf16_e32 v162, v119, v119
	v_dot2c_f32_bf16_e32 v162, v120, v120
	v_lshlrev_b32_e32 v118, 16, v182
	v_and_b32_e32 v119, 0xffff0000, v182
	v_lshlrev_b32_e32 v122, 16, v184
	v_and_b32_e32 v123, 0xffff0000, v184
	v_dot2c_f32_bf16_e32 v162, v121, v121
	v_lshlrev_b32_e32 v120, 16, v183
	v_and_b32_e32 v121, 0xffff0000, v183
	v_lshlrev_b32_e32 v124, 16, v185
	v_and_b32_e32 v125, 0xffff0000, v185
	v_pk_add_f32 v[110:111], v[110:111], v[118:119]
	v_pk_add_f32 v[106:107], v[106:107], v[122:123]
	v_pk_add_f32 v[112:113], v[112:113], v[120:121]
	v_pk_add_f32 v[118:119], v[108:109], v[124:125]
	v_cvt_pk_bf16_f32 v108, v110, v111
	v_cvt_pk_bf16_f32 v109, v112, v113
	v_cvt_pk_bf16_f32 v110, v106, v107
	v_mov_b32_e32 v106, v1
	v_dot2c_f32_bf16_e32 v106, v108, v108
	v_dot2c_f32_bf16_e32 v106, v109, v109
	v_dot2c_f32_bf16_e32 v106, v110, v110
	v_cvt_pk_bf16_f32 v111, v118, v119
	global_store_dwordx4 v[226:227], v[108:111], off offset:2048 nt
	v_dot2c_f32_bf16_e32 v106, v111, v111
	v_lshlrev_b32_e32 v112, 16, v180
	v_lshlrev_b32_e32 v108, 16, v178
	v_and_b32_e32 v109, 0xffff0000, v178
	v_and_b32_e32 v113, 0xffff0000, v180
	v_lshlrev_b32_e32 v118, 16, v181
	v_and_b32_e32 v119, 0xffff0000, v181
	v_lshlrev_b32_e32 v110, 16, v179
	v_and_b32_e32 v111, 0xffff0000, v179
	v_pk_add_f32 v[102:103], v[102:103], v[108:109]
	v_pk_add_f32 v[108:109], v[100:101], v[118:119]
	v_pk_add_f32 v[100:101], v[98:99], v[112:113]
	v_cvt_pk_bf16_f32 v98, v102, v103
	v_pk_add_f32 v[104:105], v[104:105], v[110:111]
	v_dot2c_f32_bf16_e32 v106, v98, v98
	v_cvt_pk_bf16_f32 v99, v104, v105
	v_cvt_pk_bf16_f32 v100, v100, v101
	v_cvt_pk_bf16_f32 v101, v108, v109
	global_store_dwordx4 v[224:225], v[98:101], off offset:2048 nt
	v_dot2c_f32_bf16_e32 v106, v99, v99
	v_dot2c_f32_bf16_e32 v106, v100, v100
	v_lshlrev_b32_e32 v98, 16, v174
	v_and_b32_e32 v99, 0xffff0000, v174
	v_lshlrev_b32_e32 v102, 16, v176
	v_and_b32_e32 v103, 0xffff0000, v176
	v_dot2c_f32_bf16_e32 v106, v101, v101
	v_lshlrev_b32_e32 v100, 16, v175
	v_and_b32_e32 v101, 0xffff0000, v175
	v_lshlrev_b32_e32 v104, 16, v177
	v_and_b32_e32 v105, 0xffff0000, v177
	v_pk_add_f32 v[94:95], v[94:95], v[98:99]
	v_pk_add_f32 v[90:91], v[90:91], v[102:103]
	v_pk_add_f32 v[96:97], v[96:97], v[100:101]
	v_pk_add_f32 v[98:99], v[92:93], v[104:105]
	v_cvt_pk_bf16_f32 v92, v94, v95
	v_cvt_pk_bf16_f32 v93, v96, v97
	v_cvt_pk_bf16_f32 v94, v90, v91
	v_mov_b32_e32 v90, v1
	v_dot2c_f32_bf16_e32 v90, v92, v92
	v_dot2c_f32_bf16_e32 v90, v93, v93
	v_dot2c_f32_bf16_e32 v90, v94, v94
	v_cvt_pk_bf16_f32 v95, v98, v99
	global_store_dwordx4 v[222:223], v[92:95], off nt
	v_dot2c_f32_bf16_e32 v90, v95, v95
	v_lshlrev_b32_e32 v96, 16, v172
	v_lshlrev_b32_e32 v92, 16, v170
	v_and_b32_e32 v93, 0xffff0000, v170
	v_and_b32_e32 v97, 0xffff0000, v172
	v_lshlrev_b32_e32 v98, 16, v173
	v_and_b32_e32 v99, 0xffff0000, v173
	v_lshlrev_b32_e32 v94, 16, v171
	v_and_b32_e32 v95, 0xffff0000, v171
	v_pk_add_f32 v[86:87], v[86:87], v[92:93]
	v_pk_add_f32 v[92:93], v[84:85], v[98:99]
	v_pk_add_f32 v[84:85], v[82:83], v[96:97]
	v_cvt_pk_bf16_f32 v82, v86, v87
	v_pk_add_f32 v[88:89], v[88:89], v[94:95]
	v_dot2c_f32_bf16_e32 v90, v82, v82
	v_cvt_pk_bf16_f32 v83, v88, v89
	v_cvt_pk_bf16_f32 v84, v84, v85
	v_cvt_pk_bf16_f32 v85, v92, v93
	global_store_dwordx4 v[220:221], v[82:85], off nt
	v_dot2c_f32_bf16_e32 v90, v83, v83
	v_dot2c_f32_bf16_e32 v90, v84, v84
	v_lshlrev_b32_e32 v82, 16, v158
	v_and_b32_e32 v83, 0xffff0000, v158
	v_lshlrev_b32_e32 v86, 16, v160
	v_and_b32_e32 v87, 0xffff0000, v160
	v_lshlrev_b32_e32 v88, 16, v161
	v_and_b32_e32 v89, 0xffff0000, v161
	v_dot2c_f32_bf16_e32 v90, v85, v85
	v_lshlrev_b32_e32 v84, 16, v159
	v_and_b32_e32 v85, 0xffff0000, v159
	v_pk_add_f32 v[70:71], v[70:71], v[82:83]
	v_pk_add_f32 v[82:83], v[68:69], v[88:89]
	v_pk_add_f32 v[68:69], v[66:67], v[86:87]
	v_pk_add_f32 v[72:73], v[72:73], v[84:85]
	v_cvt_pk_bf16_f32 v66, v70, v71
	v_lshlrev_b32_e32 v70, 16, v156
	v_cvt_pk_bf16_f32 v67, v72, v73
	v_cvt_pk_bf16_f32 v68, v68, v69
	v_cvt_pk_bf16_f32 v69, v82, v83
	v_mov_b32_e32 v82, v1
	v_dot2c_f32_bf16_e32 v82, v66, v66
	v_dot2c_f32_bf16_e32 v82, v67, v67
	v_dot2c_f32_bf16_e32 v82, v68, v68
	global_store_dwordx4 v[222:223], v[66:69], off offset:2048 nt
	v_dot2c_f32_bf16_e32 v82, v69, v69
	v_and_b32_e32 v71, 0xffff0000, v156
	v_lshlrev_b32_e32 v66, 16, v154
	v_and_b32_e32 v67, 0xffff0000, v154
	v_lshlrev_b32_e32 v68, 16, v155
	v_and_b32_e32 v69, 0xffff0000, v155
	v_lshlrev_b32_e32 v72, 16, v157
	v_and_b32_e32 v73, 0xffff0000, v157
	v_pk_add_f32 v[56:57], v[56:57], v[68:69]
	v_pk_add_f32 v[54:55], v[54:55], v[66:67]
	v_pk_add_f32 v[66:67], v[52:53], v[72:73]
	v_pk_add_f32 v[52:53], v[50:51], v[70:71]
	v_cvt_pk_bf16_f32 v50, v54, v55
	v_cvt_pk_bf16_f32 v51, v56, v57
	v_lshlrev_b32_e32 v54, 16, v152
	v_dot2c_f32_bf16_e32 v82, v50, v50
	v_cvt_pk_bf16_f32 v52, v52, v53
	v_cvt_pk_bf16_f32 v53, v66, v67
	global_store_dwordx4 v[220:221], v[50:53], off offset:2048 nt
	v_dot2c_f32_bf16_e32 v82, v51, v51
	v_dot2c_f32_bf16_e32 v82, v52, v52
	v_lshlrev_b32_e32 v50, 16, v150
	v_and_b32_e32 v51, 0xffff0000, v150
	v_pk_add_f32 v[50:51], v[78:79], v[50:51]
	v_mov_b32_e32 v66, v1
	v_dot2c_f32_bf16_e32 v82, v53, v53
	v_lshlrev_b32_e32 v52, 16, v151
	v_and_b32_e32 v53, 0xffff0000, v151
	v_cvt_pk_bf16_f32 v50, v50, v51
	v_and_b32_e32 v55, 0xffff0000, v152
	v_dot2c_f32_bf16_e32 v66, v50, v50
	v_lshlrev_b32_e32 v56, 16, v153
	v_and_b32_e32 v57, 0xffff0000, v153
	v_pk_add_f32 v[52:53], v[80:81], v[52:53]
	v_pk_add_f32 v[56:57], v[76:77], v[56:57]
	v_cvt_pk_bf16_f32 v51, v52, v53
	v_pk_add_f32 v[54:55], v[74:75], v[54:55]
	v_dot2c_f32_bf16_e32 v66, v51, v51
	v_cvt_pk_bf16_f32 v52, v54, v55
	v_cvt_pk_bf16_f32 v53, v56, v57
	global_store_dwordx4 v[214:215], v[50:53], off offset:-4096 nt
	v_dot2c_f32_bf16_e32 v66, v52, v52
	v_dot2c_f32_bf16_e32 v66, v53, v53
	v_lshlrev_b32_e32 v50, 16, v146
	v_and_b32_e32 v51, 0xffff0000, v146
	v_pk_add_f32 v[50:51], v[62:63], v[50:51]
	v_lshlrev_b32_e32 v52, 16, v147
	v_and_b32_e32 v53, 0xffff0000, v147
	v_lshlrev_b32_e32 v54, 16, v148
	v_and_b32_e32 v55, 0xffff0000, v148
	v_lshlrev_b32_e32 v56, 16, v149
	v_and_b32_e32 v57, 0xffff0000, v149
	v_cvt_pk_bf16_f32 v50, v50, v51
	v_pk_add_f32 v[52:53], v[64:65], v[52:53]
	v_dot2c_f32_bf16_e32 v66, v50, v50
	v_pk_add_f32 v[56:57], v[60:61], v[56:57]
	v_pk_add_f32 v[54:55], v[58:59], v[54:55]
	v_cvt_pk_bf16_f32 v51, v52, v53
	s_nop 0
	v_dot2c_f32_bf16_e32 v66, v51, v51
	v_cvt_pk_bf16_f32 v52, v54, v55
	v_cvt_pk_bf16_f32 v53, v56, v57
	global_store_dwordx4 v[212:213], v[50:53], off offset:-4096 nt
	v_dot2c_f32_bf16_e32 v66, v52, v52
	v_lshlrev_b32_e32 v54, 16, v144
	v_lshlrev_b32_e32 v50, 16, v142
	v_and_b32_e32 v51, 0xffff0000, v142
	v_and_b32_e32 v55, 0xffff0000, v144
	v_lshlrev_b32_e32 v56, 16, v145
	v_and_b32_e32 v57, 0xffff0000, v145
	v_dot2c_f32_bf16_e32 v66, v53, v53
	v_lshlrev_b32_e32 v52, 16, v143
	v_and_b32_e32 v53, 0xffff0000, v143
	v_pk_add_f32 v[46:47], v[46:47], v[50:51]
	v_pk_add_f32 v[50:51], v[44:45], v[56:57]
	v_pk_add_f32 v[44:45], v[42:43], v[54:55]
	v_pk_add_f32 v[48:49], v[48:49], v[52:53]
	v_cvt_pk_bf16_f32 v42, v46, v47
	v_lshlrev_b32_e32 v46, 16, v140
	v_cvt_pk_bf16_f32 v43, v48, v49
	v_cvt_pk_bf16_f32 v44, v44, v45
	v_cvt_pk_bf16_f32 v45, v50, v51
	v_mov_b32_e32 v50, v1
	v_dot2c_f32_bf16_e32 v50, v42, v42
	v_dot2c_f32_bf16_e32 v50, v43, v43
	v_dot2c_f32_bf16_e32 v50, v44, v44
	global_store_dwordx4 v[218:219], v[42:45], off offset:2048 nt
	v_dot2c_f32_bf16_e32 v50, v45, v45
	v_and_b32_e32 v47, 0xffff0000, v140
	v_lshlrev_b32_e32 v42, 16, v138
	v_and_b32_e32 v43, 0xffff0000, v138
	v_lshlrev_b32_e32 v48, 16, v141
	v_and_b32_e32 v49, 0xffff0000, v141
	v_lshlrev_b32_e32 v44, 16, v139
	v_and_b32_e32 v45, 0xffff0000, v139
	v_pk_add_f32 v[38:39], v[38:39], v[42:43]
	v_pk_add_f32 v[42:43], v[36:37], v[48:49]
	v_pk_add_f32 v[36:37], v[34:35], v[46:47]
	v_cvt_pk_bf16_f32 v34, v38, v39
	v_pk_add_f32 v[40:41], v[40:41], v[44:45]
	v_dot2c_f32_bf16_e32 v50, v34, v34
	v_cvt_pk_bf16_f32 v35, v40, v41
	v_cvt_pk_bf16_f32 v36, v36, v37
	v_cvt_pk_bf16_f32 v37, v42, v43
	global_store_dwordx4 v[216:217], v[34:37], off offset:2048 nt
	v_dot2c_f32_bf16_e32 v50, v35, v35
	v_dot2c_f32_bf16_e32 v50, v36, v36
	v_lshlrev_b32_e32 v34, 16, v134
	v_and_b32_e32 v35, 0xffff0000, v134
	v_lshlrev_b32_e32 v38, 16, v136
	v_and_b32_e32 v39, 0xffff0000, v136
	v_lshlrev_b32_e32 v40, 16, v137
	v_and_b32_e32 v41, 0xffff0000, v137
	v_dot2c_f32_bf16_e32 v50, v37, v37
	v_lshlrev_b32_e32 v36, 16, v135
	v_and_b32_e32 v37, 0xffff0000, v135
	v_pk_add_f32 v[30:31], v[30:31], v[34:35]
	v_pk_add_f32 v[34:35], v[28:29], v[40:41]
	v_pk_add_f32 v[28:29], v[26:27], v[38:39]
	v_pk_add_f32 v[32:33], v[32:33], v[36:37]
	v_cvt_pk_bf16_f32 v26, v30, v31
	v_lshlrev_b32_e32 v30, 16, v132
	v_cvt_pk_bf16_f32 v27, v32, v33
	v_cvt_pk_bf16_f32 v28, v28, v29
	v_cvt_pk_bf16_f32 v29, v34, v35
	v_mov_b32_e32 v34, v1
	v_dot2c_f32_bf16_e32 v34, v26, v26
	v_dot2c_f32_bf16_e32 v34, v27, v27
	v_dot2c_f32_bf16_e32 v34, v28, v28
	global_store_dwordx4 v[214:215], v[26:29], off nt
	v_dot2c_f32_bf16_e32 v34, v29, v29
	v_and_b32_e32 v31, 0xffff0000, v132
	v_lshlrev_b32_e32 v26, 16, v130
	v_and_b32_e32 v27, 0xffff0000, v130
	v_lshlrev_b32_e32 v32, 16, v133
	v_and_b32_e32 v33, 0xffff0000, v133
	v_lshlrev_b32_e32 v28, 16, v131
	v_and_b32_e32 v29, 0xffff0000, v131
	v_pk_add_f32 v[22:23], v[22:23], v[26:27]
	v_pk_add_f32 v[26:27], v[20:21], v[32:33]
	v_pk_add_f32 v[20:21], v[18:19], v[30:31]
	v_cvt_pk_bf16_f32 v18, v22, v23
	v_pk_add_f32 v[24:25], v[24:25], v[28:29]
	v_dot2c_f32_bf16_e32 v34, v18, v18
	v_cvt_pk_bf16_f32 v19, v24, v25
	v_cvt_pk_bf16_f32 v20, v20, v21
	v_cvt_pk_bf16_f32 v21, v26, v27
	global_store_dwordx4 v[212:213], v[18:21], off nt
	v_dot2c_f32_bf16_e32 v34, v19, v19
	v_dot2c_f32_bf16_e32 v34, v20, v20
	v_lshlrev_b32_e32 v18, 16, v126
	v_and_b32_e32 v19, 0xffff0000, v126
	v_lshlrev_b32_e32 v22, 16, v128
	v_and_b32_e32 v23, 0xffff0000, v128
	v_lshlrev_b32_e32 v24, 16, v129
	v_and_b32_e32 v25, 0xffff0000, v129
	v_dot2c_f32_bf16_e32 v34, v21, v21
	v_lshlrev_b32_e32 v20, 16, v127
	v_and_b32_e32 v21, 0xffff0000, v127
	v_pk_add_f32 v[14:15], v[14:15], v[18:19]
	v_pk_add_f32 v[18:19], v[12:13], v[24:25]
	v_pk_add_f32 v[12:13], v[10:11], v[22:23]
	v_pk_add_f32 v[16:17], v[16:17], v[20:21]
	v_cvt_pk_bf16_f32 v10, v14, v15
	v_lshlrev_b32_e32 v14, 16, v116
	v_cvt_pk_bf16_f32 v11, v16, v17
	v_cvt_pk_bf16_f32 v12, v12, v13
	v_cvt_pk_bf16_f32 v13, v18, v19
	v_mov_b32_e32 v18, v1
	v_dot2c_f32_bf16_e32 v18, v10, v10
	v_dot2c_f32_bf16_e32 v18, v11, v11
	v_dot2c_f32_bf16_e32 v18, v12, v12
	global_store_dwordx4 v[214:215], v[10:13], off offset:2048 nt
	v_dot2c_f32_bf16_e32 v18, v13, v13
	v_and_b32_e32 v15, 0xffff0000, v116
	v_lshlrev_b32_e32 v10, 16, v114
	v_and_b32_e32 v11, 0xffff0000, v114
	v_lshlrev_b32_e32 v16, 16, v117
	v_and_b32_e32 v17, 0xffff0000, v117
	v_lshlrev_b32_e32 v12, 16, v115
	v_and_b32_e32 v13, 0xffff0000, v115
	v_pk_add_f32 v[6:7], v[6:7], v[10:11]
	v_pk_add_f32 v[10:11], v[4:5], v[16:17]
	v_pk_add_f32 v[4:5], v[2:3], v[14:15]
	v_cvt_pk_bf16_f32 v2, v6, v7
	v_pk_add_f32 v[8:9], v[8:9], v[12:13]
	v_dot2c_f32_bf16_e32 v18, v2, v2
	v_cvt_pk_bf16_f32 v3, v8, v9
	v_cvt_pk_bf16_f32 v4, v4, v5
	v_cvt_pk_bf16_f32 v5, v10, v11
	global_store_dwordx4 v[212:213], v[2:5], off offset:2048 nt
	v_dot2c_f32_bf16_e32 v18, v3, v3
	v_dot2c_f32_bf16_e32 v18, v4, v4
	v_dot2c_f32_bf16_e32 v18, v5, v5
	ds_bpermute_b32 v2, v241, v162
	ds_bpermute_b32 v3, v241, v106
	ds_bpermute_b32 v4, v241, v90
	ds_bpermute_b32 v5, v241, v82
	ds_bpermute_b32 v6, v241, v66
	ds_bpermute_b32 v7, v241, v50
	ds_bpermute_b32 v8, v241, v34
	ds_bpermute_b32 v9, v241, v18
	s_waitcnt lgkmcnt(7)
	v_add_f32_e32 v2, v162, v2
	s_waitcnt lgkmcnt(6)
	v_add_f32_e32 v3, v106, v3
	s_waitcnt lgkmcnt(5)
	v_add_f32_e32 v4, v90, v4
	s_waitcnt lgkmcnt(4)
	v_add_f32_e32 v5, v82, v5
	s_waitcnt lgkmcnt(3)
	v_add_f32_e32 v6, v66, v6
	s_waitcnt lgkmcnt(2)
	v_add_f32_e32 v7, v50, v7
	s_waitcnt lgkmcnt(1)
	v_add_f32_e32 v8, v34, v8
	s_waitcnt lgkmcnt(0)
	v_add_f32_e32 v11, v18, v9
	v_bitop3_b32 v17, v239, s11, v240 bitop3:0x36
	ds_bpermute_b32 v9, v17, v2
	ds_bpermute_b32 v10, v17, v3
	ds_bpermute_b32 v12, v17, v4
	ds_bpermute_b32 v13, v17, v5
	ds_bpermute_b32 v14, v17, v6
	ds_bpermute_b32 v15, v17, v7
	ds_bpermute_b32 v16, v17, v8
	ds_bpermute_b32 v17, v17, v11
	s_and_saveexec_b64 s[26:27], vcc
	s_cbranch_execz .LBB0_1061
	s_lshl_b32 s11, s69, 8
	s_add_i32 s11, s11, s61
	s_waitcnt lgkmcnt(5)
	v_add_f32_e32 v12, v4, v12
	v_add_f32_e32 v4, v2, v9
	v_or_b32_e32 v2, s11, v211
	s_mov_b32 s11, 0x49800000
	v_fma_f32 v4, v4, s11, 0.5
	v_trunc_f32_e32 v4, v4
	s_waitcnt lgkmcnt(4)
	v_add_f32_e32 v13, v5, v13
	v_mul_f32_e32 v5, 0x2f800000, v4
	v_floor_f32_e32 v5, v5
	v_fmac_f32_e32 v4, 0xcf800000, v5
	v_cvt_u32_f32_e32 v4, v4
	v_cvt_u32_f32_e32 v5, v5
	v_add_f32_e32 v10, v3, v10
	v_ashrrev_i32_e32 v3, 31, v2
	v_lshl_add_u64 v[2:3], v[2:3], 3, s[46:47]
	global_atomic_add_x2 v[2:3], v[4:5], off
	v_fma_f32 v4, v10, s11, 0.5
	v_trunc_f32_e32 v4, v4
	v_mul_f32_e32 v5, 0x2f800000, v4
	v_floor_f32_e32 v5, v5
	v_fmac_f32_e32 v4, 0xcf800000, v5
	v_cvt_u32_f32_e32 v4, v4
	v_cvt_u32_f32_e32 v5, v5
	s_waitcnt lgkmcnt(3)
	v_add_f32_e32 v6, v6, v14
	s_waitcnt lgkmcnt(2)
	v_add_f32_e32 v7, v7, v15
	s_waitcnt lgkmcnt(1)
	v_add_f32_e32 v8, v8, v16
	global_atomic_add_x2 v[2:3], v[4:5], off offset:128
	v_fma_f32 v4, v12, s11, 0.5
	v_trunc_f32_e32 v4, v4
	v_mul_f32_e32 v5, 0x2f800000, v4
	v_floor_f32_e32 v5, v5
	v_fmac_f32_e32 v4, 0xcf800000, v5
	v_cvt_u32_f32_e32 v4, v4
	v_cvt_u32_f32_e32 v5, v5
	s_waitcnt lgkmcnt(0)
	v_add_f32_e32 v11, v11, v17
	global_atomic_add_x2 v[2:3], v[4:5], off offset:256
	v_fma_f32 v4, v13, s11, 0.5
	v_trunc_f32_e32 v4, v4
	v_mul_f32_e32 v5, 0x2f800000, v4
	v_floor_f32_e32 v5, v5
	v_fmac_f32_e32 v4, 0xcf800000, v5
	v_cvt_u32_f32_e32 v4, v4
	v_cvt_u32_f32_e32 v5, v5
	global_atomic_add_x2 v[2:3], v[4:5], off offset:384
	v_fma_f32 v4, v6, s11, 0.5
	v_trunc_f32_e32 v4, v4
	v_mul_f32_e32 v5, 0x2f800000, v4
	v_floor_f32_e32 v5, v5
	v_fmac_f32_e32 v4, 0xcf800000, v5
	v_cvt_u32_f32_e32 v4, v4
	v_cvt_u32_f32_e32 v5, v5
	global_atomic_add_x2 v[2:3], v[4:5], off offset:1024
	v_fma_f32 v4, v7, s11, 0.5
	v_trunc_f32_e32 v4, v4
	v_mul_f32_e32 v5, 0x2f800000, v4
	v_floor_f32_e32 v5, v5
	v_fmac_f32_e32 v4, 0xcf800000, v5
	v_cvt_u32_f32_e32 v4, v4
	v_cvt_u32_f32_e32 v5, v5
	global_atomic_add_x2 v[2:3], v[4:5], off offset:1152
	v_fma_f32 v4, v8, s11, 0.5
	v_trunc_f32_e32 v4, v4
	v_mul_f32_e32 v5, 0x2f800000, v4
	v_floor_f32_e32 v5, v5
	v_fmac_f32_e32 v4, 0xcf800000, v5
	v_cvt_u32_f32_e32 v4, v4
	v_cvt_u32_f32_e32 v5, v5
	global_atomic_add_x2 v[2:3], v[4:5], off offset:1280
	v_fma_f32 v4, v11, s11, 0.5
	v_trunc_f32_e32 v4, v4
	v_mul_f32_e32 v5, 0x2f800000, v4
	v_floor_f32_e32 v5, v5
	v_fmac_f32_e32 v4, 0xcf800000, v5
	v_cvt_u32_f32_e32 v4, v4
	v_cvt_u32_f32_e32 v5, v5
	global_atomic_add_x2 v[2:3], v[4:5], off offset:1408
	s_branch .LBB0_1061

.LBB0_1228:
	s_lshl_b32 s26, s11, 5
	s_lshl_b32 s21, s21, 2
	s_add_i32 s26, s26, s21
	s_or_b32 s26, s26, s60
	s_ashr_i32 s27, s26, 31
	s_lshl_b64 s[26:27], s[26:27], 8
	v_mbcnt_lo_u32_b32 v238, -1, 0
	v_mbcnt_hi_u32_b32 v238, -1, v238
	s_add_u32 s21, s26, s57
	v_ashrrev_i32_e32 v123, 4, v238
	v_and_b32_e32 v122, 15, v238
	s_addc_u32 s26, s27, s61
	v_lshlrev_b32_e32 v116, 3, v123
	v_or_b32_e32 v114, s21, v122
	v_mov_b32_e32 v115, s26
	v_ashrrev_i32_e32 v117, 31, v116
	v_lshl_add_u64 v[116:117], v[116:117], 1, s[50:51]
	v_lshlrev_b64 v[114:115], 7, v[114:115]
	v_lshl_add_u64 v[224:225], v[116:117], 0, v[114:115]
	global_load_dwordx4 v[194:197], v[224:225], off
	s_mov_b32 s21, 0x10000
	v_add_co_u32_e32 v222, vcc, s21, v224
	s_mov_b32 s21, 0x11000
	s_nop 0
	v_addc_co_u32_e32 v223, vcc, 0, v225, vcc
	v_add_co_u32_e32 v218, vcc, s21, v224
	s_movk_i32 s21, 0x4000
	s_nop 0
	v_addc_co_u32_e32 v219, vcc, 0, v225, vcc
	global_load_dwordx4 v[186:189], v[218:219], off offset:-4096
	global_load_dwordx4 v[182:185], v[224:225], off offset:2048
	global_load_dwordx4 v[178:181], v[222:223], off offset:2048
	v_add_co_u32_e32 v220, vcc, s94, v224
	v_lshlrev_b32_e32 v239, 6, v123
	s_nop 0
	v_addc_co_u32_e32 v221, vcc, 0, v225, vcc
	global_load_dwordx4 v[174:177], v[220:221], off
	global_load_dwordx4 v[162:165], v[218:219], off
	global_load_dwordx4 v[158:161], v[220:221], off offset:2048
	global_load_dwordx4 v[154:157], v[218:219], off offset:2048
	v_add_co_u32_e32 v216, vcc, s21, v224
	s_movk_i32 s21, 0x5000
	s_nop 0
	v_addc_co_u32_e32 v217, vcc, 0, v225, vcc
	v_add_co_u32_e32 v212, vcc, s21, v224
	s_mov_b32 s21, 0x14000
	s_nop 0
	v_addc_co_u32_e32 v213, vcc, 0, v225, vcc
	global_load_dwordx4 v[150:153], v[212:213], off offset:-4096
	v_add_co_u32_e32 v214, vcc, s21, v224
	s_mov_b32 s21, 0x15000
	s_nop 0
	v_addc_co_u32_e32 v215, vcc, 0, v225, vcc
	v_add_co_u32_e32 v210, vcc, s21, v224
	v_lshlrev_b32_e32 v240, 2, v122
	s_nop 0
	v_addc_co_u32_e32 v211, vcc, 0, v225, vcc
	global_load_dwordx4 v[146:149], v[210:211], off offset:-4096
	global_load_dwordx4 v[142:145], v[216:217], off offset:2048
	global_load_dwordx4 v[138:141], v[214:215], off offset:2048
	global_load_dwordx4 v[134:137], v[212:213], off
	global_load_dwordx4 v[130:133], v[210:211], off
	global_load_dwordx4 v[122:125], v[212:213], off offset:2048
	global_load_dwordx4 v[114:117], v[210:211], off offset:2048
	v_bitop3_b32 v241, v239, 64, v240 bitop3:0x36
	s_movk_i32 s21, 0x80
	v_cmp_gt_u32_e32 vcc, 16, v238
	s_waitcnt vmcnt(0)
	v_lshlrev_b32_e32 v190, 16, v194
	v_and_b32_e32 v191, 0xffff0000, v194
	v_lshlrev_b32_e32 v194, 16, v195
	v_and_b32_e32 v195, 0xffff0000, v195
	v_pk_fma_f32 v[166:167], v[166:167], 0.5, v[190:191] op_sel_hi:[1,0,1]
	v_pk_fma_f32 v[194:195], v[168:169], 0.5, v[194:195] op_sel_hi:[1,0,1]
	v_cvt_pk_bf16_f32 v168, v166, v167
	v_mov_b32_e32 v166, v1
	v_lshlrev_b32_e32 v198, 16, v196
	v_and_b32_e32 v199, 0xffff0000, v196
	v_dot2c_f32_bf16_e32 v166, v168, v168
	v_lshlrev_b32_e32 v196, 16, v197
	v_and_b32_e32 v197, 0xffff0000, v197
	v_pk_fma_f32 v[170:171], v[170:171], 0.5, v[198:199] op_sel_hi:[1,0,1]
	v_cvt_pk_bf16_f32 v169, v194, v195
	v_pk_fma_f32 v[172:173], v[172:173], 0.5, v[196:197] op_sel_hi:[1,0,1]
	v_dot2c_f32_bf16_e32 v166, v169, v169
	v_cvt_pk_bf16_f32 v170, v170, v171
	v_cvt_pk_bf16_f32 v171, v172, v173
	global_store_dwordx4 v[224:225], v[168:171], off nt
	v_dot2c_f32_bf16_e32 v166, v170, v170
	v_dot2c_f32_bf16_e32 v166, v171, v171
	v_lshlrev_b32_e32 v168, 16, v186
	v_and_b32_e32 v169, 0xffff0000, v186
	v_lshlrev_b32_e32 v170, 16, v187
	v_and_b32_e32 v171, 0xffff0000, v187
	v_lshlrev_b32_e32 v172, 16, v188
	v_and_b32_e32 v173, 0xffff0000, v188
	v_lshlrev_b32_e32 v186, 16, v189
	v_and_b32_e32 v187, 0xffff0000, v189
	v_pk_fma_f32 v[126:127], v[126:127], 0.5, v[168:169] op_sel_hi:[1,0,1]
	v_pk_fma_f32 v[168:169], v[120:121], 0.5, v[186:187] op_sel_hi:[1,0,1]
	v_pk_fma_f32 v[120:121], v[118:119], 0.5, v[172:173] op_sel_hi:[1,0,1]
	v_cvt_pk_bf16_f32 v118, v126, v127
	v_pk_fma_f32 v[128:129], v[128:129], 0.5, v[170:171] op_sel_hi:[1,0,1]
	v_dot2c_f32_bf16_e32 v166, v118, v118
	v_cvt_pk_bf16_f32 v119, v128, v129
	v_cvt_pk_bf16_f32 v120, v120, v121
	v_cvt_pk_bf16_f32 v121, v168, v169
	global_store_dwordx4 v[218:219], v[118:121], off offset:-4096 nt
	v_dot2c_f32_bf16_e32 v166, v119, v119
	v_dot2c_f32_bf16_e32 v166, v120, v120
	v_lshlrev_b32_e32 v118, 16, v182
	v_and_b32_e32 v119, 0xffff0000, v182
	v_lshlrev_b32_e32 v126, 16, v184
	v_and_b32_e32 v127, 0xffff0000, v184
	v_dot2c_f32_bf16_e32 v166, v121, v121
	v_lshlrev_b32_e32 v120, 16, v183
	v_and_b32_e32 v121, 0xffff0000, v183
	v_lshlrev_b32_e32 v128, 16, v185
	v_and_b32_e32 v129, 0xffff0000, v185
	v_pk_fma_f32 v[110:111], v[110:111], 0.5, v[118:119] op_sel_hi:[1,0,1]
	v_pk_fma_f32 v[106:107], v[106:107], 0.5, v[126:127] op_sel_hi:[1,0,1]
	v_pk_fma_f32 v[112:113], v[112:113], 0.5, v[120:121] op_sel_hi:[1,0,1]
	v_pk_fma_f32 v[118:119], v[108:109], 0.5, v[128:129] op_sel_hi:[1,0,1]
	v_cvt_pk_bf16_f32 v108, v110, v111
	v_cvt_pk_bf16_f32 v109, v112, v113
	v_cvt_pk_bf16_f32 v110, v106, v107
	v_mov_b32_e32 v106, v1
	v_dot2c_f32_bf16_e32 v106, v108, v108
	v_dot2c_f32_bf16_e32 v106, v109, v109
	v_dot2c_f32_bf16_e32 v106, v110, v110
	v_cvt_pk_bf16_f32 v111, v118, v119
	global_store_dwordx4 v[224:225], v[108:111], off offset:2048 nt
	v_dot2c_f32_bf16_e32 v106, v111, v111
	v_lshlrev_b32_e32 v112, 16, v180
	v_lshlrev_b32_e32 v108, 16, v178
	v_and_b32_e32 v109, 0xffff0000, v178
	v_and_b32_e32 v113, 0xffff0000, v180
	v_lshlrev_b32_e32 v118, 16, v181
	v_and_b32_e32 v119, 0xffff0000, v181
	v_lshlrev_b32_e32 v110, 16, v179
	v_and_b32_e32 v111, 0xffff0000, v179
	v_pk_fma_f32 v[102:103], v[102:103], 0.5, v[108:109] op_sel_hi:[1,0,1]
	v_pk_fma_f32 v[108:109], v[100:101], 0.5, v[118:119] op_sel_hi:[1,0,1]
	v_pk_fma_f32 v[100:101], v[98:99], 0.5, v[112:113] op_sel_hi:[1,0,1]
	v_cvt_pk_bf16_f32 v98, v102, v103
	v_pk_fma_f32 v[104:105], v[104:105], 0.5, v[110:111] op_sel_hi:[1,0,1]
	v_dot2c_f32_bf16_e32 v106, v98, v98
	v_cvt_pk_bf16_f32 v99, v104, v105
	v_cvt_pk_bf16_f32 v100, v100, v101
	v_cvt_pk_bf16_f32 v101, v108, v109
	global_store_dwordx4 v[222:223], v[98:101], off offset:2048 nt
	v_dot2c_f32_bf16_e32 v106, v99, v99
	v_dot2c_f32_bf16_e32 v106, v100, v100
	v_lshlrev_b32_e32 v98, 16, v174
	v_and_b32_e32 v99, 0xffff0000, v174
	v_lshlrev_b32_e32 v102, 16, v176
	v_and_b32_e32 v103, 0xffff0000, v176
	v_dot2c_f32_bf16_e32 v106, v101, v101
	v_lshlrev_b32_e32 v100, 16, v175
	v_and_b32_e32 v101, 0xffff0000, v175
	v_lshlrev_b32_e32 v104, 16, v177
	v_and_b32_e32 v105, 0xffff0000, v177
	v_pk_fma_f32 v[94:95], v[94:95], 0.5, v[98:99] op_sel_hi:[1,0,1]
	v_pk_fma_f32 v[90:91], v[90:91], 0.5, v[102:103] op_sel_hi:[1,0,1]
	v_pk_fma_f32 v[96:97], v[96:97], 0.5, v[100:101] op_sel_hi:[1,0,1]
	v_pk_fma_f32 v[98:99], v[92:93], 0.5, v[104:105] op_sel_hi:[1,0,1]
	v_cvt_pk_bf16_f32 v92, v94, v95
	v_cvt_pk_bf16_f32 v93, v96, v97
	v_cvt_pk_bf16_f32 v94, v90, v91
	v_mov_b32_e32 v90, v1
	v_dot2c_f32_bf16_e32 v90, v92, v92
	v_dot2c_f32_bf16_e32 v90, v93, v93
	v_dot2c_f32_bf16_e32 v90, v94, v94
	v_cvt_pk_bf16_f32 v95, v98, v99
	global_store_dwordx4 v[220:221], v[92:95], off nt
	v_dot2c_f32_bf16_e32 v90, v95, v95
	v_lshlrev_b32_e32 v96, 16, v164
	v_lshlrev_b32_e32 v92, 16, v162
	v_and_b32_e32 v93, 0xffff0000, v162
	v_and_b32_e32 v97, 0xffff0000, v164
	v_lshlrev_b32_e32 v98, 16, v165
	v_and_b32_e32 v99, 0xffff0000, v165
	v_lshlrev_b32_e32 v94, 16, v163
	v_and_b32_e32 v95, 0xffff0000, v163
	v_pk_fma_f32 v[86:87], v[86:87], 0.5, v[92:93] op_sel_hi:[1,0,1]
	v_pk_fma_f32 v[92:93], v[84:85], 0.5, v[98:99] op_sel_hi:[1,0,1]
	v_pk_fma_f32 v[84:85], v[82:83], 0.5, v[96:97] op_sel_hi:[1,0,1]
	v_cvt_pk_bf16_f32 v82, v86, v87
	v_pk_fma_f32 v[88:89], v[88:89], 0.5, v[94:95] op_sel_hi:[1,0,1]
	v_dot2c_f32_bf16_e32 v90, v82, v82
	v_cvt_pk_bf16_f32 v83, v88, v89
	v_cvt_pk_bf16_f32 v84, v84, v85
	v_cvt_pk_bf16_f32 v85, v92, v93
	global_store_dwordx4 v[218:219], v[82:85], off nt
	v_dot2c_f32_bf16_e32 v90, v83, v83
	v_dot2c_f32_bf16_e32 v90, v84, v84
	v_lshlrev_b32_e32 v82, 16, v158
	v_and_b32_e32 v83, 0xffff0000, v158
	v_lshlrev_b32_e32 v86, 16, v160
	v_and_b32_e32 v87, 0xffff0000, v160
	v_lshlrev_b32_e32 v88, 16, v161
	v_and_b32_e32 v89, 0xffff0000, v161
	v_dot2c_f32_bf16_e32 v90, v85, v85
	v_lshlrev_b32_e32 v84, 16, v159
	v_and_b32_e32 v85, 0xffff0000, v159
	v_pk_fma_f32 v[78:79], v[78:79], 0.5, v[82:83] op_sel_hi:[1,0,1]
	v_pk_fma_f32 v[82:83], v[72:73], 0.5, v[88:89] op_sel_hi:[1,0,1]
	v_pk_fma_f32 v[72:73], v[70:71], 0.5, v[86:87] op_sel_hi:[1,0,1]
	v_pk_fma_f32 v[80:81], v[80:81], 0.5, v[84:85] op_sel_hi:[1,0,1]
	v_cvt_pk_bf16_f32 v70, v78, v79
	v_lshlrev_b32_e32 v78, 16, v156
	v_cvt_pk_bf16_f32 v71, v80, v81
	v_cvt_pk_bf16_f32 v72, v72, v73
	v_cvt_pk_bf16_f32 v73, v82, v83
	v_mov_b32_e32 v82, v1
	v_dot2c_f32_bf16_e32 v82, v70, v70
	v_dot2c_f32_bf16_e32 v82, v71, v71
	v_dot2c_f32_bf16_e32 v82, v72, v72
	global_store_dwordx4 v[220:221], v[70:73], off offset:2048 nt
	v_dot2c_f32_bf16_e32 v82, v73, v73
	v_and_b32_e32 v79, 0xffff0000, v156
	v_lshlrev_b32_e32 v70, 16, v154
	v_and_b32_e32 v71, 0xffff0000, v154
	v_lshlrev_b32_e32 v72, 16, v155
	v_and_b32_e32 v73, 0xffff0000, v155
	v_lshlrev_b32_e32 v80, 16, v157
	v_and_b32_e32 v81, 0xffff0000, v157
	v_pk_fma_f32 v[64:65], v[64:65], 0.5, v[72:73] op_sel_hi:[1,0,1]
	v_pk_fma_f32 v[62:63], v[62:63], 0.5, v[70:71] op_sel_hi:[1,0,1]
	v_pk_fma_f32 v[70:71], v[56:57], 0.5, v[80:81] op_sel_hi:[1,0,1]
	v_pk_fma_f32 v[56:57], v[54:55], 0.5, v[78:79] op_sel_hi:[1,0,1]
	v_cvt_pk_bf16_f32 v54, v62, v63
	v_cvt_pk_bf16_f32 v55, v64, v65
	v_lshlrev_b32_e32 v62, 16, v152
	v_dot2c_f32_bf16_e32 v82, v54, v54
	v_cvt_pk_bf16_f32 v56, v56, v57
	v_cvt_pk_bf16_f32 v57, v70, v71
	global_store_dwordx4 v[218:219], v[54:57], off offset:2048 nt
	v_dot2c_f32_bf16_e32 v82, v55, v55
	v_and_b32_e32 v63, 0xffff0000, v152
	v_lshlrev_b32_e32 v54, 16, v150
	v_and_b32_e32 v55, 0xffff0000, v150
	v_dot2c_f32_bf16_e32 v82, v56, v56
	v_pk_fma_f32 v[54:55], v[74:75], 0.5, v[54:55] op_sel_hi:[1,0,1]
	v_pk_fma_f32 v[62:63], v[66:67], 0.5, v[62:63] op_sel_hi:[1,0,1]
	v_mov_b32_e32 v66, v1
	v_dot2c_f32_bf16_e32 v82, v57, v57
	v_lshlrev_b32_e32 v56, 16, v151
	v_and_b32_e32 v57, 0xffff0000, v151
	v_cvt_pk_bf16_f32 v54, v54, v55
	v_lshlrev_b32_e32 v64, 16, v153
	v_dot2c_f32_bf16_e32 v66, v54, v54
	v_and_b32_e32 v65, 0xffff0000, v153
	v_pk_fma_f32 v[56:57], v[76:77], 0.5, v[56:57] op_sel_hi:[1,0,1]
	v_pk_fma_f32 v[64:65], v[68:69], 0.5, v[64:65] op_sel_hi:[1,0,1]
	v_cvt_pk_bf16_f32 v55, v56, v57
	v_cvt_pk_bf16_f32 v56, v62, v63
	v_lshlrev_b32_e32 v62, 16, v148
	v_dot2c_f32_bf16_e32 v66, v55, v55
	v_dot2c_f32_bf16_e32 v66, v56, v56
	v_cvt_pk_bf16_f32 v57, v64, v65
	global_store_dwordx4 v[212:213], v[54:57], off offset:-4096 nt
	v_dot2c_f32_bf16_e32 v66, v57, v57
	v_and_b32_e32 v63, 0xffff0000, v148
	v_lshlrev_b32_e32 v54, 16, v146
	v_and_b32_e32 v55, 0xffff0000, v146
	v_lshlrev_b32_e32 v64, 16, v149
	v_and_b32_e32 v65, 0xffff0000, v149
	v_lshlrev_b32_e32 v56, 16, v147
	v_and_b32_e32 v57, 0xffff0000, v147
	v_pk_fma_f32 v[54:55], v[58:59], 0.5, v[54:55] op_sel_hi:[1,0,1]
	v_pk_fma_f32 v[58:59], v[52:53], 0.5, v[64:65] op_sel_hi:[1,0,1]
	v_pk_fma_f32 v[52:53], v[50:51], 0.5, v[62:63] op_sel_hi:[1,0,1]
	v_cvt_pk_bf16_f32 v50, v54, v55
	v_pk_fma_f32 v[56:57], v[60:61], 0.5, v[56:57] op_sel_hi:[1,0,1]
	v_dot2c_f32_bf16_e32 v66, v50, v50
	v_cvt_pk_bf16_f32 v51, v56, v57
	v_cvt_pk_bf16_f32 v52, v52, v53
	v_cvt_pk_bf16_f32 v53, v58, v59
	global_store_dwordx4 v[210:211], v[50:53], off offset:-4096 nt
	v_dot2c_f32_bf16_e32 v66, v51, v51
	v_dot2c_f32_bf16_e32 v66, v52, v52
	v_lshlrev_b32_e32 v50, 16, v142
	v_and_b32_e32 v51, 0xffff0000, v142
	v_lshlrev_b32_e32 v54, 16, v144
	v_and_b32_e32 v55, 0xffff0000, v144
	v_lshlrev_b32_e32 v56, 16, v145
	v_and_b32_e32 v57, 0xffff0000, v145
	v_dot2c_f32_bf16_e32 v66, v53, v53
	v_lshlrev_b32_e32 v52, 16, v143
	v_and_b32_e32 v53, 0xffff0000, v143
	v_pk_fma_f32 v[46:47], v[46:47], 0.5, v[50:51] op_sel_hi:[1,0,1]
	v_pk_fma_f32 v[50:51], v[44:45], 0.5, v[56:57] op_sel_hi:[1,0,1]
	v_pk_fma_f32 v[44:45], v[42:43], 0.5, v[54:55] op_sel_hi:[1,0,1]
	v_pk_fma_f32 v[48:49], v[48:49], 0.5, v[52:53] op_sel_hi:[1,0,1]
	v_cvt_pk_bf16_f32 v42, v46, v47
	v_lshlrev_b32_e32 v46, 16, v140
	v_cvt_pk_bf16_f32 v43, v48, v49
	v_cvt_pk_bf16_f32 v44, v44, v45
	v_cvt_pk_bf16_f32 v45, v50, v51
	v_mov_b32_e32 v50, v1
	v_dot2c_f32_bf16_e32 v50, v42, v42
	v_dot2c_f32_bf16_e32 v50, v43, v43
	v_dot2c_f32_bf16_e32 v50, v44, v44
	global_store_dwordx4 v[216:217], v[42:45], off offset:2048 nt
	v_dot2c_f32_bf16_e32 v50, v45, v45
	v_and_b32_e32 v47, 0xffff0000, v140
	v_lshlrev_b32_e32 v42, 16, v138
	v_and_b32_e32 v43, 0xffff0000, v138
	v_lshlrev_b32_e32 v48, 16, v141
	v_and_b32_e32 v49, 0xffff0000, v141
	v_lshlrev_b32_e32 v44, 16, v139
	v_and_b32_e32 v45, 0xffff0000, v139
	v_pk_fma_f32 v[38:39], v[38:39], 0.5, v[42:43] op_sel_hi:[1,0,1]
	v_pk_fma_f32 v[42:43], v[36:37], 0.5, v[48:49] op_sel_hi:[1,0,1]
	v_pk_fma_f32 v[36:37], v[34:35], 0.5, v[46:47] op_sel_hi:[1,0,1]
	v_cvt_pk_bf16_f32 v34, v38, v39
	v_pk_fma_f32 v[40:41], v[40:41], 0.5, v[44:45] op_sel_hi:[1,0,1]
	v_dot2c_f32_bf16_e32 v50, v34, v34
	v_cvt_pk_bf16_f32 v35, v40, v41
	v_cvt_pk_bf16_f32 v36, v36, v37
	v_cvt_pk_bf16_f32 v37, v42, v43
	global_store_dwordx4 v[214:215], v[34:37], off offset:2048 nt
	v_dot2c_f32_bf16_e32 v50, v35, v35
	v_dot2c_f32_bf16_e32 v50, v36, v36
	v_lshlrev_b32_e32 v34, 16, v134
	v_and_b32_e32 v35, 0xffff0000, v134
	v_lshlrev_b32_e32 v38, 16, v136
	v_and_b32_e32 v39, 0xffff0000, v136
	v_lshlrev_b32_e32 v40, 16, v137
	v_and_b32_e32 v41, 0xffff0000, v137
	v_dot2c_f32_bf16_e32 v50, v37, v37
	v_lshlrev_b32_e32 v36, 16, v135
	v_and_b32_e32 v37, 0xffff0000, v135
	v_pk_fma_f32 v[30:31], v[30:31], 0.5, v[34:35] op_sel_hi:[1,0,1]
	v_pk_fma_f32 v[34:35], v[28:29], 0.5, v[40:41] op_sel_hi:[1,0,1]
	v_pk_fma_f32 v[28:29], v[26:27], 0.5, v[38:39] op_sel_hi:[1,0,1]
	v_pk_fma_f32 v[32:33], v[32:33], 0.5, v[36:37] op_sel_hi:[1,0,1]
	v_cvt_pk_bf16_f32 v26, v30, v31
	v_lshlrev_b32_e32 v30, 16, v132
	v_cvt_pk_bf16_f32 v27, v32, v33
	v_cvt_pk_bf16_f32 v28, v28, v29
	v_cvt_pk_bf16_f32 v29, v34, v35
	v_mov_b32_e32 v34, v1
	v_dot2c_f32_bf16_e32 v34, v26, v26
	v_dot2c_f32_bf16_e32 v34, v27, v27
	v_dot2c_f32_bf16_e32 v34, v28, v28
	global_store_dwordx4 v[212:213], v[26:29], off nt
	v_dot2c_f32_bf16_e32 v34, v29, v29
	v_and_b32_e32 v31, 0xffff0000, v132
	v_lshlrev_b32_e32 v26, 16, v130
	v_and_b32_e32 v27, 0xffff0000, v130
	v_lshlrev_b32_e32 v32, 16, v133
	v_and_b32_e32 v33, 0xffff0000, v133
	v_lshlrev_b32_e32 v28, 16, v131
	v_and_b32_e32 v29, 0xffff0000, v131
	v_pk_fma_f32 v[22:23], v[22:23], 0.5, v[26:27] op_sel_hi:[1,0,1]
	v_pk_fma_f32 v[26:27], v[20:21], 0.5, v[32:33] op_sel_hi:[1,0,1]
	v_pk_fma_f32 v[20:21], v[18:19], 0.5, v[30:31] op_sel_hi:[1,0,1]
	v_cvt_pk_bf16_f32 v18, v22, v23
	v_pk_fma_f32 v[24:25], v[24:25], 0.5, v[28:29] op_sel_hi:[1,0,1]
	v_dot2c_f32_bf16_e32 v34, v18, v18
	v_cvt_pk_bf16_f32 v19, v24, v25
	v_cvt_pk_bf16_f32 v20, v20, v21
	v_cvt_pk_bf16_f32 v21, v26, v27
	global_store_dwordx4 v[210:211], v[18:21], off nt
	v_dot2c_f32_bf16_e32 v34, v19, v19
	v_dot2c_f32_bf16_e32 v34, v20, v20
	v_lshlrev_b32_e32 v18, 16, v122
	v_and_b32_e32 v19, 0xffff0000, v122
	v_lshlrev_b32_e32 v22, 16, v124
	v_and_b32_e32 v23, 0xffff0000, v124
	v_lshlrev_b32_e32 v24, 16, v125
	v_and_b32_e32 v25, 0xffff0000, v125
	v_dot2c_f32_bf16_e32 v34, v21, v21
	v_lshlrev_b32_e32 v20, 16, v123
	v_and_b32_e32 v21, 0xffff0000, v123
	v_pk_fma_f32 v[14:15], v[14:15], 0.5, v[18:19] op_sel_hi:[1,0,1]
	v_pk_fma_f32 v[18:19], v[12:13], 0.5, v[24:25] op_sel_hi:[1,0,1]
	v_pk_fma_f32 v[12:13], v[10:11], 0.5, v[22:23] op_sel_hi:[1,0,1]
	v_pk_fma_f32 v[16:17], v[16:17], 0.5, v[20:21] op_sel_hi:[1,0,1]
	v_cvt_pk_bf16_f32 v10, v14, v15
	v_lshlrev_b32_e32 v14, 16, v116
	v_cvt_pk_bf16_f32 v11, v16, v17
	v_cvt_pk_bf16_f32 v12, v12, v13
	v_cvt_pk_bf16_f32 v13, v18, v19
	v_mov_b32_e32 v18, v1
	v_dot2c_f32_bf16_e32 v18, v10, v10
	v_dot2c_f32_bf16_e32 v18, v11, v11
	v_dot2c_f32_bf16_e32 v18, v12, v12
	global_store_dwordx4 v[212:213], v[10:13], off offset:2048 nt
	v_dot2c_f32_bf16_e32 v18, v13, v13
	v_and_b32_e32 v15, 0xffff0000, v116
	v_lshlrev_b32_e32 v10, 16, v114
	v_and_b32_e32 v11, 0xffff0000, v114
	v_lshlrev_b32_e32 v16, 16, v117
	v_and_b32_e32 v17, 0xffff0000, v117
	v_lshlrev_b32_e32 v12, 16, v115
	v_and_b32_e32 v13, 0xffff0000, v115
	v_pk_fma_f32 v[6:7], v[6:7], 0.5, v[10:11] op_sel_hi:[1,0,1]
	v_pk_fma_f32 v[10:11], v[4:5], 0.5, v[16:17] op_sel_hi:[1,0,1]
	v_pk_fma_f32 v[4:5], v[2:3], 0.5, v[14:15] op_sel_hi:[1,0,1]
	v_cvt_pk_bf16_f32 v2, v6, v7
	v_pk_fma_f32 v[8:9], v[8:9], 0.5, v[12:13] op_sel_hi:[1,0,1]
	v_dot2c_f32_bf16_e32 v18, v2, v2
	v_cvt_pk_bf16_f32 v3, v8, v9
	v_cvt_pk_bf16_f32 v4, v4, v5
	v_cvt_pk_bf16_f32 v5, v10, v11
	global_store_dwordx4 v[210:211], v[2:5], off offset:2048 nt
	v_dot2c_f32_bf16_e32 v18, v3, v3
	v_dot2c_f32_bf16_e32 v18, v4, v4
	v_dot2c_f32_bf16_e32 v18, v5, v5
	ds_bpermute_b32 v2, v241, v166
	ds_bpermute_b32 v3, v241, v106
	ds_bpermute_b32 v4, v241, v90
	ds_bpermute_b32 v5, v241, v82
	ds_bpermute_b32 v6, v241, v66
	ds_bpermute_b32 v7, v241, v50
	ds_bpermute_b32 v8, v241, v34
	ds_bpermute_b32 v9, v241, v18
	s_waitcnt lgkmcnt(7)
	v_add_f32_e32 v2, v166, v2
	s_waitcnt lgkmcnt(6)
	v_add_f32_e32 v3, v106, v3
	s_waitcnt lgkmcnt(5)
	v_add_f32_e32 v4, v90, v4
	s_waitcnt lgkmcnt(4)
	v_add_f32_e32 v5, v82, v5
	s_waitcnt lgkmcnt(3)
	v_add_f32_e32 v6, v66, v6
	s_waitcnt lgkmcnt(2)
	v_add_f32_e32 v7, v50, v7
	s_waitcnt lgkmcnt(1)
	v_add_f32_e32 v8, v34, v8
	s_waitcnt lgkmcnt(0)
	v_add_f32_e32 v11, v18, v9
	v_bitop3_b32 v17, v239, s21, v240 bitop3:0x36
	ds_bpermute_b32 v9, v17, v2
	ds_bpermute_b32 v10, v17, v3
	ds_bpermute_b32 v12, v17, v4
	ds_bpermute_b32 v13, v17, v5
	ds_bpermute_b32 v14, v17, v6
	ds_bpermute_b32 v15, v17, v7
	ds_bpermute_b32 v16, v17, v8
	ds_bpermute_b32 v17, v17, v11
	s_and_saveexec_b64 s[26:27], vcc
	s_cbranch_execz .LBB0_1214
	s_lshl_b32 s11, s11, 8
	s_add_i32 s11, s11, s57
	s_waitcnt lgkmcnt(5)
	v_add_f32_e32 v12, v4, v12
	v_add_f32_e32 v4, v2, v9
	v_or_b32_e32 v2, s11, v238
	s_mov_b32 s11, 0x49800000
	v_fma_f32 v4, v4, s11, 0.5
	v_trunc_f32_e32 v4, v4
	s_waitcnt lgkmcnt(4)
	v_add_f32_e32 v13, v5, v13
	v_mul_f32_e32 v5, 0x2f800000, v4
	v_floor_f32_e32 v5, v5
	v_fmac_f32_e32 v4, 0xcf800000, v5
	v_cvt_u32_f32_e32 v4, v4
	v_cvt_u32_f32_e32 v5, v5
	v_add_f32_e32 v10, v3, v10
	v_ashrrev_i32_e32 v3, 31, v2
	v_lshl_add_u64 v[2:3], v[2:3], 3, s[44:45]
	global_atomic_add_x2 v[2:3], v[4:5], off
	v_fma_f32 v4, v10, s11, 0.5
	v_trunc_f32_e32 v4, v4
	v_mul_f32_e32 v5, 0x2f800000, v4
	v_floor_f32_e32 v5, v5
	v_fmac_f32_e32 v4, 0xcf800000, v5
	v_cvt_u32_f32_e32 v4, v4
	v_cvt_u32_f32_e32 v5, v5
	s_waitcnt lgkmcnt(3)
	v_add_f32_e32 v6, v6, v14
	s_waitcnt lgkmcnt(2)
	v_add_f32_e32 v7, v7, v15
	s_waitcnt lgkmcnt(1)
	v_add_f32_e32 v8, v8, v16
	global_atomic_add_x2 v[2:3], v[4:5], off offset:128
	v_fma_f32 v4, v12, s11, 0.5
	v_trunc_f32_e32 v4, v4
	v_mul_f32_e32 v5, 0x2f800000, v4
	v_floor_f32_e32 v5, v5
	v_fmac_f32_e32 v4, 0xcf800000, v5
	v_cvt_u32_f32_e32 v4, v4
	v_cvt_u32_f32_e32 v5, v5
	s_waitcnt lgkmcnt(0)
	v_add_f32_e32 v11, v11, v17
	global_atomic_add_x2 v[2:3], v[4:5], off offset:256
	v_fma_f32 v4, v13, s11, 0.5
	v_trunc_f32_e32 v4, v4
	v_mul_f32_e32 v5, 0x2f800000, v4
	v_floor_f32_e32 v5, v5
	v_fmac_f32_e32 v4, 0xcf800000, v5
	v_cvt_u32_f32_e32 v4, v4
	v_cvt_u32_f32_e32 v5, v5
	global_atomic_add_x2 v[2:3], v[4:5], off offset:384
	v_fma_f32 v4, v6, s11, 0.5
	v_trunc_f32_e32 v4, v4
	v_mul_f32_e32 v5, 0x2f800000, v4
	v_floor_f32_e32 v5, v5
	v_fmac_f32_e32 v4, 0xcf800000, v5
	v_cvt_u32_f32_e32 v4, v4
	v_cvt_u32_f32_e32 v5, v5
	global_atomic_add_x2 v[2:3], v[4:5], off offset:1024
	v_fma_f32 v4, v7, s11, 0.5
	v_trunc_f32_e32 v4, v4
	v_mul_f32_e32 v5, 0x2f800000, v4
	v_floor_f32_e32 v5, v5
	v_fmac_f32_e32 v4, 0xcf800000, v5
	v_cvt_u32_f32_e32 v4, v4
	v_cvt_u32_f32_e32 v5, v5
	global_atomic_add_x2 v[2:3], v[4:5], off offset:1152
	v_fma_f32 v4, v8, s11, 0.5
	v_trunc_f32_e32 v4, v4
	v_mul_f32_e32 v5, 0x2f800000, v4
	v_floor_f32_e32 v5, v5
	v_fmac_f32_e32 v4, 0xcf800000, v5
	v_cvt_u32_f32_e32 v4, v4
	v_cvt_u32_f32_e32 v5, v5
	global_atomic_add_x2 v[2:3], v[4:5], off offset:1280
	v_fma_f32 v4, v11, s11, 0.5
	v_trunc_f32_e32 v4, v4
	v_mul_f32_e32 v5, 0x2f800000, v4
	v_floor_f32_e32 v5, v5
	v_fmac_f32_e32 v4, 0xcf800000, v5
	v_cvt_u32_f32_e32 v4, v4
	v_cvt_u32_f32_e32 v5, v5
	global_atomic_add_x2 v[2:3], v[4:5], off offset:1408
	s_branch .LBB0_1214
